# P0 cooperative transposer: gain loads issued behind the first two regions' loads
# baseline (speedup 1.0000x reference)
; #define GAS __attribute__((address_space(1)))
; #define LAS __attribute__((address_space(3)))
; #define LDS_WAIT() asm volatile("s_waitcnt lgkmcnt(0)" ::: "memory")
;     const int pr = item >> 1, kb = 2 * (pr / nblk) + (item & 1), nb = pr % nblk, k0 = 64 * kb, n0 = 32 * nb;
;     const int nr = n0 + (lane & 31); const int sc = MAP == 1 ? src_col_in(nr) : nr;
;     float v[32];
; #pragma unroll
;     for (int i = 0; i < 32; ++i) v[i] = sc >= 0 ? W[(size_t)(k0 + 2 * i + (lane >> 5)) * Nsrc + sc] : 0.f;
; #pragma unroll
;     for (int i = 0; i < 32; ++i) { const int k = k0 + 2 * i + (lane >> 5); float x = v[i] * wscale; if (KS) x *= (k < ksplit ? ksA[k] : ksB[k - ksplit]); scr[(2 * i + (lane >> 5)) * 33 + (lane & 31)] = x; }
;     LDS_WAIT(); asm volatile("" ::: "memory");
;     const int c = lane & 7;
; #pragma unroll
;     for (int j = 0; j < 4; ++j) { const int n = (lane >> 3) + 8 * j; const LAS float* s = scr + (8 * c) * 33 + n;
;         const unsigned long long o = (unsigned long long)pg8::pk4_fp8(s[0 * 33], s[1 * 33], s[2 * 33], s[3 * 33]) | ((unsigned long long)pg8::pk4_fp8(s[4 * 33], s[5 * 33], s[6 * 33], s[7 * 33]) << 32);
;         *(GAS unsigned long long*)(WT + (size_t)(n0 + n) * K + k0 + 8 * c) = o; }
;     LDS_WAIT(); asm volatile("" ::: "memory");
; }
.Lco_wup_layer:
	s_mov_b64 s[4:5], s[16:17]
	s_mov_b64 s[6:7], s[18:19]
	s_mov_b32 s24, 0
	s_mov_b32 s25, 0
	s_mov_b32 s44, 0xc3e00000
	v_mov_b32_e32 v246, 0x43e00000
	s_mov_b64 s[8:9], s[4:5]
	global_load_dwordx4 v[144:147], v208, s[8:9]
	s_add_u32 s8, s8, 0x20000
	s_addc_u32 s9, s9, 0
	global_load_dwordx4 v[148:151], v208, s[8:9]
	s_add_u32 s8, s8, 0x20000
	s_addc_u32 s9, s9, 0
	global_load_dwordx4 v[152:155], v208, s[8:9]
	s_add_u32 s8, s8, 0x20000
	s_addc_u32 s9, s9, 0
	global_load_dwordx4 v[156:159], v208, s[8:9]
	s_add_u32 s8, s8, 0x20000
	s_addc_u32 s9, s9, 0
	global_load_dwordx4 v[160:163], v208, s[8:9]
	s_add_u32 s8, s8, 0x20000
	s_addc_u32 s9, s9, 0
	global_load_dwordx4 v[164:167], v208, s[8:9]
	s_add_u32 s8, s8, 0x20000
	s_addc_u32 s9, s9, 0
	global_load_dwordx4 v[168:171], v208, s[8:9]
	s_add_u32 s8, s8, 0x20000
	s_addc_u32 s9, s9, 0
	global_load_dwordx4 v[172:175], v208, s[8:9]
	s_add_u32 s4, s4, 0x1000
	s_addc_u32 s5, s5, 0
	s_mov_b64 s[8:9], s[4:5]
	global_load_dwordx4 v[176:179], v208, s[8:9]
	s_add_u32 s8, s8, 0x20000
	s_addc_u32 s9, s9, 0
	global_load_dwordx4 v[180:183], v208, s[8:9]
	s_add_u32 s8, s8, 0x20000
	s_addc_u32 s9, s9, 0
	global_load_dwordx4 v[184:187], v208, s[8:9]
	s_add_u32 s8, s8, 0x20000
	s_addc_u32 s9, s9, 0
	global_load_dwordx4 v[188:191], v208, s[8:9]
	s_add_u32 s8, s8, 0x20000
	s_addc_u32 s9, s9, 0
	global_load_dwordx4 v[192:195], v208, s[8:9]
	s_add_u32 s8, s8, 0x20000
	s_addc_u32 s9, s9, 0
	global_load_dwordx4 v[196:199], v208, s[8:9]
	s_add_u32 s8, s8, 0x20000
	s_addc_u32 s9, s9, 0
	global_load_dwordx4 v[200:203], v208, s[8:9]
	s_add_u32 s8, s8, 0x20000
	s_addc_u32 s9, s9, 0
	global_load_dwordx4 v[204:207], v208, s[8:9]
	s_add_u32 s4, s4, 0x1000
	s_addc_u32 s5, s5, 0
	global_load_dword v218, v217, s[10:11] offset:0
	global_load_dword v219, v217, s[10:11] offset:8
	global_load_dword v220, v217, s[10:11] offset:16
	global_load_dword v221, v217, s[10:11] offset:24
	global_load_dword v222, v217, s[10:11] offset:32
	global_load_dword v223, v217, s[10:11] offset:40
	global_load_dword v224, v217, s[10:11] offset:48
	global_load_dword v225, v217, s[10:11] offset:56
	s_waitcnt vmcnt(0)
	v_mul_f32_e32 v218, 0x42800000, v218
	v_mul_f32_e32 v219, 0x42800000, v219
	v_mul_f32_e32 v220, 0x42800000, v220
	v_mul_f32_e32 v221, 0x42800000, v221
	v_mul_f32_e32 v222, 0x42800000, v222
	v_mul_f32_e32 v223, 0x42800000, v223
	v_mul_f32_e32 v224, 0x42800000, v224
	v_mul_f32_e32 v225, 0x42800000, v225
	s_waitcnt vmcnt(8)
	v_mul_f32_e32 v144, v218, v144
	v_mul_f32_e32 v145, v218, v145
	v_mul_f32_e32 v146, v218, v146
	v_mul_f32_e32 v147, v218, v147
	ds_write_b128 v209, v[144:147]
	v_mul_f32_e32 v148, v219, v148
	v_mul_f32_e32 v149, v219, v149
	v_mul_f32_e32 v150, v219, v150
	v_mul_f32_e32 v151, v219, v151
	ds_write_b128 v209, v[148:151] offset:1024
	v_mul_f32_e32 v152, v220, v152
	v_mul_f32_e32 v153, v220, v153
	v_mul_f32_e32 v154, v220, v154
	v_mul_f32_e32 v155, v220, v155
	ds_write_b128 v209, v[152:155] offset:2048
	v_mul_f32_e32 v156, v221, v156
	v_mul_f32_e32 v157, v221, v157
	v_mul_f32_e32 v158, v221, v158
	v_mul_f32_e32 v159, v221, v159
	ds_write_b128 v209, v[156:159] offset:3072
	v_mul_f32_e32 v160, v222, v160
	v_mul_f32_e32 v161, v222, v161
	v_mul_f32_e32 v162, v222, v162
	v_mul_f32_e32 v163, v222, v163
	ds_write_b128 v209, v[160:163] offset:4096
	v_mul_f32_e32 v164, v223, v164
	v_mul_f32_e32 v165, v223, v165
	v_mul_f32_e32 v166, v223, v166
	v_mul_f32_e32 v167, v223, v167
	ds_write_b128 v209, v[164:167] offset:5120
	v_mul_f32_e32 v168, v224, v168
	v_mul_f32_e32 v169, v224, v169
	v_mul_f32_e32 v170, v224, v170
	v_mul_f32_e32 v171, v224, v171
	ds_write_b128 v209, v[168:171] offset:6144
	v_mul_f32_e32 v172, v225, v172
	v_mul_f32_e32 v173, v225, v173
	v_mul_f32_e32 v174, v225, v174
	v_mul_f32_e32 v175, v225, v175
	ds_write_b128 v209, v[172:175] offset:7168
	s_waitcnt lgkmcnt(0)
	s_barrier
	s_mov_b64 s[8:9], s[4:5]
	global_load_dwordx4 v[144:147], v208, s[8:9]
	s_add_u32 s8, s8, 0x20000
	s_addc_u32 s9, s9, 0
	global_load_dwordx4 v[148:151], v208, s[8:9]
	s_add_u32 s8, s8, 0x20000
	s_addc_u32 s9, s9, 0
	global_load_dwordx4 v[152:155], v208, s[8:9]
	s_add_u32 s8, s8, 0x20000
	s_addc_u32 s9, s9, 0
	global_load_dwordx4 v[156:159], v208, s[8:9]
	s_add_u32 s8, s8, 0x20000
	s_addc_u32 s9, s9, 0
	global_load_dwordx4 v[160:163], v208, s[8:9]
	s_add_u32 s8, s8, 0x20000
	s_addc_u32 s9, s9, 0
	global_load_dwordx4 v[164:167], v208, s[8:9]
	s_add_u32 s8, s8, 0x20000
	s_addc_u32 s9, s9, 0
	global_load_dwordx4 v[168:171], v208, s[8:9]
	s_add_u32 s8, s8, 0x20000
	s_addc_u32 s9, s9, 0
	global_load_dwordx4 v[172:175], v208, s[8:9]
	s_add_u32 s4, s4, 0x1000
	s_addc_u32 s5, s5, 0
	ds_read_b32 v226, v211
	ds_read_b32 v227, v211 offset:512
	ds_read_b32 v228, v211 offset:1024
	ds_read_b32 v229, v211 offset:1536
	ds_read_b32 v230, v211 offset:2048
	ds_read_b32 v231, v211 offset:2560
	ds_read_b32 v232, v211 offset:3072
	ds_read_b32 v233, v211 offset:3584
	ds_read_b32 v234, v211 offset:4096
	ds_read_b32 v235, v211 offset:4608
	ds_read_b32 v236, v211 offset:5120
	ds_read_b32 v237, v211 offset:5632
	ds_read_b32 v238, v211 offset:6144
	ds_read_b32 v239, v211 offset:6656
	ds_read_b32 v240, v211 offset:7168
	ds_read_b32 v241, v211 offset:7680
	s_waitcnt lgkmcnt(0)
; #define GAS __attribute__((address_space(1)))
; #define LAS __attribute__((address_space(3)))
; #define LDS_WAIT() asm volatile("s_waitcnt lgkmcnt(0)" ::: "memory")
;     const int pr = item >> 1, kb = 2 * (pr / nblk) + (item & 1), nb = pr % nblk, k0 = 64 * kb, n0 = 32 * nb;
;     const int nr = n0 + (lane & 31); const int sc = MAP == 1 ? src_col_in(nr) : nr;
;     float v[32];
; #pragma unroll
;     for (int i = 0; i < 32; ++i) v[i] = sc >= 0 ? W[(size_t)(k0 + 2 * i + (lane >> 5)) * Nsrc + sc] : 0.f;
; #pragma unroll
;     for (int i = 0; i < 32; ++i) { const int k = k0 + 2 * i + (lane >> 5); float x = v[i] * wscale; if (KS) x *= (k < ksplit ? ksA[k] : ksB[k - ksplit]); scr[(2 * i + (lane >> 5)) * 33 + (lane & 31)] = x; }
;     LDS_WAIT(); asm volatile("" ::: "memory");
;     const int c = lane & 7;
; #pragma unroll
;     for (int j = 0; j < 4; ++j) { const int n = (lane >> 3) + 8 * j; const LAS float* s = scr + (8 * c) * 33 + n;
;         const unsigned long long o = (unsigned long long)pg8::pk4_fp8(s[0 * 33], s[1 * 33], s[2 * 33], s[3 * 33]) | ((unsigned long long)pg8::pk4_fp8(s[4 * 33], s[5 * 33], s[6 * 33], s[7 * 33]) << 32);
;         *(GAS unsigned long long*)(WT + (size_t)(n0 + n) * K + k0 + 8 * c) = o; }
;     LDS_WAIT(); asm volatile("" ::: "memory");
; }
	v_max_f32_e32 v226, v226, v226
	v_max_f32_e32 v227, v227, v227
	v_max_f32_e32 v228, v228, v228
	v_max_f32_e32 v229, v229, v229
	v_max_f32_e32 v230, v230, v230
	v_max_f32_e32 v231, v231, v231
	v_max_f32_e32 v232, v232, v232
	v_max_f32_e32 v233, v233, v233
	v_max_f32_e32 v234, v234, v234
	v_max_f32_e32 v235, v235, v235
	v_max_f32_e32 v236, v236, v236
	v_max_f32_e32 v237, v237, v237
	v_max_f32_e32 v238, v238, v238
	v_max_f32_e32 v239, v239, v239
	v_max_f32_e32 v240, v240, v240
	v_max_f32_e32 v241, v241, v241
	v_med3_f32 v226, v226, s44, v246
	v_med3_f32 v227, v227, s44, v246
	v_med3_f32 v228, v228, s44, v246
	v_med3_f32 v229, v229, s44, v246
	v_med3_f32 v230, v230, s44, v246
	v_med3_f32 v231, v231, s44, v246
	v_med3_f32 v232, v232, s44, v246
	v_med3_f32 v233, v233, s44, v246
	v_med3_f32 v234, v234, s44, v246
	v_med3_f32 v235, v235, s44, v246
	v_med3_f32 v236, v236, s44, v246
	v_med3_f32 v237, v237, s44, v246
	v_med3_f32 v238, v238, s44, v246
	v_med3_f32 v239, v239, s44, v246
	v_med3_f32 v240, v240, s44, v246
	v_med3_f32 v241, v241, s44, v246
	v_mov_b32_e32 v242, 0
	v_mov_b32_e32 v243, 0
	v_mov_b32_e32 v244, 0
	v_mov_b32_e32 v245, 0
	v_cvt_pk_fp8_f32 v242, v226, v227
	v_cvt_pk_fp8_f32 v243, v230, v231
	v_cvt_pk_fp8_f32 v244, v234, v235
	v_cvt_pk_fp8_f32 v245, v238, v239
	v_cvt_pk_fp8_f32 v242, v228, v229 op_sel:[0,0,1]
	v_cvt_pk_fp8_f32 v243, v232, v233 op_sel:[0,0,1]
	v_cvt_pk_fp8_f32 v244, v236, v237 op_sel:[0,0,1]
	v_cvt_pk_fp8_f32 v245, v240, v241 op_sel:[0,0,1]
	s_nop 0
	global_store_dwordx4 v215, v[242:245], s[6:7]
	ds_read_b32 v226, v213
	ds_read_b32 v227, v213 offset:512
	ds_read_b32 v228, v213 offset:1024
	ds_read_b32 v229, v213 offset:1536
	ds_read_b32 v230, v213 offset:2048
	ds_read_b32 v231, v213 offset:2560
	ds_read_b32 v232, v213 offset:3072
	ds_read_b32 v233, v213 offset:3584
	ds_read_b32 v234, v213 offset:4096
	ds_read_b32 v235, v213 offset:4608
	ds_read_b32 v236, v213 offset:5120
	ds_read_b32 v237, v213 offset:5632
	ds_read_b32 v238, v213 offset:6144
	ds_read_b32 v239, v213 offset:6656
	ds_read_b32 v240, v213 offset:7168
	ds_read_b32 v241, v213 offset:7680
	s_waitcnt lgkmcnt(0)
	v_max_f32_e32 v226, v226, v226
	v_max_f32_e32 v227, v227, v227
	v_max_f32_e32 v228, v228, v228
	v_max_f32_e32 v229, v229, v229
	v_max_f32_e32 v230, v230, v230
	v_max_f32_e32 v231, v231, v231
	v_max_f32_e32 v232, v232, v232
	v_max_f32_e32 v233, v233, v233
	v_max_f32_e32 v234, v234, v234
	v_max_f32_e32 v235, v235, v235
	v_max_f32_e32 v236, v236, v236
	v_max_f32_e32 v237, v237, v237
	v_max_f32_e32 v238, v238, v238
	v_max_f32_e32 v239, v239, v239
	v_max_f32_e32 v240, v240, v240
	v_max_f32_e32 v241, v241, v241
	v_med3_f32 v226, v226, s44, v246
	v_med3_f32 v227, v227, s44, v246
	v_med3_f32 v228, v228, s44, v246
	v_med3_f32 v229, v229, s44, v246
	v_med3_f32 v230, v230, s44, v246
	v_med3_f32 v231, v231, s44, v246
	v_med3_f32 v232, v232, s44, v246
	v_med3_f32 v233, v233, s44, v246
	v_med3_f32 v234, v234, s44, v246
	v_med3_f32 v235, v235, s44, v246
	v_med3_f32 v236, v236, s44, v246
	v_med3_f32 v237, v237, s44, v246
	v_med3_f32 v238, v238, s44, v246
	v_med3_f32 v239, v239, s44, v246
	v_med3_f32 v240, v240, s44, v246
	v_med3_f32 v241, v241, s44, v246
	v_mov_b32_e32 v242, 0
	v_mov_b32_e32 v243, 0
	v_mov_b32_e32 v244, 0
	v_mov_b32_e32 v245, 0
	v_cvt_pk_fp8_f32 v242, v226, v227
	v_cvt_pk_fp8_f32 v243, v230, v231
	v_cvt_pk_fp8_f32 v244, v234, v235
	v_cvt_pk_fp8_f32 v245, v238, v239
	v_cvt_pk_fp8_f32 v242, v228, v229 op_sel:[0,0,1]
	v_cvt_pk_fp8_f32 v243, v232, v233 op_sel:[0,0,1]
	v_cvt_pk_fp8_f32 v244, v236, v237 op_sel:[0,0,1]
	v_cvt_pk_fp8_f32 v245, v240, v241 op_sel:[0,0,1]
	s_nop 0
	global_store_dwordx4 v216, v[242:245], s[6:7]
	s_add_u32 s6, s6, 0x400000
	s_addc_u32 s7, s7, 0
	s_waitcnt vmcnt(10)
	v_mul_f32_e32 v176, v218, v176
	v_mul_f32_e32 v177, v218, v177
	v_mul_f32_e32 v178, v218, v178
	v_mul_f32_e32 v179, v218, v179
	ds_write_b128 v210, v[176:179]
	v_mul_f32_e32 v180, v219, v180
	v_mul_f32_e32 v181, v219, v181
	v_mul_f32_e32 v182, v219, v182
	v_mul_f32_e32 v183, v219, v183
	ds_write_b128 v210, v[180:183] offset:1024
	v_mul_f32_e32 v184, v220, v184
	v_mul_f32_e32 v185, v220, v185
	v_mul_f32_e32 v186, v220, v186
	v_mul_f32_e32 v187, v220, v187
	ds_write_b128 v210, v[184:187] offset:2048
	v_mul_f32_e32 v188, v221, v188
	v_mul_f32_e32 v189, v221, v189
	v_mul_f32_e32 v190, v221, v190
	v_mul_f32_e32 v191, v221, v191
	ds_write_b128 v210, v[188:191] offset:3072
	v_mul_f32_e32 v192, v222, v192
	v_mul_f32_e32 v193, v222, v193
	v_mul_f32_e32 v194, v222, v194
	v_mul_f32_e32 v195, v222, v195
	ds_write_b128 v210, v[192:195] offset:4096
	v_mul_f32_e32 v196, v223, v196
	v_mul_f32_e32 v197, v223, v197
	v_mul_f32_e32 v198, v223, v198
	v_mul_f32_e32 v199, v223, v199
	ds_write_b128 v210, v[196:199] offset:5120
	v_mul_f32_e32 v200, v224, v200
	v_mul_f32_e32 v201, v224, v201
	v_mul_f32_e32 v202, v224, v202
	v_mul_f32_e32 v203, v224, v203
	ds_write_b128 v210, v[200:203] offset:6144
	v_mul_f32_e32 v204, v225, v204
	v_mul_f32_e32 v205, v225, v205
	v_mul_f32_e32 v206, v225, v206
	v_mul_f32_e32 v207, v225, v207
	ds_write_b128 v210, v[204:207] offset:7168
	s_waitcnt lgkmcnt(0)
	s_barrier
; #define GAS __attribute__((address_space(1)))
; #define LAS __attribute__((address_space(3)))
; #define LDS_WAIT() asm volatile("s_waitcnt lgkmcnt(0)" ::: "memory")
;     const int pr = item >> 1, kb = 2 * (pr / nblk) + (item & 1), nb = pr % nblk, k0 = 64 * kb, n0 = 32 * nb;
;     const int nr = n0 + (lane & 31); const int sc = MAP == 1 ? src_col_in(nr) : nr;
;     float v[32];
; #pragma unroll
;     for (int i = 0; i < 32; ++i) v[i] = sc >= 0 ? W[(size_t)(k0 + 2 * i + (lane >> 5)) * Nsrc + sc] : 0.f;
; #pragma unroll
;     for (int i = 0; i < 32; ++i) { const int k = k0 + 2 * i + (lane >> 5); float x = v[i] * wscale; if (KS) x *= (k < ksplit ? ksA[k] : ksB[k - ksplit]); scr[(2 * i + (lane >> 5)) * 33 + (lane & 31)] = x; }
;     LDS_WAIT(); asm volatile("" ::: "memory");
;     const int c = lane & 7;
; #pragma unroll
;     for (int j = 0; j < 4; ++j) { const int n = (lane >> 3) + 8 * j; const LAS float* s = scr + (8 * c) * 33 + n;
;         const unsigned long long o = (unsigned long long)pg8::pk4_fp8(s[0 * 33], s[1 * 33], s[2 * 33], s[3 * 33]) | ((unsigned long long)pg8::pk4_fp8(s[4 * 33], s[5 * 33], s[6 * 33], s[7 * 33]) << 32);
;         *(GAS unsigned long long*)(WT + (size_t)(n0 + n) * K + k0 + 8 * c) = o; }
;     LDS_WAIT(); asm volatile("" ::: "memory");
; }
	s_mov_b64 s[8:9], s[4:5]
	global_load_dwordx4 v[176:179], v208, s[8:9]
	s_add_u32 s8, s8, 0x20000
	s_addc_u32 s9, s9, 0
	global_load_dwordx4 v[180:183], v208, s[8:9]
	s_add_u32 s8, s8, 0x20000
	s_addc_u32 s9, s9, 0
	global_load_dwordx4 v[184:187], v208, s[8:9]
	s_add_u32 s8, s8, 0x20000
	s_addc_u32 s9, s9, 0
	global_load_dwordx4 v[188:191], v208, s[8:9]
	s_add_u32 s8, s8, 0x20000
	s_addc_u32 s9, s9, 0
	global_load_dwordx4 v[192:195], v208, s[8:9]
	s_add_u32 s8, s8, 0x20000
	s_addc_u32 s9, s9, 0
	global_load_dwordx4 v[196:199], v208, s[8:9]
	s_add_u32 s8, s8, 0x20000
	s_addc_u32 s9, s9, 0
	global_load_dwordx4 v[200:203], v208, s[8:9]
	s_add_u32 s8, s8, 0x20000
	s_addc_u32 s9, s9, 0
	global_load_dwordx4 v[204:207], v208, s[8:9]
	s_add_u32 s4, s4, 0x1000
	s_addc_u32 s5, s5, 0
	ds_read_b32 v226, v212
	ds_read_b32 v227, v212 offset:512
	ds_read_b32 v228, v212 offset:1024
	ds_read_b32 v229, v212 offset:1536
	ds_read_b32 v230, v212 offset:2048
	ds_read_b32 v231, v212 offset:2560
	ds_read_b32 v232, v212 offset:3072
	ds_read_b32 v233, v212 offset:3584
	ds_read_b32 v234, v212 offset:4096
	ds_read_b32 v235, v212 offset:4608
	ds_read_b32 v236, v212 offset:5120
	ds_read_b32 v237, v212 offset:5632
	ds_read_b32 v238, v212 offset:6144
	ds_read_b32 v239, v212 offset:6656
	ds_read_b32 v240, v212 offset:7168
	ds_read_b32 v241, v212 offset:7680
	s_waitcnt lgkmcnt(0)
	v_max_f32_e32 v226, v226, v226
	v_max_f32_e32 v227, v227, v227
	v_max_f32_e32 v228, v228, v228
	v_max_f32_e32 v229, v229, v229
	v_max_f32_e32 v230, v230, v230
	v_max_f32_e32 v231, v231, v231
	v_max_f32_e32 v232, v232, v232
	v_max_f32_e32 v233, v233, v233
	v_max_f32_e32 v234, v234, v234
	v_max_f32_e32 v235, v235, v235
	v_max_f32_e32 v236, v236, v236
	v_max_f32_e32 v237, v237, v237
	v_max_f32_e32 v238, v238, v238
	v_max_f32_e32 v239, v239, v239
	v_max_f32_e32 v240, v240, v240
	v_max_f32_e32 v241, v241, v241
	v_med3_f32 v226, v226, s44, v246
	v_med3_f32 v227, v227, s44, v246
	v_med3_f32 v228, v228, s44, v246
	v_med3_f32 v229, v229, s44, v246
	v_med3_f32 v230, v230, s44, v246
	v_med3_f32 v231, v231, s44, v246
	v_med3_f32 v232, v232, s44, v246
	v_med3_f32 v233, v233, s44, v246
	v_med3_f32 v234, v234, s44, v246
	v_med3_f32 v235, v235, s44, v246
	v_med3_f32 v236, v236, s44, v246
	v_med3_f32 v237, v237, s44, v246
	v_med3_f32 v238, v238, s44, v246
	v_med3_f32 v239, v239, s44, v246
	v_med3_f32 v240, v240, s44, v246
	v_med3_f32 v241, v241, s44, v246
	v_mov_b32_e32 v242, 0
	v_mov_b32_e32 v243, 0
	v_mov_b32_e32 v244, 0
	v_mov_b32_e32 v245, 0
	v_cvt_pk_fp8_f32 v242, v226, v227
	v_cvt_pk_fp8_f32 v243, v230, v231
	v_cvt_pk_fp8_f32 v244, v234, v235
	v_cvt_pk_fp8_f32 v245, v238, v239
	v_cvt_pk_fp8_f32 v242, v228, v229 op_sel:[0,0,1]
	v_cvt_pk_fp8_f32 v243, v232, v233 op_sel:[0,0,1]
	v_cvt_pk_fp8_f32 v244, v236, v237 op_sel:[0,0,1]
	v_cvt_pk_fp8_f32 v245, v240, v241 op_sel:[0,0,1]
	s_nop 0
	global_store_dwordx4 v215, v[242:245], s[6:7]
	ds_read_b32 v226, v214
	ds_read_b32 v227, v214 offset:512
	ds_read_b32 v228, v214 offset:1024
	ds_read_b32 v229, v214 offset:1536
	ds_read_b32 v230, v214 offset:2048
	ds_read_b32 v231, v214 offset:2560
	ds_read_b32 v232, v214 offset:3072
	ds_read_b32 v233, v214 offset:3584
	ds_read_b32 v234, v214 offset:4096
	ds_read_b32 v235, v214 offset:4608
	ds_read_b32 v236, v214 offset:5120
	ds_read_b32 v237, v214 offset:5632
	ds_read_b32 v238, v214 offset:6144
	ds_read_b32 v239, v214 offset:6656
	ds_read_b32 v240, v214 offset:7168
	ds_read_b32 v241, v214 offset:7680
	s_waitcnt lgkmcnt(0)
	v_max_f32_e32 v226, v226, v226
	v_max_f32_e32 v227, v227, v227
	v_max_f32_e32 v228, v228, v228
	v_max_f32_e32 v229, v229, v229
	v_max_f32_e32 v230, v230, v230
	v_max_f32_e32 v231, v231, v231
	v_max_f32_e32 v232, v232, v232
	v_max_f32_e32 v233, v233, v233
	v_max_f32_e32 v234, v234, v234
	v_max_f32_e32 v235, v235, v235
	v_max_f32_e32 v236, v236, v236
	v_max_f32_e32 v237, v237, v237
	v_max_f32_e32 v238, v238, v238
	v_max_f32_e32 v239, v239, v239
	v_max_f32_e32 v240, v240, v240
	v_max_f32_e32 v241, v241, v241
	v_med3_f32 v226, v226, s44, v246
	v_med3_f32 v227, v227, s44, v246
	v_med3_f32 v228, v228, s44, v246
	v_med3_f32 v229, v229, s44, v246
	v_med3_f32 v230, v230, s44, v246
	v_med3_f32 v231, v231, s44, v246
	v_med3_f32 v232, v232, s44, v246
	v_med3_f32 v233, v233, s44, v246
	v_med3_f32 v234, v234, s44, v246
	v_med3_f32 v235, v235, s44, v246
	v_med3_f32 v236, v236, s44, v246
	v_med3_f32 v237, v237, s44, v246
	v_med3_f32 v238, v238, s44, v246
	v_med3_f32 v239, v239, s44, v246
	v_med3_f32 v240, v240, s44, v246
	v_med3_f32 v241, v241, s44, v246
	v_mov_b32_e32 v242, 0
	v_mov_b32_e32 v243, 0
	v_mov_b32_e32 v244, 0
	v_mov_b32_e32 v245, 0
	v_cvt_pk_fp8_f32 v242, v226, v227
	v_cvt_pk_fp8_f32 v243, v230, v231
	v_cvt_pk_fp8_f32 v244, v234, v235
	v_cvt_pk_fp8_f32 v245, v238, v239
	v_cvt_pk_fp8_f32 v242, v228, v229 op_sel:[0,0,1]
	v_cvt_pk_fp8_f32 v243, v232, v233 op_sel:[0,0,1]
	v_cvt_pk_fp8_f32 v244, v236, v237 op_sel:[0,0,1]
	v_cvt_pk_fp8_f32 v245, v240, v241 op_sel:[0,0,1]
	s_nop 0
	global_store_dwordx4 v216, v[242:245], s[6:7]
	s_add_u32 s6, s6, 0x400000
	s_addc_u32 s7, s7, 0
	s_mov_b32 s12, 6

; #define GAS __attribute__((address_space(1)))
; #define LAS __attribute__((address_space(3)))
; #define LDS_WAIT() asm volatile("s_waitcnt lgkmcnt(0)" ::: "memory")
;     const int pr = item >> 1, kb = 2 * (pr / nblk) + (item & 1), nb = pr % nblk, k0 = 64 * kb, n0 = 32 * nb;
;     const int nr = n0 + (lane & 31); const int sc = MAP == 1 ? src_col_in(nr) : nr;
;     float v[32];
; #pragma unroll
;     for (int i = 0; i < 32; ++i) v[i] = sc >= 0 ? W[(size_t)(k0 + 2 * i + (lane >> 5)) * Nsrc + sc] : 0.f;
; #pragma unroll
;     for (int i = 0; i < 32; ++i) { const int k = k0 + 2 * i + (lane >> 5); float x = v[i] * wscale; if (KS) x *= (k < ksplit ? ksA[k] : ksB[k - ksplit]); scr[(2 * i + (lane >> 5)) * 33 + (lane & 31)] = x; }
;     LDS_WAIT(); asm volatile("" ::: "memory");
;     const int c = lane & 7;
; #pragma unroll
;     for (int j = 0; j < 4; ++j) { const int n = (lane >> 3) + 8 * j; const LAS float* s = scr + (8 * c) * 33 + n;
;         const unsigned long long o = (unsigned long long)pg8::pk4_fp8(s[0 * 33], s[1 * 33], s[2 * 33], s[3 * 33]) | ((unsigned long long)pg8::pk4_fp8(s[4 * 33], s[5 * 33], s[6 * 33], s[7 * 33]) << 32);
;         *(GAS unsigned long long*)(WT + (size_t)(n0 + n) * K + k0 + 8 * c) = o; }
;     LDS_WAIT(); asm volatile("" ::: "memory");
; }
.Lco_wdn_loop:
	s_waitcnt vmcnt(12)
	v_mul_f32_e32 v144, 0x43000000, v144
	v_mul_f32_e32 v145, 0x43000000, v145
	v_mul_f32_e32 v146, 0x43000000, v146
	v_mul_f32_e32 v147, 0x43000000, v147
	ds_write_b128 v209, v[144:147]
	v_mul_f32_e32 v148, 0x43000000, v148
	v_mul_f32_e32 v149, 0x43000000, v149
	v_mul_f32_e32 v150, 0x43000000, v150
	v_mul_f32_e32 v151, 0x43000000, v151
	ds_write_b128 v209, v[148:151] offset:1024
	v_mul_f32_e32 v152, 0x43000000, v152
	v_mul_f32_e32 v153, 0x43000000, v153
	v_mul_f32_e32 v154, 0x43000000, v154
	v_mul_f32_e32 v155, 0x43000000, v155
	ds_write_b128 v209, v[152:155] offset:2048
	v_mul_f32_e32 v156, 0x43000000, v156
	v_mul_f32_e32 v157, 0x43000000, v157
	v_mul_f32_e32 v158, 0x43000000, v158
	v_mul_f32_e32 v159, 0x43000000, v159
	ds_write_b128 v209, v[156:159] offset:3072
	v_mul_f32_e32 v160, 0x43000000, v160
	v_mul_f32_e32 v161, 0x43000000, v161
	v_mul_f32_e32 v162, 0x43000000, v162
	v_mul_f32_e32 v163, 0x43000000, v163
	ds_write_b128 v209, v[160:163] offset:4096
	v_mul_f32_e32 v164, 0x43000000, v164
	v_mul_f32_e32 v165, 0x43000000, v165
	v_mul_f32_e32 v166, 0x43000000, v166
	v_mul_f32_e32 v167, 0x43000000, v167
	ds_write_b128 v209, v[164:167] offset:5120
	v_mul_f32_e32 v168, 0x43000000, v168
	v_mul_f32_e32 v169, 0x43000000, v169
	v_mul_f32_e32 v170, 0x43000000, v170
	v_mul_f32_e32 v171, 0x43000000, v171
	ds_write_b128 v209, v[168:171] offset:6144
	v_mul_f32_e32 v172, 0x43000000, v172
	v_mul_f32_e32 v173, 0x43000000, v173
	v_mul_f32_e32 v174, 0x43000000, v174
	v_mul_f32_e32 v175, 0x43000000, v175
	ds_write_b128 v209, v[172:175] offset:7168
	s_waitcnt lgkmcnt(0)
	s_barrier
	s_mov_b64 s[8:9], s[4:5]
	global_load_dwordx4 v[144:147], v208, s[8:9]
	s_add_u32 s8, s8, 0x8000
	s_addc_u32 s9, s9, 0
	global_load_dwordx4 v[148:151], v208, s[8:9]
	s_add_u32 s8, s8, 0x8000
	s_addc_u32 s9, s9, 0
	global_load_dwordx4 v[152:155], v208, s[8:9]
	s_add_u32 s8, s8, 0x8000
	s_addc_u32 s9, s9, 0
	global_load_dwordx4 v[156:159], v208, s[8:9]
	s_add_u32 s8, s8, 0x8000
	s_addc_u32 s9, s9, 0
	global_load_dwordx4 v[160:163], v208, s[8:9]
	s_add_u32 s8, s8, 0x8000
	s_addc_u32 s9, s9, 0
	global_load_dwordx4 v[164:167], v208, s[8:9]
	s_add_u32 s8, s8, 0x8000
	s_addc_u32 s9, s9, 0
	global_load_dwordx4 v[168:171], v208, s[8:9]
	s_add_u32 s8, s8, 0x8000
	s_addc_u32 s9, s9, 0
	global_load_dwordx4 v[172:175], v208, s[8:9]
	s_add_i32 s24, s24, 1
	s_and_b32 s26, s24, 3
	s_cmp_eq_u32 s26, 0
	s_mov_b32 s26, 0x3ffd000
	s_cselect_b32 s26, s26, 0x1000
	s_add_u32 s4, s4, s26
	s_addc_u32 s5, s5, 0
	ds_read_b32 v226, v211
	ds_read_b32 v227, v211 offset:512
	ds_read_b32 v228, v211 offset:1024
	ds_read_b32 v229, v211 offset:1536
	ds_read_b32 v230, v211 offset:2048
	ds_read_b32 v231, v211 offset:2560
	ds_read_b32 v232, v211 offset:3072
	ds_read_b32 v233, v211 offset:3584
	ds_read_b32 v234, v211 offset:4096
	ds_read_b32 v235, v211 offset:4608
	ds_read_b32 v236, v211 offset:5120
	ds_read_b32 v237, v211 offset:5632
	ds_read_b32 v238, v211 offset:6144
	ds_read_b32 v239, v211 offset:6656
	ds_read_b32 v240, v211 offset:7168
	ds_read_b32 v241, v211 offset:7680
	s_waitcnt lgkmcnt(0)
	v_max_f32_e32 v226, v226, v226
	v_max_f32_e32 v227, v227, v227
	v_max_f32_e32 v228, v228, v228
	v_max_f32_e32 v229, v229, v229
	v_max_f32_e32 v230, v230, v230
	v_max_f32_e32 v231, v231, v231
	v_max_f32_e32 v232, v232, v232
	v_max_f32_e32 v233, v233, v233
	v_max_f32_e32 v234, v234, v234
	v_max_f32_e32 v235, v235, v235
	v_max_f32_e32 v236, v236, v236
	v_max_f32_e32 v237, v237, v237
	v_max_f32_e32 v238, v238, v238
	v_max_f32_e32 v239, v239, v239
	v_max_f32_e32 v240, v240, v240
	v_max_f32_e32 v241, v241, v241
	v_med3_f32 v226, v226, s44, v246
	v_med3_f32 v227, v227, s44, v246
	v_med3_f32 v228, v228, s44, v246
	v_med3_f32 v229, v229, s44, v246
	v_med3_f32 v230, v230, s44, v246
	v_med3_f32 v231, v231, s44, v246
	v_med3_f32 v232, v232, s44, v246
	v_med3_f32 v233, v233, s44, v246
	v_med3_f32 v234, v234, s44, v246
	v_med3_f32 v235, v235, s44, v246
	v_med3_f32 v236, v236, s44, v246
	v_med3_f32 v237, v237, s44, v246
	v_med3_f32 v238, v238, s44, v246
	v_med3_f32 v239, v239, s44, v246
	v_med3_f32 v240, v240, s44, v246
	v_med3_f32 v241, v241, s44, v246
	v_mov_b32_e32 v242, 0
	v_mov_b32_e32 v243, 0
	v_mov_b32_e32 v244, 0
	v_mov_b32_e32 v245, 0
	v_cvt_pk_fp8_f32 v242, v226, v227
	v_cvt_pk_fp8_f32 v243, v230, v231
	v_cvt_pk_fp8_f32 v244, v234, v235
	v_cvt_pk_fp8_f32 v245, v238, v239
	v_cvt_pk_fp8_f32 v242, v228, v229 op_sel:[0,0,1]
	v_cvt_pk_fp8_f32 v243, v232, v233 op_sel:[0,0,1]
	v_cvt_pk_fp8_f32 v244, v236, v237 op_sel:[0,0,1]
	v_cvt_pk_fp8_f32 v245, v240, v241 op_sel:[0,0,1]
	s_nop 0
	global_store_dwordx4 v215, v[242:245], s[6:7]
	ds_read_b32 v226, v213
	ds_read_b32 v227, v213 offset:512
	ds_read_b32 v228, v213 offset:1024
	ds_read_b32 v229, v213 offset:1536
	ds_read_b32 v230, v213 offset:2048
	ds_read_b32 v231, v213 offset:2560
	ds_read_b32 v232, v213 offset:3072
	ds_read_b32 v233, v213 offset:3584
	ds_read_b32 v234, v213 offset:4096
	ds_read_b32 v235, v213 offset:4608
	ds_read_b32 v236, v213 offset:5120
	ds_read_b32 v237, v213 offset:5632
	ds_read_b32 v238, v213 offset:6144
	ds_read_b32 v239, v213 offset:6656
	ds_read_b32 v240, v213 offset:7168
	ds_read_b32 v241, v213 offset:7680
	s_waitcnt lgkmcnt(0)
; #define GAS __attribute__((address_space(1)))
; #define LAS __attribute__((address_space(3)))
; #define LDS_WAIT() asm volatile("s_waitcnt lgkmcnt(0)" ::: "memory")
;     const int pr = item >> 1, kb = 2 * (pr / nblk) + (item & 1), nb = pr % nblk, k0 = 64 * kb, n0 = 32 * nb;
;     const int nr = n0 + (lane & 31); const int sc = MAP == 1 ? src_col_in(nr) : nr;
;     float v[32];
; #pragma unroll
;     for (int i = 0; i < 32; ++i) v[i] = sc >= 0 ? W[(size_t)(k0 + 2 * i + (lane >> 5)) * Nsrc + sc] : 0.f;
; #pragma unroll
;     for (int i = 0; i < 32; ++i) { const int k = k0 + 2 * i + (lane >> 5); float x = v[i] * wscale; if (KS) x *= (k < ksplit ? ksA[k] : ksB[k - ksplit]); scr[(2 * i + (lane >> 5)) * 33 + (lane & 31)] = x; }
;     LDS_WAIT(); asm volatile("" ::: "memory");
;     const int c = lane & 7;
; #pragma unroll
;     for (int j = 0; j < 4; ++j) { const int n = (lane >> 3) + 8 * j; const LAS float* s = scr + (8 * c) * 33 + n;
;         const unsigned long long o = (unsigned long long)pg8::pk4_fp8(s[0 * 33], s[1 * 33], s[2 * 33], s[3 * 33]) | ((unsigned long long)pg8::pk4_fp8(s[4 * 33], s[5 * 33], s[6 * 33], s[7 * 33]) << 32);
;         *(GAS unsigned long long*)(WT + (size_t)(n0 + n) * K + k0 + 8 * c) = o; }
;     LDS_WAIT(); asm volatile("" ::: "memory");
; }
	v_max_f32_e32 v226, v226, v226
	v_max_f32_e32 v227, v227, v227
	v_max_f32_e32 v228, v228, v228
	v_max_f32_e32 v229, v229, v229
	v_max_f32_e32 v230, v230, v230
	v_max_f32_e32 v231, v231, v231
	v_max_f32_e32 v232, v232, v232
	v_max_f32_e32 v233, v233, v233
	v_max_f32_e32 v234, v234, v234
	v_max_f32_e32 v235, v235, v235
	v_max_f32_e32 v236, v236, v236
	v_max_f32_e32 v237, v237, v237
	v_max_f32_e32 v238, v238, v238
	v_max_f32_e32 v239, v239, v239
	v_max_f32_e32 v240, v240, v240
	v_max_f32_e32 v241, v241, v241
	v_med3_f32 v226, v226, s44, v246
	v_med3_f32 v227, v227, s44, v246
	v_med3_f32 v228, v228, s44, v246
	v_med3_f32 v229, v229, s44, v246
	v_med3_f32 v230, v230, s44, v246
	v_med3_f32 v231, v231, s44, v246
	v_med3_f32 v232, v232, s44, v246
	v_med3_f32 v233, v233, s44, v246
	v_med3_f32 v234, v234, s44, v246
	v_med3_f32 v235, v235, s44, v246
	v_med3_f32 v236, v236, s44, v246
	v_med3_f32 v237, v237, s44, v246
	v_med3_f32 v238, v238, s44, v246
	v_med3_f32 v239, v239, s44, v246
	v_med3_f32 v240, v240, s44, v246
	v_med3_f32 v241, v241, s44, v246
	v_mov_b32_e32 v242, 0
	v_mov_b32_e32 v243, 0
	v_mov_b32_e32 v244, 0
	v_mov_b32_e32 v245, 0
	v_cvt_pk_fp8_f32 v242, v226, v227
	v_cvt_pk_fp8_f32 v243, v230, v231
	v_cvt_pk_fp8_f32 v244, v234, v235
	v_cvt_pk_fp8_f32 v245, v238, v239
	v_cvt_pk_fp8_f32 v242, v228, v229 op_sel:[0,0,1]
	v_cvt_pk_fp8_f32 v243, v232, v233 op_sel:[0,0,1]
	v_cvt_pk_fp8_f32 v244, v236, v237 op_sel:[0,0,1]
	v_cvt_pk_fp8_f32 v245, v240, v241 op_sel:[0,0,1]
	s_nop 0
	global_store_dwordx4 v216, v[242:245], s[6:7]
	s_add_i32 s25, s25, 1
	s_and_b32 s26, s25, 3
	s_cmp_eq_u32 s26, 0
	s_mov_b32 s26, 0xfd001000
	s_cselect_b32 s26, s26, 0x1000000
	s_cselect_b32 s27, -1, 0
	s_add_u32 s6, s6, s26
	s_addc_u32 s7, s7, s27
	s_waitcnt vmcnt(12)
	v_mul_f32_e32 v176, 0x43000000, v176
	v_mul_f32_e32 v177, 0x43000000, v177
	v_mul_f32_e32 v178, 0x43000000, v178
	v_mul_f32_e32 v179, 0x43000000, v179
	ds_write_b128 v210, v[176:179]
	v_mul_f32_e32 v180, 0x43000000, v180
	v_mul_f32_e32 v181, 0x43000000, v181
	v_mul_f32_e32 v182, 0x43000000, v182
	v_mul_f32_e32 v183, 0x43000000, v183
	ds_write_b128 v210, v[180:183] offset:1024
	v_mul_f32_e32 v184, 0x43000000, v184
	v_mul_f32_e32 v185, 0x43000000, v185
	v_mul_f32_e32 v186, 0x43000000, v186
	v_mul_f32_e32 v187, 0x43000000, v187
	ds_write_b128 v210, v[184:187] offset:2048
	v_mul_f32_e32 v188, 0x43000000, v188
	v_mul_f32_e32 v189, 0x43000000, v189
	v_mul_f32_e32 v190, 0x43000000, v190
	v_mul_f32_e32 v191, 0x43000000, v191
	ds_write_b128 v210, v[188:191] offset:3072
	v_mul_f32_e32 v192, 0x43000000, v192
	v_mul_f32_e32 v193, 0x43000000, v193
	v_mul_f32_e32 v194, 0x43000000, v194
	v_mul_f32_e32 v195, 0x43000000, v195
	ds_write_b128 v210, v[192:195] offset:4096
	v_mul_f32_e32 v196, 0x43000000, v196
	v_mul_f32_e32 v197, 0x43000000, v197
	v_mul_f32_e32 v198, 0x43000000, v198
	v_mul_f32_e32 v199, 0x43000000, v199
	ds_write_b128 v210, v[196:199] offset:5120
	v_mul_f32_e32 v200, 0x43000000, v200
	v_mul_f32_e32 v201, 0x43000000, v201
	v_mul_f32_e32 v202, 0x43000000, v202
	v_mul_f32_e32 v203, 0x43000000, v203
	ds_write_b128 v210, v[200:203] offset:6144
	v_mul_f32_e32 v204, 0x43000000, v204
	v_mul_f32_e32 v205, 0x43000000, v205
	v_mul_f32_e32 v206, 0x43000000, v206
	v_mul_f32_e32 v207, 0x43000000, v207
	ds_write_b128 v210, v[204:207] offset:7168
	s_waitcnt lgkmcnt(0)
	s_barrier
	s_mov_b64 s[8:9], s[4:5]
	global_load_dwordx4 v[176:179], v208, s[8:9]
	s_add_u32 s8, s8, 0x8000
	s_addc_u32 s9, s9, 0
	global_load_dwordx4 v[180:183], v208, s[8:9]
	s_add_u32 s8, s8, 0x8000
	s_addc_u32 s9, s9, 0
	global_load_dwordx4 v[184:187], v208, s[8:9]
	s_add_u32 s8, s8, 0x8000
	s_addc_u32 s9, s9, 0
	global_load_dwordx4 v[188:191], v208, s[8:9]
	s_add_u32 s8, s8, 0x8000
	s_addc_u32 s9, s9, 0
	global_load_dwordx4 v[192:195], v208, s[8:9]
	s_add_u32 s8, s8, 0x8000
	s_addc_u32 s9, s9, 0
	global_load_dwordx4 v[196:199], v208, s[8:9]
	s_add_u32 s8, s8, 0x8000
	s_addc_u32 s9, s9, 0
	global_load_dwordx4 v[200:203], v208, s[8:9]
	s_add_u32 s8, s8, 0x8000
	s_addc_u32 s9, s9, 0
	global_load_dwordx4 v[204:207], v208, s[8:9]
	s_add_i32 s24, s24, 1
	s_and_b32 s26, s24, 3
	s_cmp_eq_u32 s26, 0
	s_mov_b32 s26, 0x3ffd000
	s_cselect_b32 s26, s26, 0x1000
	s_add_u32 s4, s4, s26
	s_addc_u32 s5, s5, 0
	ds_read_b32 v226, v212
	ds_read_b32 v227, v212 offset:512
	ds_read_b32 v228, v212 offset:1024
	ds_read_b32 v229, v212 offset:1536
	ds_read_b32 v230, v212 offset:2048
	ds_read_b32 v231, v212 offset:2560
	ds_read_b32 v232, v212 offset:3072
	ds_read_b32 v233, v212 offset:3584
	ds_read_b32 v234, v212 offset:4096
	ds_read_b32 v235, v212 offset:4608
	ds_read_b32 v236, v212 offset:5120
	ds_read_b32 v237, v212 offset:5632
	ds_read_b32 v238, v212 offset:6144
	ds_read_b32 v239, v212 offset:6656
	ds_read_b32 v240, v212 offset:7168
	ds_read_b32 v241, v212 offset:7680
	s_waitcnt lgkmcnt(0)
; #define GAS __attribute__((address_space(1)))
; #define LAS __attribute__((address_space(3)))
; #define LDS_WAIT() asm volatile("s_waitcnt lgkmcnt(0)" ::: "memory")
;     const int pr = item >> 1, kb = 2 * (pr / nblk) + (item & 1), nb = pr % nblk, k0 = 64 * kb, n0 = 32 * nb;
;     const int nr = n0 + (lane & 31); const int sc = MAP == 1 ? src_col_in(nr) : nr;
;     float v[32];
; #pragma unroll
;     for (int i = 0; i < 32; ++i) v[i] = sc >= 0 ? W[(size_t)(k0 + 2 * i + (lane >> 5)) * Nsrc + sc] : 0.f;
; #pragma unroll
;     for (int i = 0; i < 32; ++i) { const int k = k0 + 2 * i + (lane >> 5); float x = v[i] * wscale; if (KS) x *= (k < ksplit ? ksA[k] : ksB[k - ksplit]); scr[(2 * i + (lane >> 5)) * 33 + (lane & 31)] = x; }
;     LDS_WAIT(); asm volatile("" ::: "memory");
;     const int c = lane & 7;
; #pragma unroll
;     for (int j = 0; j < 4; ++j) { const int n = (lane >> 3) + 8 * j; const LAS float* s = scr + (8 * c) * 33 + n;
;         const unsigned long long o = (unsigned long long)pg8::pk4_fp8(s[0 * 33], s[1 * 33], s[2 * 33], s[3 * 33]) | ((unsigned long long)pg8::pk4_fp8(s[4 * 33], s[5 * 33], s[6 * 33], s[7 * 33]) << 32);
;         *(GAS unsigned long long*)(WT + (size_t)(n0 + n) * K + k0 + 8 * c) = o; }
;     LDS_WAIT(); asm volatile("" ::: "memory");
; }
	v_max_f32_e32 v226, v226, v226
	v_max_f32_e32 v227, v227, v227
	v_max_f32_e32 v228, v228, v228
	v_max_f32_e32 v229, v229, v229
	v_max_f32_e32 v230, v230, v230
	v_max_f32_e32 v231, v231, v231
	v_max_f32_e32 v232, v232, v232
	v_max_f32_e32 v233, v233, v233
	v_max_f32_e32 v234, v234, v234
	v_max_f32_e32 v235, v235, v235
	v_max_f32_e32 v236, v236, v236
	v_max_f32_e32 v237, v237, v237
	v_max_f32_e32 v238, v238, v238
	v_max_f32_e32 v239, v239, v239
	v_max_f32_e32 v240, v240, v240
	v_max_f32_e32 v241, v241, v241
	v_med3_f32 v226, v226, s44, v246
	v_med3_f32 v227, v227, s44, v246
	v_med3_f32 v228, v228, s44, v246
	v_med3_f32 v229, v229, s44, v246
	v_med3_f32 v230, v230, s44, v246
	v_med3_f32 v231, v231, s44, v246
	v_med3_f32 v232, v232, s44, v246
	v_med3_f32 v233, v233, s44, v246
	v_med3_f32 v234, v234, s44, v246
	v_med3_f32 v235, v235, s44, v246
	v_med3_f32 v236, v236, s44, v246
	v_med3_f32 v237, v237, s44, v246
	v_med3_f32 v238, v238, s44, v246
	v_med3_f32 v239, v239, s44, v246
	v_med3_f32 v240, v240, s44, v246
	v_med3_f32 v241, v241, s44, v246
	v_mov_b32_e32 v242, 0
	v_mov_b32_e32 v243, 0
	v_mov_b32_e32 v244, 0
	v_mov_b32_e32 v245, 0
	v_cvt_pk_fp8_f32 v242, v226, v227
	v_cvt_pk_fp8_f32 v243, v230, v231
	v_cvt_pk_fp8_f32 v244, v234, v235
	v_cvt_pk_fp8_f32 v245, v238, v239
	v_cvt_pk_fp8_f32 v242, v228, v229 op_sel:[0,0,1]
	v_cvt_pk_fp8_f32 v243, v232, v233 op_sel:[0,0,1]
	v_cvt_pk_fp8_f32 v244, v236, v237 op_sel:[0,0,1]
	v_cvt_pk_fp8_f32 v245, v240, v241 op_sel:[0,0,1]
	s_nop 0
	global_store_dwordx4 v215, v[242:245], s[6:7]
	ds_read_b32 v226, v214
	ds_read_b32 v227, v214 offset:512
	ds_read_b32 v228, v214 offset:1024
	ds_read_b32 v229, v214 offset:1536
	ds_read_b32 v230, v214 offset:2048
	ds_read_b32 v231, v214 offset:2560
	ds_read_b32 v232, v214 offset:3072
	ds_read_b32 v233, v214 offset:3584
	ds_read_b32 v234, v214 offset:4096
	ds_read_b32 v235, v214 offset:4608
	ds_read_b32 v236, v214 offset:5120
	ds_read_b32 v237, v214 offset:5632
	ds_read_b32 v238, v214 offset:6144
	ds_read_b32 v239, v214 offset:6656
	ds_read_b32 v240, v214 offset:7168
	ds_read_b32 v241, v214 offset:7680
	s_waitcnt lgkmcnt(0)
	v_max_f32_e32 v226, v226, v226
	v_max_f32_e32 v227, v227, v227
	v_max_f32_e32 v228, v228, v228
	v_max_f32_e32 v229, v229, v229
	v_max_f32_e32 v230, v230, v230
	v_max_f32_e32 v231, v231, v231
	v_max_f32_e32 v232, v232, v232
	v_max_f32_e32 v233, v233, v233
	v_max_f32_e32 v234, v234, v234
	v_max_f32_e32 v235, v235, v235
	v_max_f32_e32 v236, v236, v236
	v_max_f32_e32 v237, v237, v237
	v_max_f32_e32 v238, v238, v238
	v_max_f32_e32 v239, v239, v239
	v_max_f32_e32 v240, v240, v240
	v_max_f32_e32 v241, v241, v241
	v_med3_f32 v226, v226, s44, v246
	v_med3_f32 v227, v227, s44, v246
	v_med3_f32 v228, v228, s44, v246
	v_med3_f32 v229, v229, s44, v246
	v_med3_f32 v230, v230, s44, v246
	v_med3_f32 v231, v231, s44, v246
	v_med3_f32 v232, v232, s44, v246
	v_med3_f32 v233, v233, s44, v246
	v_med3_f32 v234, v234, s44, v246
	v_med3_f32 v235, v235, s44, v246
	v_med3_f32 v236, v236, s44, v246
	v_med3_f32 v237, v237, s44, v246
	v_med3_f32 v238, v238, s44, v246
	v_med3_f32 v239, v239, s44, v246
	v_med3_f32 v240, v240, s44, v246
	v_med3_f32 v241, v241, s44, v246
	v_mov_b32_e32 v242, 0
	v_mov_b32_e32 v243, 0
	v_mov_b32_e32 v244, 0
	v_mov_b32_e32 v245, 0
	v_cvt_pk_fp8_f32 v242, v226, v227
	v_cvt_pk_fp8_f32 v243, v230, v231
	v_cvt_pk_fp8_f32 v244, v234, v235
	v_cvt_pk_fp8_f32 v245, v238, v239
	v_cvt_pk_fp8_f32 v242, v228, v229 op_sel:[0,0,1]
	v_cvt_pk_fp8_f32 v243, v232, v233 op_sel:[0,0,1]
	v_cvt_pk_fp8_f32 v244, v236, v237 op_sel:[0,0,1]
	v_cvt_pk_fp8_f32 v245, v240, v241 op_sel:[0,0,1]
	s_nop 0
	global_store_dwordx4 v216, v[242:245], s[6:7]
	s_add_i32 s25, s25, 1
	s_and_b32 s26, s25, 3
	s_cmp_eq_u32 s26, 0
	s_mov_b32 s26, 0xfd001000
	s_cselect_b32 s26, s26, 0x1000000
	s_cselect_b32 s27, -1, 0
	s_add_u32 s6, s6, s26
	s_addc_u32 s7, s7, s27
	s_sub_i32 s12, s12, 1
	s_cmp_lg_u32 s12, 0
	s_cbranch_scc1 .Lco_wdn_loop
	s_waitcnt vmcnt(12)
	v_mul_f32_e32 v144, 0x43000000, v144
	v_mul_f32_e32 v145, 0x43000000, v145
	v_mul_f32_e32 v146, 0x43000000, v146
	v_mul_f32_e32 v147, 0x43000000, v147
	ds_write_b128 v209, v[144:147]
	v_mul_f32_e32 v148, 0x43000000, v148
	v_mul_f32_e32 v149, 0x43000000, v149
	v_mul_f32_e32 v150, 0x43000000, v150
	v_mul_f32_e32 v151, 0x43000000, v151
	ds_write_b128 v209, v[148:151] offset:1024
	v_mul_f32_e32 v152, 0x43000000, v152
	v_mul_f32_e32 v153, 0x43000000, v153
	v_mul_f32_e32 v154, 0x43000000, v154
	v_mul_f32_e32 v155, 0x43000000, v155
	ds_write_b128 v209, v[152:155] offset:2048
	v_mul_f32_e32 v156, 0x43000000, v156
	v_mul_f32_e32 v157, 0x43000000, v157
	v_mul_f32_e32 v158, 0x43000000, v158
	v_mul_f32_e32 v159, 0x43000000, v159
	ds_write_b128 v209, v[156:159] offset:3072
	v_mul_f32_e32 v160, 0x43000000, v160
	v_mul_f32_e32 v161, 0x43000000, v161
	v_mul_f32_e32 v162, 0x43000000, v162
	v_mul_f32_e32 v163, 0x43000000, v163
	ds_write_b128 v209, v[160:163] offset:4096
	v_mul_f32_e32 v164, 0x43000000, v164
	v_mul_f32_e32 v165, 0x43000000, v165
	v_mul_f32_e32 v166, 0x43000000, v166
	v_mul_f32_e32 v167, 0x43000000, v167
	ds_write_b128 v209, v[164:167] offset:5120
	v_mul_f32_e32 v168, 0x43000000, v168
	v_mul_f32_e32 v169, 0x43000000, v169
	v_mul_f32_e32 v170, 0x43000000, v170
	v_mul_f32_e32 v171, 0x43000000, v171
	ds_write_b128 v209, v[168:171] offset:6144
	v_mul_f32_e32 v172, 0x43000000, v172
	v_mul_f32_e32 v173, 0x43000000, v173
	v_mul_f32_e32 v174, 0x43000000, v174
	v_mul_f32_e32 v175, 0x43000000, v175
	ds_write_b128 v209, v[172:175] offset:7168
	s_waitcnt lgkmcnt(0)
	s_barrier
; #define GAS __attribute__((address_space(1)))
; #define LAS __attribute__((address_space(3)))
; #define LDS_WAIT() asm volatile("s_waitcnt lgkmcnt(0)" ::: "memory")
;     const int pr = item >> 1, kb = 2 * (pr / nblk) + (item & 1), nb = pr % nblk, k0 = 64 * kb, n0 = 32 * nb;
;     const int nr = n0 + (lane & 31); const int sc = MAP == 1 ? src_col_in(nr) : nr;
;     float v[32];
; #pragma unroll
;     for (int i = 0; i < 32; ++i) v[i] = sc >= 0 ? W[(size_t)(k0 + 2 * i + (lane >> 5)) * Nsrc + sc] : 0.f;
; #pragma unroll
;     for (int i = 0; i < 32; ++i) { const int k = k0 + 2 * i + (lane >> 5); float x = v[i] * wscale; if (KS) x *= (k < ksplit ? ksA[k] : ksB[k - ksplit]); scr[(2 * i + (lane >> 5)) * 33 + (lane & 31)] = x; }
;     LDS_WAIT(); asm volatile("" ::: "memory");
;     const int c = lane & 7;
; #pragma unroll
;     for (int j = 0; j < 4; ++j) { const int n = (lane >> 3) + 8 * j; const LAS float* s = scr + (8 * c) * 33 + n;
;         const unsigned long long o = (unsigned long long)pg8::pk4_fp8(s[0 * 33], s[1 * 33], s[2 * 33], s[3 * 33]) | ((unsigned long long)pg8::pk4_fp8(s[4 * 33], s[5 * 33], s[6 * 33], s[7 * 33]) << 32);
;         *(GAS unsigned long long*)(WT + (size_t)(n0 + n) * K + k0 + 8 * c) = o; }
;     LDS_WAIT(); asm volatile("" ::: "memory");
; }
	ds_read_b32 v226, v211
	ds_read_b32 v227, v211 offset:512
	ds_read_b32 v228, v211 offset:1024
	ds_read_b32 v229, v211 offset:1536
	ds_read_b32 v230, v211 offset:2048
	ds_read_b32 v231, v211 offset:2560
	ds_read_b32 v232, v211 offset:3072
	ds_read_b32 v233, v211 offset:3584
	ds_read_b32 v234, v211 offset:4096
	ds_read_b32 v235, v211 offset:4608
	ds_read_b32 v236, v211 offset:5120
	ds_read_b32 v237, v211 offset:5632
	ds_read_b32 v238, v211 offset:6144
	ds_read_b32 v239, v211 offset:6656
	ds_read_b32 v240, v211 offset:7168
	ds_read_b32 v241, v211 offset:7680
	s_waitcnt lgkmcnt(0)
	v_max_f32_e32 v226, v226, v226
	v_max_f32_e32 v227, v227, v227
	v_max_f32_e32 v228, v228, v228
	v_max_f32_e32 v229, v229, v229
	v_max_f32_e32 v230, v230, v230
	v_max_f32_e32 v231, v231, v231
	v_max_f32_e32 v232, v232, v232
	v_max_f32_e32 v233, v233, v233
	v_max_f32_e32 v234, v234, v234
	v_max_f32_e32 v235, v235, v235
	v_max_f32_e32 v236, v236, v236
	v_max_f32_e32 v237, v237, v237
	v_max_f32_e32 v238, v238, v238
	v_max_f32_e32 v239, v239, v239
	v_max_f32_e32 v240, v240, v240
	v_max_f32_e32 v241, v241, v241
	v_med3_f32 v226, v226, s44, v246
	v_med3_f32 v227, v227, s44, v246
	v_med3_f32 v228, v228, s44, v246
	v_med3_f32 v229, v229, s44, v246
	v_med3_f32 v230, v230, s44, v246
	v_med3_f32 v231, v231, s44, v246
	v_med3_f32 v232, v232, s44, v246
	v_med3_f32 v233, v233, s44, v246
	v_med3_f32 v234, v234, s44, v246
	v_med3_f32 v235, v235, s44, v246
	v_med3_f32 v236, v236, s44, v246
	v_med3_f32 v237, v237, s44, v246
	v_med3_f32 v238, v238, s44, v246
	v_med3_f32 v239, v239, s44, v246
	v_med3_f32 v240, v240, s44, v246
	v_med3_f32 v241, v241, s44, v246
	v_mov_b32_e32 v242, 0
	v_mov_b32_e32 v243, 0
	v_mov_b32_e32 v244, 0
	v_mov_b32_e32 v245, 0
	v_cvt_pk_fp8_f32 v242, v226, v227
	v_cvt_pk_fp8_f32 v243, v230, v231
	v_cvt_pk_fp8_f32 v244, v234, v235
	v_cvt_pk_fp8_f32 v245, v238, v239
	v_cvt_pk_fp8_f32 v242, v228, v229 op_sel:[0,0,1]
	v_cvt_pk_fp8_f32 v243, v232, v233 op_sel:[0,0,1]
	v_cvt_pk_fp8_f32 v244, v236, v237 op_sel:[0,0,1]
	v_cvt_pk_fp8_f32 v245, v240, v241 op_sel:[0,0,1]
	s_nop 0
	global_store_dwordx4 v215, v[242:245], s[6:7]
	ds_read_b32 v226, v213
	ds_read_b32 v227, v213 offset:512
	ds_read_b32 v228, v213 offset:1024
	ds_read_b32 v229, v213 offset:1536
	ds_read_b32 v230, v213 offset:2048
	ds_read_b32 v231, v213 offset:2560
	ds_read_b32 v232, v213 offset:3072
	ds_read_b32 v233, v213 offset:3584
	ds_read_b32 v234, v213 offset:4096
	ds_read_b32 v235, v213 offset:4608
	ds_read_b32 v236, v213 offset:5120
	ds_read_b32 v237, v213 offset:5632
	ds_read_b32 v238, v213 offset:6144
	ds_read_b32 v239, v213 offset:6656
	ds_read_b32 v240, v213 offset:7168
	ds_read_b32 v241, v213 offset:7680
	s_waitcnt lgkmcnt(0)
	v_max_f32_e32 v226, v226, v226
	v_max_f32_e32 v227, v227, v227
	v_max_f32_e32 v228, v228, v228
	v_max_f32_e32 v229, v229, v229
	v_max_f32_e32 v230, v230, v230
	v_max_f32_e32 v231, v231, v231
	v_max_f32_e32 v232, v232, v232
	v_max_f32_e32 v233, v233, v233
	v_max_f32_e32 v234, v234, v234
	v_max_f32_e32 v235, v235, v235
	v_max_f32_e32 v236, v236, v236
	v_max_f32_e32 v237, v237, v237
	v_max_f32_e32 v238, v238, v238
	v_max_f32_e32 v239, v239, v239
	v_max_f32_e32 v240, v240, v240
	v_max_f32_e32 v241, v241, v241
	v_med3_f32 v226, v226, s44, v246
	v_med3_f32 v227, v227, s44, v246
	v_med3_f32 v228, v228, s44, v246
	v_med3_f32 v229, v229, s44, v246
	v_med3_f32 v230, v230, s44, v246
	v_med3_f32 v231, v231, s44, v246
	v_med3_f32 v232, v232, s44, v246
	v_med3_f32 v233, v233, s44, v246
	v_med3_f32 v234, v234, s44, v246
	v_med3_f32 v235, v235, s44, v246
	v_med3_f32 v236, v236, s44, v246
	v_med3_f32 v237, v237, s44, v246
	v_med3_f32 v238, v238, s44, v246
	v_med3_f32 v239, v239, s44, v246
	v_med3_f32 v240, v240, s44, v246
	v_med3_f32 v241, v241, s44, v246
	v_mov_b32_e32 v242, 0
	v_mov_b32_e32 v243, 0
	v_mov_b32_e32 v244, 0
	v_mov_b32_e32 v245, 0
	v_cvt_pk_fp8_f32 v242, v226, v227
	v_cvt_pk_fp8_f32 v243, v230, v231
	v_cvt_pk_fp8_f32 v244, v234, v235
	v_cvt_pk_fp8_f32 v245, v238, v239
	v_cvt_pk_fp8_f32 v242, v228, v229 op_sel:[0,0,1]
	v_cvt_pk_fp8_f32 v243, v232, v233 op_sel:[0,0,1]
	v_cvt_pk_fp8_f32 v244, v236, v237 op_sel:[0,0,1]
	v_cvt_pk_fp8_f32 v245, v240, v241 op_sel:[0,0,1]
	s_nop 0
	global_store_dwordx4 v216, v[242:245], s[6:7]
	s_add_i32 s25, s25, 1
	s_and_b32 s26, s25, 3
	s_cmp_eq_u32 s26, 0
	s_mov_b32 s26, 0xfd001000
	s_cselect_b32 s26, s26, 0x1000000
	s_cselect_b32 s27, -1, 0
	s_add_u32 s6, s6, s26
	s_addc_u32 s7, s7, s27
	s_waitcnt vmcnt(4)
	v_mul_f32_e32 v176, 0x43000000, v176
	v_mul_f32_e32 v177, 0x43000000, v177
	v_mul_f32_e32 v178, 0x43000000, v178
	v_mul_f32_e32 v179, 0x43000000, v179
	ds_write_b128 v210, v[176:179]
	v_mul_f32_e32 v180, 0x43000000, v180
	v_mul_f32_e32 v181, 0x43000000, v181
	v_mul_f32_e32 v182, 0x43000000, v182
	v_mul_f32_e32 v183, 0x43000000, v183
	ds_write_b128 v210, v[180:183] offset:1024
	v_mul_f32_e32 v184, 0x43000000, v184
	v_mul_f32_e32 v185, 0x43000000, v185
	v_mul_f32_e32 v186, 0x43000000, v186
	v_mul_f32_e32 v187, 0x43000000, v187
	ds_write_b128 v210, v[184:187] offset:2048
	v_mul_f32_e32 v188, 0x43000000, v188
	v_mul_f32_e32 v189, 0x43000000, v189
	v_mul_f32_e32 v190, 0x43000000, v190
	v_mul_f32_e32 v191, 0x43000000, v191
	ds_write_b128 v210, v[188:191] offset:3072
	v_mul_f32_e32 v192, 0x43000000, v192
	v_mul_f32_e32 v193, 0x43000000, v193
	v_mul_f32_e32 v194, 0x43000000, v194
	v_mul_f32_e32 v195, 0x43000000, v195
	ds_write_b128 v210, v[192:195] offset:4096
	v_mul_f32_e32 v196, 0x43000000, v196
	v_mul_f32_e32 v197, 0x43000000, v197
	v_mul_f32_e32 v198, 0x43000000, v198
	v_mul_f32_e32 v199, 0x43000000, v199
	ds_write_b128 v210, v[196:199] offset:5120
	v_mul_f32_e32 v200, 0x43000000, v200
	v_mul_f32_e32 v201, 0x43000000, v201
	v_mul_f32_e32 v202, 0x43000000, v202
	v_mul_f32_e32 v203, 0x43000000, v203
	ds_write_b128 v210, v[200:203] offset:6144
	v_mul_f32_e32 v204, 0x43000000, v204
	v_mul_f32_e32 v205, 0x43000000, v205
	v_mul_f32_e32 v206, 0x43000000, v206
	v_mul_f32_e32 v207, 0x43000000, v207
	ds_write_b128 v210, v[204:207] offset:7168
	s_waitcnt lgkmcnt(0)
	s_barrier
; #define GAS __attribute__((address_space(1)))
;     const int pr = item >> 1, kb = 2 * (pr / nblk) + (item & 1), nb = pr % nblk, k0 = 64 * kb, n0 = 32 * nb;
;     const int nr = n0 + (lane & 31); const int sc = MAP == 1 ? src_col_in(nr) : nr;
;     float v[32];
; #pragma unroll
;     for (int i = 0; i < 32; ++i) v[i] = sc >= 0 ? W[(size_t)(k0 + 2 * i + (lane >> 5)) * Nsrc + sc] : 0.f;
; #pragma unroll
;     for (int i = 0; i < 32; ++i) { const int k = k0 + 2 * i + (lane >> 5); float x = v[i] * wscale; if (KS) x *= (k < ksplit ? ksA[k] : ksB[k - ksplit]); scr[(2 * i + (lane >> 5)) * 33 + (lane & 31)] = x; }
;     LDS_WAIT(); asm volatile("" ::: "memory");
;     const int c = lane & 7;
; #pragma unroll
;     for (int j = 0; j < 4; ++j) { const int n = (lane >> 3) + 8 * j; const LAS float* s = scr + (8 * c) * 33 + n;
;         const unsigned long long o = (unsigned long long)pg8::pk4_fp8(s[0 * 33], s[1 * 33], s[2 * 33], s[3 * 33]) | ((unsigned long long)pg8::pk4_fp8(s[4 * 33], s[5 * 33], s[6 * 33], s[7 * 33]) << 32);
;         *(GAS unsigned long long*)(WT + (size_t)(n0 + n) * K + k0 + 8 * c) = o; }
;     LDS_WAIT(); asm volatile("" ::: "memory");
; }
; __global__ void __launch_bounds__(NWAVES * 64, 2) hybrid_fwd(Args args) {
;     ...
;         for (int rep = 0; rep < REP_PRO; ++rep)
;         for (int it = gw; it < DEPTH * I_L; it += NGW) {
;             const int l = it / I_L; int r = it % I_L;
;             if (r < I_IN) { if (l >= PROJ_F8_FROM) p0_transpose_item_f8<true, 1>(args.in[2] + (size_t)l * DM * NSRC, DM, NSRC, NPROJ / 32, (unsigned char*)(ws + WS_WIN + l * SZ_WIN), WUP8_SCALE, args.in[1] + l * DM, args.in[1] + l * DM, DM, scr, r, lane);
;                 else p0_transpose_item<1, true>(args.in[2] + (size_t)l * DM * NSRC, DM, NSRC, NPROJ / 32, (bf16*)(ws + WS_WIN + l * SZ_WIN), args.in[1] + l * DM, args.in[1] + l * DM, DM, scr, r, lane); continue; } r -= I_IN;
;             if (r < I_O) { if (l >= WO_F8_FROM) p0_transpose_item_f8<true>(args.in[13] + (size_t)l * DM * DM, DM, DM, DM / 32, (unsigned char*)(ws + WS_WO + l * SZ_WO), 64.f, args.in[6] + l * 2048, args.in[12] + l * 2048, 2048, scr, r, lane);
;                 else p0_transpose_item<0, true>(args.in[13] + (size_t)l * DM * DM, DM, DM, DM / 32, (bf16*)(ws + WS_WO + l * SZ_WO), args.in[6] + l * 2048, args.in[12] + l * 2048, 2048, scr, r, lane); continue; } r -= I_O;
	ds_read_b32 v226, v212
	ds_read_b32 v227, v212 offset:512
	ds_read_b32 v228, v212 offset:1024
	ds_read_b32 v229, v212 offset:1536
	ds_read_b32 v230, v212 offset:2048
	ds_read_b32 v231, v212 offset:2560
	ds_read_b32 v232, v212 offset:3072
	ds_read_b32 v233, v212 offset:3584
	ds_read_b32 v234, v212 offset:4096
	ds_read_b32 v235, v212 offset:4608
	ds_read_b32 v236, v212 offset:5120
	ds_read_b32 v237, v212 offset:5632
	ds_read_b32 v238, v212 offset:6144
	ds_read_b32 v239, v212 offset:6656
	ds_read_b32 v240, v212 offset:7168
	ds_read_b32 v241, v212 offset:7680
	s_waitcnt lgkmcnt(0)
	v_max_f32_e32 v226, v226, v226
	v_max_f32_e32 v227, v227, v227
	v_max_f32_e32 v228, v228, v228
	v_max_f32_e32 v229, v229, v229
	v_max_f32_e32 v230, v230, v230
	v_max_f32_e32 v231, v231, v231
	v_max_f32_e32 v232, v232, v232
	v_max_f32_e32 v233, v233, v233
	v_max_f32_e32 v234, v234, v234
	v_max_f32_e32 v235, v235, v235
	v_max_f32_e32 v236, v236, v236
	v_max_f32_e32 v237, v237, v237
	v_max_f32_e32 v238, v238, v238
	v_max_f32_e32 v239, v239, v239
	v_max_f32_e32 v240, v240, v240
	v_max_f32_e32 v241, v241, v241
	v_med3_f32 v226, v226, s44, v246
	v_med3_f32 v227, v227, s44, v246
	v_med3_f32 v228, v228, s44, v246
	v_med3_f32 v229, v229, s44, v246
	v_med3_f32 v230, v230, s44, v246
	v_med3_f32 v231, v231, s44, v246
	v_med3_f32 v232, v232, s44, v246
	v_med3_f32 v233, v233, s44, v246
	v_med3_f32 v234, v234, s44, v246
	v_med3_f32 v235, v235, s44, v246
	v_med3_f32 v236, v236, s44, v246
	v_med3_f32 v237, v237, s44, v246
	v_med3_f32 v238, v238, s44, v246
	v_med3_f32 v239, v239, s44, v246
	v_med3_f32 v240, v240, s44, v246
	v_med3_f32 v241, v241, s44, v246
	v_mov_b32_e32 v242, 0
	v_mov_b32_e32 v243, 0
	v_mov_b32_e32 v244, 0
	v_mov_b32_e32 v245, 0
	v_cvt_pk_fp8_f32 v242, v226, v227
	v_cvt_pk_fp8_f32 v243, v230, v231
	v_cvt_pk_fp8_f32 v244, v234, v235
	v_cvt_pk_fp8_f32 v245, v238, v239
	v_cvt_pk_fp8_f32 v242, v228, v229 op_sel:[0,0,1]
	v_cvt_pk_fp8_f32 v243, v232, v233 op_sel:[0,0,1]
	v_cvt_pk_fp8_f32 v244, v236, v237 op_sel:[0,0,1]
	v_cvt_pk_fp8_f32 v245, v240, v241 op_sel:[0,0,1]
	s_nop 0
	global_store_dwordx4 v215, v[242:245], s[6:7]
	ds_read_b32 v226, v214
	ds_read_b32 v227, v214 offset:512
	ds_read_b32 v228, v214 offset:1024
	ds_read_b32 v229, v214 offset:1536
	ds_read_b32 v230, v214 offset:2048
	ds_read_b32 v231, v214 offset:2560
	ds_read_b32 v232, v214 offset:3072
	ds_read_b32 v233, v214 offset:3584
	ds_read_b32 v234, v214 offset:4096
	ds_read_b32 v235, v214 offset:4608
	ds_read_b32 v236, v214 offset:5120
	ds_read_b32 v237, v214 offset:5632
	ds_read_b32 v238, v214 offset:6144
	ds_read_b32 v239, v214 offset:6656
	ds_read_b32 v240, v214 offset:7168
	ds_read_b32 v241, v214 offset:7680
	s_waitcnt lgkmcnt(0)
	v_max_f32_e32 v226, v226, v226
	v_max_f32_e32 v227, v227, v227
	v_max_f32_e32 v228, v228, v228
	v_max_f32_e32 v229, v229, v229
	v_max_f32_e32 v230, v230, v230
	v_max_f32_e32 v231, v231, v231
	v_max_f32_e32 v232, v232, v232
	v_max_f32_e32 v233, v233, v233
	v_max_f32_e32 v234, v234, v234
	v_max_f32_e32 v235, v235, v235
	v_max_f32_e32 v236, v236, v236
	v_max_f32_e32 v237, v237, v237
	v_max_f32_e32 v238, v238, v238
	v_max_f32_e32 v239, v239, v239
	v_max_f32_e32 v240, v240, v240
	v_max_f32_e32 v241, v241, v241
	v_med3_f32 v226, v226, s44, v246
	v_med3_f32 v227, v227, s44, v246
	v_med3_f32 v228, v228, s44, v246
	v_med3_f32 v229, v229, s44, v246
	v_med3_f32 v230, v230, s44, v246
	v_med3_f32 v231, v231, s44, v246
	v_med3_f32 v232, v232, s44, v246
	v_med3_f32 v233, v233, s44, v246
	v_med3_f32 v234, v234, s44, v246
	v_med3_f32 v235, v235, s44, v246
	v_med3_f32 v236, v236, s44, v246
	v_med3_f32 v237, v237, s44, v246
	v_med3_f32 v238, v238, s44, v246
	v_med3_f32 v239, v239, s44, v246
	v_med3_f32 v240, v240, s44, v246
	v_med3_f32 v241, v241, s44, v246
	v_mov_b32_e32 v242, 0
	v_mov_b32_e32 v243, 0
	v_mov_b32_e32 v244, 0
	v_mov_b32_e32 v245, 0
	v_cvt_pk_fp8_f32 v242, v226, v227
	v_cvt_pk_fp8_f32 v243, v230, v231
	v_cvt_pk_fp8_f32 v244, v234, v235
	v_cvt_pk_fp8_f32 v245, v238, v239
	v_cvt_pk_fp8_f32 v242, v228, v229 op_sel:[0,0,1]
	v_cvt_pk_fp8_f32 v243, v232, v233 op_sel:[0,0,1]
	v_cvt_pk_fp8_f32 v244, v236, v237 op_sel:[0,0,1]
	v_cvt_pk_fp8_f32 v245, v240, v241 op_sel:[0,0,1]
	s_nop 0
	global_store_dwordx4 v216, v[242:245], s[6:7]
	s_add_i32 s25, s25, 1
	s_and_b32 s26, s25, 3
	s_cmp_eq_u32 s26, 0
	s_mov_b32 s26, 0xfd001000
	s_cselect_b32 s26, s26, 0x1000000
	s_cselect_b32 s27, -1, 0
	s_add_u32 s6, s6, s26
	s_addc_u32 s7, s7, s27
	s_add_u32 s16, s16, 0x10000000
	s_addc_u32 s17, s17, 0
	s_add_u32 s18, s18, 0x8000000
	s_addc_u32 s19, s19, 0
	s_add_i32 s13, s13, 1
	s_cmp_lg_u32 s13, 2
	s_cbranch_scc1 .Lco_wdn_layer
; #define GAS __attribute__((address_space(1)))
; #define LAS __attribute__((address_space(3)))
; #define LDS_WAIT() asm volatile("s_waitcnt lgkmcnt(0)" ::: "memory")
; __device__ __forceinline__ unsigned pk2(float lo, float hi) { return f2bf(lo) | (f2bf(hi) << 16); }
; __device__ __forceinline__ int src_col_in(int c) {
;     if (c < 5120) { const int blk = c >> 7, p = c & 127; const bool rope = blk < 16 || ((((blk - 16) >> 2) & 1) == 0); const int d = rope ? (p >> 1) + 64 * (p & 1) : p; return blk * 128 + d; }
;     if (c < OFF_Z) return c + 2096;
;     if (c < OFF_G) return c - 4048;
;     if (c < OFF_DT) return 5120 + (c - OFF_G);
;     if (c < NSRC) return c;
;     return -1;
; }
; __device__ __forceinline__ int nat_dim(int p) { return (p >> 1) + 64 * (p & 1); }
; template <int MAP, bool KS, bool KPERM = false>
; __device__ __forceinline__ void p0_transpose_item(const float* W, int K, int Nsrc, int nblk, bf16* WT, const float* ksA, const float* ksB, int ksplit, LAS float* scr, int item, int lane) {
;     const int kb = item / nblk, nb = item % nblk, k0 = 64 * kb, n0 = 32 * nb;
;     const int nr = n0 + (lane & 31); const int sc = MAP == 1 ? src_col_in(nr) : (MAP == 2 ? nat_dim(nr) : nr);
;     float v[32];
; #pragma unroll
;     for (int i = 0; i < 32; ++i) { const int k = k0 + 2 * i + (lane >> 5); const int ksrc = KPERM ? ((k & ~127) + nat_dim(k & 127)) : k;
;         v[i] = sc >= 0 ? W[(size_t)ksrc * Nsrc + sc] : 0.f; }
; #pragma unroll
;     for (int i = 0; i < 32; ++i) { const int kk = 2 * i + (lane >> 5); const int k = k0 + kk;
;         if (KS) v[i] *= (k < ksplit ? ksA[k] : ksB[k - ksplit]);
;         scr[kk * 33 + (lane & 31)] = v[i]; }
;     LDS_WAIT(); asm volatile("" ::: "memory");
;     const int c = lane & 7;
; #pragma unroll
;     for (int j = 0; j < 4; ++j) { const int n = (lane >> 3) + 8 * j; const LAS float* s = scr + (8 * c) * 33 + n;
;         v4u o; o.x = pk2(s[0 * 33], s[1 * 33]); o.y = pk2(s[2 * 33], s[3 * 33]); o.z = pk2(s[4 * 33], s[5 * 33]); o.w = pk2(s[6 * 33], s[7 * 33]);
;         *(GAS v4u*)(WT + (size_t)(n0 + n) * K + k0 + 8 * c) = o; }
;     LDS_WAIT(); asm volatile("" ::: "memory");
; }
	v_lshrrev_b32_e32 v246, 5, v249
	v_lshl_add_u32 v246, v250, 4, v246
	v_and_b32_e32 v247, 31, v249
	v_lshlrev_b32_e32 v247, 4, v247
	s_mov_b32 s20, 0xb140
	v_mad_u32_u24 v208, v246, s20, v247
	v_lshrrev_b32_e32 v246, 4, v249
	v_lshl_add_u32 v246, v250, 4, v246
	v_and_b32_e32 v247, 15, v249
	v_lshlrev_b32_e32 v247, 4, v247
	v_lshl_add_u32 v100, v246, 13, v247
	v_and_b32_e32 v248, 63, v246
	v_lshlrev_b32_e32 v248, 1, v248
	v_lshrrev_b32_e32 v246, 6, v246
	v_or_b32_e32 v248, v248, v246
	v_lshl_add_u32 v104, v248, 13, v247
	v_lshrrev_b32_e32 v246, 4, v249
	v_lshl_add_u32 v246, v250, 4, v246
	v_add_u32_e32 v246, 4, v246
	v_and_b32_e32 v247, 15, v249
	v_lshlrev_b32_e32 v247, 4, v247
	v_lshl_add_u32 v101, v246, 13, v247
	v_and_b32_e32 v248, 63, v246
	v_lshlrev_b32_e32 v248, 1, v248
	v_lshrrev_b32_e32 v246, 6, v246
	v_or_b32_e32 v248, v248, v246
	v_lshl_add_u32 v105, v248, 13, v247
	v_lshrrev_b32_e32 v246, 4, v249
	v_lshl_add_u32 v246, v250, 4, v246
	v_add_u32_e32 v246, 8, v246
	v_and_b32_e32 v247, 15, v249
	v_lshlrev_b32_e32 v247, 4, v247
	v_lshl_add_u32 v102, v246, 13, v247
	v_and_b32_e32 v248, 63, v246
	v_lshlrev_b32_e32 v248, 1, v248
	v_lshrrev_b32_e32 v246, 6, v246
	v_or_b32_e32 v248, v248, v246
	v_lshl_add_u32 v106, v248, 13, v247
	v_lshrrev_b32_e32 v246, 4, v249
	v_lshl_add_u32 v246, v250, 4, v246
	v_add_u32_e32 v246, 12, v246
	v_and_b32_e32 v247, 15, v249
	v_lshlrev_b32_e32 v247, 4, v247
	v_lshl_add_u32 v103, v246, 13, v247
	v_and_b32_e32 v248, 63, v246
	v_lshlrev_b32_e32 v248, 1, v248
	v_lshrrev_b32_e32 v246, 6, v246
	v_or_b32_e32 v248, v248, v246
	v_lshl_add_u32 v107, v248, 13, v247
	v_and_b32_e32 v246, 15, v249
	v_lshrrev_b32_e32 v247, 1, v246
	v_lshlrev_b32_e32 v248, 2, v250
	v_xor_b32_e32 v248, v248, v247
	v_lshlrev_b32_e32 v248, 4, v248
	v_lshl_add_u32 v248, v246, 12, v248
	v_lshrrev_b32_e32 v247, 4, v249
	v_lshl_add_u32 v112, v247, 2, v248
	v_add_u32_e32 v113, 0x10000, v112
	v_and_b32_e32 v246, 15, v249
	v_lshrrev_b32_e32 v247, 1, v246
	v_lshlrev_b32_e32 v248, 2, v250
	v_add_u32_e32 v248, 1, v248
	v_xor_b32_e32 v248, v248, v247
	v_lshlrev_b32_e32 v248, 4, v248
	v_lshl_add_u32 v248, v246, 12, v248
	v_lshrrev_b32_e32 v247, 4, v249
	v_lshl_add_u32 v114, v247, 2, v248
	v_add_u32_e32 v115, 0x10000, v114
	v_and_b32_e32 v246, 15, v249
	v_lshrrev_b32_e32 v247, 1, v246
	v_lshlrev_b32_e32 v248, 2, v250
	v_add_u32_e32 v248, 2, v248
	v_xor_b32_e32 v248, v248, v247
	v_lshlrev_b32_e32 v248, 4, v248
	v_lshl_add_u32 v248, v246, 12, v248
	v_lshrrev_b32_e32 v247, 4, v249
	v_lshl_add_u32 v116, v247, 2, v248
	v_add_u32_e32 v117, 0x10000, v116
	v_and_b32_e32 v246, 15, v249
	v_lshrrev_b32_e32 v247, 1, v246
	v_lshlrev_b32_e32 v248, 2, v250
	v_add_u32_e32 v248, 3, v248
	v_xor_b32_e32 v248, v248, v247
	v_lshlrev_b32_e32 v248, 4, v248
	v_lshl_add_u32 v248, v246, 12, v248
	v_lshrrev_b32_e32 v247, 4, v249
	v_lshl_add_u32 v118, v247, 2, v248
	v_add_u32_e32 v119, 0x10000, v118
	s_lshr_b32 s22, s15, 3
	s_and_b32 s23, s15, 7
	v_readlane_b32 s16, v253, 7
	v_readlane_b32 s17, v253, 8
	v_readlane_b32 s18, v253, 41
	v_readlane_b32 s19, v253, 42
	s_mul_i32 s20, s22, 0x58a000
	s_add_u32 s16, s16, s20
	s_addc_u32 s17, s17, 0
	s_add_u32 s18, s18, 0x200000
	s_addc_u32 s19, s19, 0
	s_lshl_b32 s20, s22, 8
	s_add_u32 s18, s18, s20
	s_addc_u32 s19, s19, 0
	v_readlane_b32 s10, v253, 5
	v_readlane_b32 s11, v253, 6
	s_lshl_b32 s20, s22, 9
	s_add_u32 s10, s10, s20
	s_addc_u32 s11, s11, 0
	s_mov_b32 s44, 0xc3e00000
	v_mov_b32_e32 v246, 0x43e00000
	s_mov_b32 s28, 0x7fff
	s_mov_b32 s29, 0x07060302
	s_mov_b32 s24, s23
	s_add_i32 s25, s23, 8
	s_lshl_b32 s20, s24, 7
	s_cmp_lt_u32 s24, 40
	s_cselect_b32 s21, 0, 0x830
	s_cmp_lt_u32 s24, 72
	s_cselect_b32 s21, s21, 0xfffff030
	s_add_i32 s20, s20, s21
	s_lshl_b32 s20, s20, 2
	s_add_u32 s8, s16, s20
	s_addc_u32 s9, s17, 0
	global_load_dwordx4 v[144:147], v208, s[8:9]
	s_add_u32 s8, s8, 0x16280
	s_addc_u32 s9, s9, 0
	global_load_dwordx4 v[148:151], v208, s[8:9]
	s_add_u32 s8, s8, 0x16280
	s_addc_u32 s9, s9, 0
	global_load_dwordx4 v[152:155], v208, s[8:9]
	s_add_u32 s8, s8, 0x16280
	s_addc_u32 s9, s9, 0
	global_load_dwordx4 v[156:159], v208, s[8:9]
	s_add_u32 s8, s8, 0x16280
	s_addc_u32 s9, s9, 0
	global_load_dwordx4 v[160:163], v208, s[8:9]
	s_add_u32 s8, s8, 0x16280
	s_addc_u32 s9, s9, 0
	global_load_dwordx4 v[164:167], v208, s[8:9]
	s_add_u32 s8, s8, 0x16280
	s_addc_u32 s9, s9, 0
	global_load_dwordx4 v[168:171], v208, s[8:9]
	s_add_u32 s8, s8, 0x16280
	s_addc_u32 s9, s9, 0
	global_load_dwordx4 v[172:175], v208, s[8:9]
	s_lshl_b32 s20, s25, 7
	s_cmp_lt_u32 s25, 40
	s_cselect_b32 s21, 0, 0x830
	s_cmp_lt_u32 s25, 72
	s_cselect_b32 s21, s21, 0xfffff030
	s_add_i32 s20, s20, s21
	s_lshl_b32 s20, s20, 2
	s_add_u32 s8, s16, s20
	s_addc_u32 s9, s17, 0
	global_load_dwordx4 v[176:179], v208, s[8:9]
	s_add_u32 s8, s8, 0x16280
	s_addc_u32 s9, s9, 0
	global_load_dwordx4 v[180:183], v208, s[8:9]
	s_add_u32 s8, s8, 0x16280
	s_addc_u32 s9, s9, 0
	global_load_dwordx4 v[184:187], v208, s[8:9]
	s_add_u32 s8, s8, 0x16280
	s_addc_u32 s9, s9, 0
	global_load_dwordx4 v[188:191], v208, s[8:9]
	s_add_u32 s8, s8, 0x16280
	s_addc_u32 s9, s9, 0
	global_load_dwordx4 v[192:195], v208, s[8:9]
	s_add_u32 s8, s8, 0x16280
	s_addc_u32 s9, s9, 0
	global_load_dwordx4 v[196:199], v208, s[8:9]
	s_add_u32 s8, s8, 0x16280
	s_addc_u32 s9, s9, 0
	global_load_dwordx4 v[200:203], v208, s[8:9]
	s_add_u32 s8, s8, 0x16280
	s_addc_u32 s9, s9, 0
	global_load_dwordx4 v[204:207], v208, s[8:9]
	global_load_dword v218, v217, s[10:11] offset:0
	global_load_dword v219, v217, s[10:11] offset:8
	global_load_dword v220, v217, s[10:11] offset:16
	global_load_dword v221, v217, s[10:11] offset:24
	global_load_dword v222, v217, s[10:11] offset:32
	global_load_dword v223, v217, s[10:11] offset:40
	global_load_dword v224, v217, s[10:11] offset:48
	global_load_dword v225, v217, s[10:11] offset:56
	s_waitcnt vmcnt(0)
; #define GAS __attribute__((address_space(1)))
; #define LAS __attribute__((address_space(3)))
; #define LDS_WAIT() asm volatile("s_waitcnt lgkmcnt(0)" ::: "memory")
; __device__ __forceinline__ unsigned pk2(float lo, float hi) { return f2bf(lo) | (f2bf(hi) << 16); }
; __device__ __forceinline__ int nat_dim(int p) { return (p >> 1) + 64 * (p & 1); }
; template <int MAP, bool KS, bool KPERM = false>
; __device__ __forceinline__ void p0_transpose_item(const float* W, int K, int Nsrc, int nblk, bf16* WT, const float* ksA, const float* ksB, int ksplit, LAS float* scr, int item, int lane) {
;     const int kb = item / nblk, nb = item % nblk, k0 = 64 * kb, n0 = 32 * nb;
;     const int nr = n0 + (lane & 31); const int sc = MAP == 1 ? src_col_in(nr) : (MAP == 2 ? nat_dim(nr) : nr);
;     float v[32];
; #pragma unroll
;     for (int i = 0; i < 32; ++i) { const int k = k0 + 2 * i + (lane >> 5); const int ksrc = KPERM ? ((k & ~127) + nat_dim(k & 127)) : k;
;         v[i] = sc >= 0 ? W[(size_t)ksrc * Nsrc + sc] : 0.f; }
; #pragma unroll
;     for (int i = 0; i < 32; ++i) { const int kk = 2 * i + (lane >> 5); const int k = k0 + kk;
;         if (KS) v[i] *= (k < ksplit ? ksA[k] : ksB[k - ksplit]);
;         scr[kk * 33 + (lane & 31)] = v[i]; }
;     LDS_WAIT(); asm volatile("" ::: "memory");
;     const int c = lane & 7;
; #pragma unroll
;     for (int j = 0; j < 4; ++j) { const int n = (lane >> 3) + 8 * j; const LAS float* s = scr + (8 * c) * 33 + n;
;         v4u o; o.x = pk2(s[0 * 33], s[1 * 33]); o.y = pk2(s[2 * 33], s[3 * 33]); o.z = pk2(s[4 * 33], s[5 * 33]); o.w = pk2(s[6 * 33], s[7 * 33]);
;         *(GAS v4u*)(WT + (size_t)(n0 + n) * K + k0 + 8 * c) = o; }
;     LDS_WAIT(); asm volatile("" ::: "memory");
; }
	s_add_i32 s26, s23, 0
	s_add_i32 s27, s23, 16
	s_waitcnt vmcnt(8)
	v_mul_f32_e32 v144, v218, v144
	v_mul_f32_e32 v145, v218, v145
	v_mul_f32_e32 v146, v218, v146
	v_mul_f32_e32 v147, v218, v147
	ds_write_b128 v209, v[144:147]
	v_mul_f32_e32 v148, v219, v148
	v_mul_f32_e32 v149, v219, v149
	v_mul_f32_e32 v150, v219, v150
	v_mul_f32_e32 v151, v219, v151
	ds_write_b128 v209, v[148:151] offset:1024
	v_mul_f32_e32 v152, v220, v152
	v_mul_f32_e32 v153, v220, v153
	v_mul_f32_e32 v154, v220, v154
	v_mul_f32_e32 v155, v220, v155
	ds_write_b128 v209, v[152:155] offset:2048
	v_mul_f32_e32 v156, v221, v156
	v_mul_f32_e32 v157, v221, v157
	v_mul_f32_e32 v158, v221, v158
	v_mul_f32_e32 v159, v221, v159
	ds_write_b128 v209, v[156:159] offset:3072
	v_mul_f32_e32 v160, v222, v160
	v_mul_f32_e32 v161, v222, v161
	v_mul_f32_e32 v162, v222, v162
	v_mul_f32_e32 v163, v222, v163
	ds_write_b128 v209, v[160:163] offset:4096
	v_mul_f32_e32 v164, v223, v164
	v_mul_f32_e32 v165, v223, v165
	v_mul_f32_e32 v166, v223, v166
	v_mul_f32_e32 v167, v223, v167
	ds_write_b128 v209, v[164:167] offset:5120
	v_mul_f32_e32 v168, v224, v168
	v_mul_f32_e32 v169, v224, v169
	v_mul_f32_e32 v170, v224, v170
	v_mul_f32_e32 v171, v224, v171
	ds_write_b128 v209, v[168:171] offset:6144
	v_mul_f32_e32 v172, v225, v172
	v_mul_f32_e32 v173, v225, v173
	v_mul_f32_e32 v174, v225, v174
	v_mul_f32_e32 v175, v225, v175
	ds_write_b128 v209, v[172:175] offset:7168
	s_waitcnt lgkmcnt(0)
	s_barrier
	s_lshl_b32 s20, s27, 7
	s_cmp_lt_u32 s27, 40
	s_cselect_b32 s21, 0, 0x830
	s_cmp_lt_u32 s27, 72
	s_cselect_b32 s21, s21, 0xfffff030
	s_add_i32 s20, s20, s21
	s_lshl_b32 s20, s20, 2
	s_add_u32 s8, s16, s20
	s_addc_u32 s9, s17, 0
	global_load_dwordx4 v[144:147], v208, s[8:9]
	s_add_u32 s8, s8, 0x16280
	s_addc_u32 s9, s9, 0
	global_load_dwordx4 v[148:151], v208, s[8:9]
	s_add_u32 s8, s8, 0x16280
	s_addc_u32 s9, s9, 0
	global_load_dwordx4 v[152:155], v208, s[8:9]
	s_add_u32 s8, s8, 0x16280
	s_addc_u32 s9, s9, 0
	global_load_dwordx4 v[156:159], v208, s[8:9]
	s_add_u32 s8, s8, 0x16280
	s_addc_u32 s9, s9, 0
	global_load_dwordx4 v[160:163], v208, s[8:9]
	s_add_u32 s8, s8, 0x16280
	s_addc_u32 s9, s9, 0
	global_load_dwordx4 v[164:167], v208, s[8:9]
	s_add_u32 s8, s8, 0x16280
	s_addc_u32 s9, s9, 0
	global_load_dwordx4 v[168:171], v208, s[8:9]
	s_add_u32 s8, s8, 0x16280
	s_addc_u32 s9, s9, 0
	global_load_dwordx4 v[172:175], v208, s[8:9]
	s_mul_i32 s20, s26, 0x100000
	s_add_u32 s6, s18, s20
	s_addc_u32 s7, s19, 0
	s_cmp_lt_u32 s26, 16
	s_cselect_b32 s20, 1, 0
	s_sub_i32 s21, s26, 16
	s_bitcmp0_b32 s21, 2
	s_cselect_b32 s21, 1, 0
	s_cmp_lt_u32 s26, 40
	s_cselect_b32 s21, s21, 0
	s_or_b32 s20, s20, s21
	s_cmp_lg_u32 s20, 0
	s_cselect_b64 s[20:21], -1, 0
	v_cndmask_b32_e64 v108, v100, v104, s[20:21]
	v_cndmask_b32_e64 v109, v101, v105, s[20:21]
	v_cndmask_b32_e64 v110, v102, v106, s[20:21]
	v_cndmask_b32_e64 v111, v103, v107, s[20:21]
	ds_read_b32 v226, v112
	ds_read_b32 v227, v112 offset:512
	ds_read_b32 v228, v112 offset:1024
	ds_read_b32 v229, v112 offset:1536
	ds_read_b32 v230, v112 offset:2048
	ds_read_b32 v231, v112 offset:2560
	ds_read_b32 v232, v112 offset:3072
	ds_read_b32 v233, v112 offset:3584
	s_waitcnt lgkmcnt(0)
	v_bfe_u32 v120, v226, 16, 1
	v_bfe_u32 v121, v227, 16, 1
	v_bfe_u32 v122, v228, 16, 1
	v_bfe_u32 v123, v229, 16, 1
	v_bfe_u32 v124, v230, 16, 1
	v_bfe_u32 v125, v231, 16, 1
	v_bfe_u32 v126, v232, 16, 1
	v_bfe_u32 v127, v233, 16, 1
	v_add3_u32 v226, v226, v120, s28
	v_add3_u32 v227, v227, v121, s28
	v_add3_u32 v228, v228, v122, s28
	v_add3_u32 v229, v229, v123, s28
	v_add3_u32 v230, v230, v124, s28
	v_add3_u32 v231, v231, v125, s28
	v_add3_u32 v232, v232, v126, s28
	v_add3_u32 v233, v233, v127, s28
	v_perm_b32 v242, v227, v226, s29
	v_perm_b32 v243, v229, v228, s29
	v_perm_b32 v244, v231, v230, s29
	v_perm_b32 v245, v233, v232, s29
	s_nop 0
	global_store_dwordx4 v108, v[242:245], s[6:7]
	ds_read_b32 v226, v114
	ds_read_b32 v227, v114 offset:512
	ds_read_b32 v228, v114 offset:1024
	ds_read_b32 v229, v114 offset:1536
	ds_read_b32 v230, v114 offset:2048
	ds_read_b32 v231, v114 offset:2560
	ds_read_b32 v232, v114 offset:3072
	ds_read_b32 v233, v114 offset:3584
	s_waitcnt lgkmcnt(0)
	v_bfe_u32 v120, v226, 16, 1
	v_bfe_u32 v121, v227, 16, 1
	v_bfe_u32 v122, v228, 16, 1
	v_bfe_u32 v123, v229, 16, 1
	v_bfe_u32 v124, v230, 16, 1
	v_bfe_u32 v125, v231, 16, 1
	v_bfe_u32 v126, v232, 16, 1
	v_bfe_u32 v127, v233, 16, 1
	v_add3_u32 v226, v226, v120, s28
	v_add3_u32 v227, v227, v121, s28
	v_add3_u32 v228, v228, v122, s28
	v_add3_u32 v229, v229, v123, s28
	v_add3_u32 v230, v230, v124, s28
	v_add3_u32 v231, v231, v125, s28
	v_add3_u32 v232, v232, v126, s28
	v_add3_u32 v233, v233, v127, s28
	v_perm_b32 v242, v227, v226, s29
	v_perm_b32 v243, v229, v228, s29
	v_perm_b32 v244, v231, v230, s29
	v_perm_b32 v245, v233, v232, s29
	s_nop 0
	global_store_dwordx4 v109, v[242:245], s[6:7]
	ds_read_b32 v226, v116
	ds_read_b32 v227, v116 offset:512
	ds_read_b32 v228, v116 offset:1024
	ds_read_b32 v229, v116 offset:1536
	ds_read_b32 v230, v116 offset:2048
	ds_read_b32 v231, v116 offset:2560
	ds_read_b32 v232, v116 offset:3072
	ds_read_b32 v233, v116 offset:3584
	s_waitcnt lgkmcnt(0)
; #define GAS __attribute__((address_space(1)))
; #define LAS __attribute__((address_space(3)))
; #define LDS_WAIT() asm volatile("s_waitcnt lgkmcnt(0)" ::: "memory")
; __device__ __forceinline__ unsigned pk2(float lo, float hi) { return f2bf(lo) | (f2bf(hi) << 16); }
; __device__ __forceinline__ int nat_dim(int p) { return (p >> 1) + 64 * (p & 1); }
; template <int MAP, bool KS, bool KPERM = false>
; __device__ __forceinline__ void p0_transpose_item(const float* W, int K, int Nsrc, int nblk, bf16* WT, const float* ksA, const float* ksB, int ksplit, LAS float* scr, int item, int lane) {
;     const int kb = item / nblk, nb = item % nblk, k0 = 64 * kb, n0 = 32 * nb;
;     const int nr = n0 + (lane & 31); const int sc = MAP == 1 ? src_col_in(nr) : (MAP == 2 ? nat_dim(nr) : nr);
;     float v[32];
; #pragma unroll
;     for (int i = 0; i < 32; ++i) { const int k = k0 + 2 * i + (lane >> 5); const int ksrc = KPERM ? ((k & ~127) + nat_dim(k & 127)) : k;
;         v[i] = sc >= 0 ? W[(size_t)ksrc * Nsrc + sc] : 0.f; }
; #pragma unroll
;     for (int i = 0; i < 32; ++i) { const int kk = 2 * i + (lane >> 5); const int k = k0 + kk;
;         if (KS) v[i] *= (k < ksplit ? ksA[k] : ksB[k - ksplit]);
;         scr[kk * 33 + (lane & 31)] = v[i]; }
;     LDS_WAIT(); asm volatile("" ::: "memory");
;     const int c = lane & 7;
; #pragma unroll
;     for (int j = 0; j < 4; ++j) { const int n = (lane >> 3) + 8 * j; const LAS float* s = scr + (8 * c) * 33 + n;
;         v4u o; o.x = pk2(s[0 * 33], s[1 * 33]); o.y = pk2(s[2 * 33], s[3 * 33]); o.z = pk2(s[4 * 33], s[5 * 33]); o.w = pk2(s[6 * 33], s[7 * 33]);
;         *(GAS v4u*)(WT + (size_t)(n0 + n) * K + k0 + 8 * c) = o; }
;     LDS_WAIT(); asm volatile("" ::: "memory");
; }
	v_bfe_u32 v120, v226, 16, 1
	v_bfe_u32 v121, v227, 16, 1
	v_bfe_u32 v122, v228, 16, 1
	v_bfe_u32 v123, v229, 16, 1
	v_bfe_u32 v124, v230, 16, 1
	v_bfe_u32 v125, v231, 16, 1
	v_bfe_u32 v126, v232, 16, 1
	v_bfe_u32 v127, v233, 16, 1
	v_add3_u32 v226, v226, v120, s28
	v_add3_u32 v227, v227, v121, s28
	v_add3_u32 v228, v228, v122, s28
	v_add3_u32 v229, v229, v123, s28
	v_add3_u32 v230, v230, v124, s28
	v_add3_u32 v231, v231, v125, s28
	v_add3_u32 v232, v232, v126, s28
	v_add3_u32 v233, v233, v127, s28
	v_perm_b32 v242, v227, v226, s29
	v_perm_b32 v243, v229, v228, s29
	v_perm_b32 v244, v231, v230, s29
	v_perm_b32 v245, v233, v232, s29
	s_nop 0
	global_store_dwordx4 v110, v[242:245], s[6:7]
	ds_read_b32 v226, v118
	ds_read_b32 v227, v118 offset:512
	ds_read_b32 v228, v118 offset:1024
	ds_read_b32 v229, v118 offset:1536
	ds_read_b32 v230, v118 offset:2048
	ds_read_b32 v231, v118 offset:2560
	ds_read_b32 v232, v118 offset:3072
	ds_read_b32 v233, v118 offset:3584
	s_waitcnt lgkmcnt(0)
	v_bfe_u32 v120, v226, 16, 1
	v_bfe_u32 v121, v227, 16, 1
	v_bfe_u32 v122, v228, 16, 1
	v_bfe_u32 v123, v229, 16, 1
	v_bfe_u32 v124, v230, 16, 1
	v_bfe_u32 v125, v231, 16, 1
	v_bfe_u32 v126, v232, 16, 1
	v_bfe_u32 v127, v233, 16, 1
	v_add3_u32 v226, v226, v120, s28
	v_add3_u32 v227, v227, v121, s28
	v_add3_u32 v228, v228, v122, s28
	v_add3_u32 v229, v229, v123, s28
	v_add3_u32 v230, v230, v124, s28
	v_add3_u32 v231, v231, v125, s28
	v_add3_u32 v232, v232, v126, s28
	v_add3_u32 v233, v233, v127, s28
	v_perm_b32 v242, v227, v226, s29
	v_perm_b32 v243, v229, v228, s29
	v_perm_b32 v244, v231, v230, s29
	v_perm_b32 v245, v233, v232, s29
	s_nop 0
	global_store_dwordx4 v111, v[242:245], s[6:7]
	s_add_i32 s26, s23, 8
	s_add_i32 s27, s23, 24
	s_waitcnt vmcnt(12)
	v_mul_f32_e32 v176, v218, v176
	v_mul_f32_e32 v177, v218, v177
	v_mul_f32_e32 v178, v218, v178
	v_mul_f32_e32 v179, v218, v179
	ds_write_b128 v210, v[176:179]
	v_mul_f32_e32 v180, v219, v180
	v_mul_f32_e32 v181, v219, v181
	v_mul_f32_e32 v182, v219, v182
	v_mul_f32_e32 v183, v219, v183
	ds_write_b128 v210, v[180:183] offset:1024
	v_mul_f32_e32 v184, v220, v184
	v_mul_f32_e32 v185, v220, v185
	v_mul_f32_e32 v186, v220, v186
	v_mul_f32_e32 v187, v220, v187
	ds_write_b128 v210, v[184:187] offset:2048
	v_mul_f32_e32 v188, v221, v188
	v_mul_f32_e32 v189, v221, v189
	v_mul_f32_e32 v190, v221, v190
	v_mul_f32_e32 v191, v221, v191
	ds_write_b128 v210, v[188:191] offset:3072
	v_mul_f32_e32 v192, v222, v192
	v_mul_f32_e32 v193, v222, v193
	v_mul_f32_e32 v194, v222, v194
	v_mul_f32_e32 v195, v222, v195
	ds_write_b128 v210, v[192:195] offset:4096
	v_mul_f32_e32 v196, v223, v196
	v_mul_f32_e32 v197, v223, v197
	v_mul_f32_e32 v198, v223, v198
	v_mul_f32_e32 v199, v223, v199
	ds_write_b128 v210, v[196:199] offset:5120
	v_mul_f32_e32 v200, v224, v200
	v_mul_f32_e32 v201, v224, v201
	v_mul_f32_e32 v202, v224, v202
	v_mul_f32_e32 v203, v224, v203
	ds_write_b128 v210, v[200:203] offset:6144
	v_mul_f32_e32 v204, v225, v204
	v_mul_f32_e32 v205, v225, v205
	v_mul_f32_e32 v206, v225, v206
	v_mul_f32_e32 v207, v225, v207
	ds_write_b128 v210, v[204:207] offset:7168
	s_waitcnt lgkmcnt(0)
	s_barrier
	s_lshl_b32 s20, s27, 7
	s_cmp_lt_u32 s27, 40
	s_cselect_b32 s21, 0, 0x830
	s_cmp_lt_u32 s27, 72
	s_cselect_b32 s21, s21, 0xfffff030
	s_add_i32 s20, s20, s21
	s_lshl_b32 s20, s20, 2
	s_add_u32 s8, s16, s20
	s_addc_u32 s9, s17, 0
	global_load_dwordx4 v[176:179], v208, s[8:9]
	s_add_u32 s8, s8, 0x16280
	s_addc_u32 s9, s9, 0
	global_load_dwordx4 v[180:183], v208, s[8:9]
	s_add_u32 s8, s8, 0x16280
	s_addc_u32 s9, s9, 0
	global_load_dwordx4 v[184:187], v208, s[8:9]
	s_add_u32 s8, s8, 0x16280
	s_addc_u32 s9, s9, 0
	global_load_dwordx4 v[188:191], v208, s[8:9]
	s_add_u32 s8, s8, 0x16280
	s_addc_u32 s9, s9, 0
	global_load_dwordx4 v[192:195], v208, s[8:9]
	s_add_u32 s8, s8, 0x16280
	s_addc_u32 s9, s9, 0
	global_load_dwordx4 v[196:199], v208, s[8:9]
	s_add_u32 s8, s8, 0x16280
	s_addc_u32 s9, s9, 0
	global_load_dwordx4 v[200:203], v208, s[8:9]
	s_add_u32 s8, s8, 0x16280
	s_addc_u32 s9, s9, 0
	global_load_dwordx4 v[204:207], v208, s[8:9]
	s_mul_i32 s20, s26, 0x100000
	s_add_u32 s6, s18, s20
	s_addc_u32 s7, s19, 0
	s_cmp_lt_u32 s26, 16
	s_cselect_b32 s20, 1, 0
	s_sub_i32 s21, s26, 16
	s_bitcmp0_b32 s21, 2
	s_cselect_b32 s21, 1, 0
	s_cmp_lt_u32 s26, 40
	s_cselect_b32 s21, s21, 0
	s_or_b32 s20, s20, s21
	s_cmp_lg_u32 s20, 0
	s_cselect_b64 s[20:21], -1, 0
	v_cndmask_b32_e64 v108, v100, v104, s[20:21]
	v_cndmask_b32_e64 v109, v101, v105, s[20:21]
	v_cndmask_b32_e64 v110, v102, v106, s[20:21]
	v_cndmask_b32_e64 v111, v103, v107, s[20:21]
	ds_read_b32 v226, v113
	ds_read_b32 v227, v113 offset:512
	ds_read_b32 v228, v113 offset:1024
	ds_read_b32 v229, v113 offset:1536
	ds_read_b32 v230, v113 offset:2048
	ds_read_b32 v231, v113 offset:2560
	ds_read_b32 v232, v113 offset:3072
	ds_read_b32 v233, v113 offset:3584
	s_waitcnt lgkmcnt(0)
	v_bfe_u32 v120, v226, 16, 1
	v_bfe_u32 v121, v227, 16, 1
	v_bfe_u32 v122, v228, 16, 1
	v_bfe_u32 v123, v229, 16, 1
	v_bfe_u32 v124, v230, 16, 1
	v_bfe_u32 v125, v231, 16, 1
	v_bfe_u32 v126, v232, 16, 1
	v_bfe_u32 v127, v233, 16, 1
	v_add3_u32 v226, v226, v120, s28
	v_add3_u32 v227, v227, v121, s28
	v_add3_u32 v228, v228, v122, s28
	v_add3_u32 v229, v229, v123, s28
	v_add3_u32 v230, v230, v124, s28
	v_add3_u32 v231, v231, v125, s28
	v_add3_u32 v232, v232, v126, s28
	v_add3_u32 v233, v233, v127, s28
	v_perm_b32 v242, v227, v226, s29
	v_perm_b32 v243, v229, v228, s29
	v_perm_b32 v244, v231, v230, s29
	v_perm_b32 v245, v233, v232, s29
	s_nop 0
	global_store_dwordx4 v108, v[242:245], s[6:7]
	ds_read_b32 v226, v115
	ds_read_b32 v227, v115 offset:512
	ds_read_b32 v228, v115 offset:1024
	ds_read_b32 v229, v115 offset:1536
	ds_read_b32 v230, v115 offset:2048
	ds_read_b32 v231, v115 offset:2560
	ds_read_b32 v232, v115 offset:3072
	ds_read_b32 v233, v115 offset:3584
	s_waitcnt lgkmcnt(0)
; #define GAS __attribute__((address_space(1)))
; #define LAS __attribute__((address_space(3)))
; #define LDS_WAIT() asm volatile("s_waitcnt lgkmcnt(0)" ::: "memory")
; __device__ __forceinline__ unsigned pk2(float lo, float hi) { return f2bf(lo) | (f2bf(hi) << 16); }
; __device__ __forceinline__ int nat_dim(int p) { return (p >> 1) + 64 * (p & 1); }
; template <int MAP, bool KS, bool KPERM = false>
; __device__ __forceinline__ void p0_transpose_item(const float* W, int K, int Nsrc, int nblk, bf16* WT, const float* ksA, const float* ksB, int ksplit, LAS float* scr, int item, int lane) {
;     const int kb = item / nblk, nb = item % nblk, k0 = 64 * kb, n0 = 32 * nb;
;     const int nr = n0 + (lane & 31); const int sc = MAP == 1 ? src_col_in(nr) : (MAP == 2 ? nat_dim(nr) : nr);
;     float v[32];
; #pragma unroll
;     for (int i = 0; i < 32; ++i) { const int k = k0 + 2 * i + (lane >> 5); const int ksrc = KPERM ? ((k & ~127) + nat_dim(k & 127)) : k;
;         v[i] = sc >= 0 ? W[(size_t)ksrc * Nsrc + sc] : 0.f; }
; #pragma unroll
;     for (int i = 0; i < 32; ++i) { const int kk = 2 * i + (lane >> 5); const int k = k0 + kk;
;         if (KS) v[i] *= (k < ksplit ? ksA[k] : ksB[k - ksplit]);
;         scr[kk * 33 + (lane & 31)] = v[i]; }
;     LDS_WAIT(); asm volatile("" ::: "memory");
;     const int c = lane & 7;
; #pragma unroll
;     for (int j = 0; j < 4; ++j) { const int n = (lane >> 3) + 8 * j; const LAS float* s = scr + (8 * c) * 33 + n;
;         v4u o; o.x = pk2(s[0 * 33], s[1 * 33]); o.y = pk2(s[2 * 33], s[3 * 33]); o.z = pk2(s[4 * 33], s[5 * 33]); o.w = pk2(s[6 * 33], s[7 * 33]);
;         *(GAS v4u*)(WT + (size_t)(n0 + n) * K + k0 + 8 * c) = o; }
;     LDS_WAIT(); asm volatile("" ::: "memory");
; }
	v_bfe_u32 v120, v226, 16, 1
	v_bfe_u32 v121, v227, 16, 1
	v_bfe_u32 v122, v228, 16, 1
	v_bfe_u32 v123, v229, 16, 1
	v_bfe_u32 v124, v230, 16, 1
	v_bfe_u32 v125, v231, 16, 1
	v_bfe_u32 v126, v232, 16, 1
	v_bfe_u32 v127, v233, 16, 1
	v_add3_u32 v226, v226, v120, s28
	v_add3_u32 v227, v227, v121, s28
	v_add3_u32 v228, v228, v122, s28
	v_add3_u32 v229, v229, v123, s28
	v_add3_u32 v230, v230, v124, s28
	v_add3_u32 v231, v231, v125, s28
	v_add3_u32 v232, v232, v126, s28
	v_add3_u32 v233, v233, v127, s28
	v_perm_b32 v242, v227, v226, s29
	v_perm_b32 v243, v229, v228, s29
	v_perm_b32 v244, v231, v230, s29
	v_perm_b32 v245, v233, v232, s29
	s_nop 0
	global_store_dwordx4 v109, v[242:245], s[6:7]
	ds_read_b32 v226, v117
	ds_read_b32 v227, v117 offset:512
	ds_read_b32 v228, v117 offset:1024
	ds_read_b32 v229, v117 offset:1536
	ds_read_b32 v230, v117 offset:2048
	ds_read_b32 v231, v117 offset:2560
	ds_read_b32 v232, v117 offset:3072
	ds_read_b32 v233, v117 offset:3584
	s_waitcnt lgkmcnt(0)
	v_bfe_u32 v120, v226, 16, 1
	v_bfe_u32 v121, v227, 16, 1
	v_bfe_u32 v122, v228, 16, 1
	v_bfe_u32 v123, v229, 16, 1
	v_bfe_u32 v124, v230, 16, 1
	v_bfe_u32 v125, v231, 16, 1
	v_bfe_u32 v126, v232, 16, 1
	v_bfe_u32 v127, v233, 16, 1
	v_add3_u32 v226, v226, v120, s28
	v_add3_u32 v227, v227, v121, s28
	v_add3_u32 v228, v228, v122, s28
	v_add3_u32 v229, v229, v123, s28
	v_add3_u32 v230, v230, v124, s28
	v_add3_u32 v231, v231, v125, s28
	v_add3_u32 v232, v232, v126, s28
	v_add3_u32 v233, v233, v127, s28
	v_perm_b32 v242, v227, v226, s29
	v_perm_b32 v243, v229, v228, s29
	v_perm_b32 v244, v231, v230, s29
	v_perm_b32 v245, v233, v232, s29
	s_nop 0
	global_store_dwordx4 v110, v[242:245], s[6:7]
	ds_read_b32 v226, v119
	ds_read_b32 v227, v119 offset:512
	ds_read_b32 v228, v119 offset:1024
	ds_read_b32 v229, v119 offset:1536
	ds_read_b32 v230, v119 offset:2048
	ds_read_b32 v231, v119 offset:2560
	ds_read_b32 v232, v119 offset:3072
	ds_read_b32 v233, v119 offset:3584
	s_waitcnt lgkmcnt(0)
	v_bfe_u32 v120, v226, 16, 1
	v_bfe_u32 v121, v227, 16, 1
	v_bfe_u32 v122, v228, 16, 1
	v_bfe_u32 v123, v229, 16, 1
	v_bfe_u32 v124, v230, 16, 1
	v_bfe_u32 v125, v231, 16, 1
	v_bfe_u32 v126, v232, 16, 1
	v_bfe_u32 v127, v233, 16, 1
	v_add3_u32 v226, v226, v120, s28
	v_add3_u32 v227, v227, v121, s28
	v_add3_u32 v228, v228, v122, s28
	v_add3_u32 v229, v229, v123, s28
	v_add3_u32 v230, v230, v124, s28
	v_add3_u32 v231, v231, v125, s28
	v_add3_u32 v232, v232, v126, s28
	v_add3_u32 v233, v233, v127, s28
	v_perm_b32 v242, v227, v226, s29
	v_perm_b32 v243, v229, v228, s29
	v_perm_b32 v244, v231, v230, s29
	v_perm_b32 v245, v233, v232, s29
	s_nop 0
	global_store_dwordx4 v111, v[242:245], s[6:7]
	s_add_i32 s26, s23, 16
	s_add_i32 s27, s23, 32
	s_waitcnt vmcnt(16)
	v_mul_f32_e32 v144, v218, v144
	v_mul_f32_e32 v145, v218, v145
	v_mul_f32_e32 v146, v218, v146
	v_mul_f32_e32 v147, v218, v147
	ds_write_b128 v209, v[144:147]
	v_mul_f32_e32 v148, v219, v148
	v_mul_f32_e32 v149, v219, v149
	v_mul_f32_e32 v150, v219, v150
	v_mul_f32_e32 v151, v219, v151
	ds_write_b128 v209, v[148:151] offset:1024
	v_mul_f32_e32 v152, v220, v152
	v_mul_f32_e32 v153, v220, v153
	v_mul_f32_e32 v154, v220, v154
	v_mul_f32_e32 v155, v220, v155
	ds_write_b128 v209, v[152:155] offset:2048
	v_mul_f32_e32 v156, v221, v156
	v_mul_f32_e32 v157, v221, v157
	v_mul_f32_e32 v158, v221, v158
	v_mul_f32_e32 v159, v221, v159
	ds_write_b128 v209, v[156:159] offset:3072
	v_mul_f32_e32 v160, v222, v160
	v_mul_f32_e32 v161, v222, v161
	v_mul_f32_e32 v162, v222, v162
	v_mul_f32_e32 v163, v222, v163
	ds_write_b128 v209, v[160:163] offset:4096
	v_mul_f32_e32 v164, v223, v164
	v_mul_f32_e32 v165, v223, v165
	v_mul_f32_e32 v166, v223, v166
	v_mul_f32_e32 v167, v223, v167
	ds_write_b128 v209, v[164:167] offset:5120
	v_mul_f32_e32 v168, v224, v168
	v_mul_f32_e32 v169, v224, v169
	v_mul_f32_e32 v170, v224, v170
	v_mul_f32_e32 v171, v224, v171
	ds_write_b128 v209, v[168:171] offset:6144
	v_mul_f32_e32 v172, v225, v172
	v_mul_f32_e32 v173, v225, v173
	v_mul_f32_e32 v174, v225, v174
	v_mul_f32_e32 v175, v225, v175
	ds_write_b128 v209, v[172:175] offset:7168
	s_waitcnt lgkmcnt(0)
	s_barrier
	s_lshl_b32 s20, s27, 7
	s_cmp_lt_u32 s27, 40
	s_cselect_b32 s21, 0, 0x830
	s_cmp_lt_u32 s27, 72
	s_cselect_b32 s21, s21, 0xfffff030
	s_add_i32 s20, s20, s21
	s_lshl_b32 s20, s20, 2
	s_add_u32 s8, s16, s20
	s_addc_u32 s9, s17, 0
	global_load_dwordx4 v[144:147], v208, s[8:9]
	s_add_u32 s8, s8, 0x16280
	s_addc_u32 s9, s9, 0
	global_load_dwordx4 v[148:151], v208, s[8:9]
	s_add_u32 s8, s8, 0x16280
	s_addc_u32 s9, s9, 0
	global_load_dwordx4 v[152:155], v208, s[8:9]
	s_add_u32 s8, s8, 0x16280
	s_addc_u32 s9, s9, 0
	global_load_dwordx4 v[156:159], v208, s[8:9]
	s_add_u32 s8, s8, 0x16280
	s_addc_u32 s9, s9, 0
	global_load_dwordx4 v[160:163], v208, s[8:9]
	s_add_u32 s8, s8, 0x16280
	s_addc_u32 s9, s9, 0
	global_load_dwordx4 v[164:167], v208, s[8:9]
	s_add_u32 s8, s8, 0x16280
	s_addc_u32 s9, s9, 0
	global_load_dwordx4 v[168:171], v208, s[8:9]
	s_add_u32 s8, s8, 0x16280
	s_addc_u32 s9, s9, 0
	global_load_dwordx4 v[172:175], v208, s[8:9]
	s_mul_i32 s20, s26, 0x100000
	s_add_u32 s6, s18, s20
	s_addc_u32 s7, s19, 0
	s_cmp_lt_u32 s26, 16
	s_cselect_b32 s20, 1, 0
	s_sub_i32 s21, s26, 16
	s_bitcmp0_b32 s21, 2
	s_cselect_b32 s21, 1, 0
	s_cmp_lt_u32 s26, 40
	s_cselect_b32 s21, s21, 0
	s_or_b32 s20, s20, s21
	s_cmp_lg_u32 s20, 0
	s_cselect_b64 s[20:21], -1, 0
	v_cndmask_b32_e64 v108, v100, v104, s[20:21]
	v_cndmask_b32_e64 v109, v101, v105, s[20:21]
	v_cndmask_b32_e64 v110, v102, v106, s[20:21]
	v_cndmask_b32_e64 v111, v103, v107, s[20:21]
	ds_read_b32 v226, v112
	ds_read_b32 v227, v112 offset:512
	ds_read_b32 v228, v112 offset:1024
	ds_read_b32 v229, v112 offset:1536
	ds_read_b32 v230, v112 offset:2048
	ds_read_b32 v231, v112 offset:2560
	ds_read_b32 v232, v112 offset:3072
	ds_read_b32 v233, v112 offset:3584
	s_waitcnt lgkmcnt(0)
; #define GAS __attribute__((address_space(1)))
; #define LAS __attribute__((address_space(3)))
; #define LDS_WAIT() asm volatile("s_waitcnt lgkmcnt(0)" ::: "memory")
; __device__ __forceinline__ unsigned pk2(float lo, float hi) { return f2bf(lo) | (f2bf(hi) << 16); }
; __device__ __forceinline__ int nat_dim(int p) { return (p >> 1) + 64 * (p & 1); }
; __device__ __forceinline__ int src_col_in(int c) {
;     if (c < 5120) { const int blk = c >> 7, p = c & 127; const bool rope = blk < 16 || ((((blk - 16) >> 2) & 1) == 0); const int d = rope ? (p >> 1) + 64 * (p & 1) : p; return blk * 128 + d; }
; template <int MAP, bool KS, bool KPERM = false>
; __device__ __forceinline__ void p0_transpose_item(const float* W, int K, int Nsrc, int nblk, bf16* WT, const float* ksA, const float* ksB, int ksplit, LAS float* scr, int item, int lane) {
;     const int kb = item / nblk, nb = item % nblk, k0 = 64 * kb, n0 = 32 * nb;
;     const int nr = n0 + (lane & 31); const int sc = MAP == 1 ? src_col_in(nr) : (MAP == 2 ? nat_dim(nr) : nr);
;     float v[32];
; #pragma unroll
;     for (int i = 0; i < 32; ++i) { const int k = k0 + 2 * i + (lane >> 5); const int ksrc = KPERM ? ((k & ~127) + nat_dim(k & 127)) : k;
;         v[i] = sc >= 0 ? W[(size_t)ksrc * Nsrc + sc] : 0.f; }
; #pragma unroll
;     for (int i = 0; i < 32; ++i) { const int kk = 2 * i + (lane >> 5); const int k = k0 + kk;
;         if (KS) v[i] *= (k < ksplit ? ksA[k] : ksB[k - ksplit]);
;         scr[kk * 33 + (lane & 31)] = v[i]; }
;     LDS_WAIT(); asm volatile("" ::: "memory");
;     const int c = lane & 7;
; #pragma unroll
;     for (int j = 0; j < 4; ++j) { const int n = (lane >> 3) + 8 * j; const LAS float* s = scr + (8 * c) * 33 + n;
;         v4u o; o.x = pk2(s[0 * 33], s[1 * 33]); o.y = pk2(s[2 * 33], s[3 * 33]); o.z = pk2(s[4 * 33], s[5 * 33]); o.w = pk2(s[6 * 33], s[7 * 33]);
;         *(GAS v4u*)(WT + (size_t)(n0 + n) * K + k0 + 8 * c) = o; }
;     LDS_WAIT(); asm volatile("" ::: "memory");
	v_bfe_u32 v120, v226, 16, 1
	v_bfe_u32 v121, v227, 16, 1
	v_bfe_u32 v122, v228, 16, 1
	v_bfe_u32 v123, v229, 16, 1
	v_bfe_u32 v124, v230, 16, 1
	v_bfe_u32 v125, v231, 16, 1
	v_bfe_u32 v126, v232, 16, 1
	v_bfe_u32 v127, v233, 16, 1
	v_add3_u32 v226, v226, v120, s28
	v_add3_u32 v227, v227, v121, s28
	v_add3_u32 v228, v228, v122, s28
	v_add3_u32 v229, v229, v123, s28
	v_add3_u32 v230, v230, v124, s28
	v_add3_u32 v231, v231, v125, s28
	v_add3_u32 v232, v232, v126, s28
	v_add3_u32 v233, v233, v127, s28
	v_perm_b32 v242, v227, v226, s29
	v_perm_b32 v243, v229, v228, s29
	v_perm_b32 v244, v231, v230, s29
	v_perm_b32 v245, v233, v232, s29
	s_nop 0
	global_store_dwordx4 v108, v[242:245], s[6:7]
	ds_read_b32 v226, v114
	ds_read_b32 v227, v114 offset:512
	ds_read_b32 v228, v114 offset:1024
	ds_read_b32 v229, v114 offset:1536
	ds_read_b32 v230, v114 offset:2048
	ds_read_b32 v231, v114 offset:2560
	ds_read_b32 v232, v114 offset:3072
	ds_read_b32 v233, v114 offset:3584
	s_waitcnt lgkmcnt(0)
	v_bfe_u32 v120, v226, 16, 1
	v_bfe_u32 v121, v227, 16, 1
	v_bfe_u32 v122, v228, 16, 1
	v_bfe_u32 v123, v229, 16, 1
	v_bfe_u32 v124, v230, 16, 1
	v_bfe_u32 v125, v231, 16, 1
	v_bfe_u32 v126, v232, 16, 1
	v_bfe_u32 v127, v233, 16, 1
	v_add3_u32 v226, v226, v120, s28
	v_add3_u32 v227, v227, v121, s28
	v_add3_u32 v228, v228, v122, s28
	v_add3_u32 v229, v229, v123, s28
	v_add3_u32 v230, v230, v124, s28
	v_add3_u32 v231, v231, v125, s28
	v_add3_u32 v232, v232, v126, s28
	v_add3_u32 v233, v233, v127, s28
	v_perm_b32 v242, v227, v226, s29
	v_perm_b32 v243, v229, v228, s29
	v_perm_b32 v244, v231, v230, s29
	v_perm_b32 v245, v233, v232, s29
	s_nop 0
	global_store_dwordx4 v109, v[242:245], s[6:7]
	ds_read_b32 v226, v116
	ds_read_b32 v227, v116 offset:512
	ds_read_b32 v228, v116 offset:1024
	ds_read_b32 v229, v116 offset:1536
	ds_read_b32 v230, v116 offset:2048
	ds_read_b32 v231, v116 offset:2560
	ds_read_b32 v232, v116 offset:3072
	ds_read_b32 v233, v116 offset:3584
	s_waitcnt lgkmcnt(0)
	v_bfe_u32 v120, v226, 16, 1
	v_bfe_u32 v121, v227, 16, 1
	v_bfe_u32 v122, v228, 16, 1
	v_bfe_u32 v123, v229, 16, 1
	v_bfe_u32 v124, v230, 16, 1
	v_bfe_u32 v125, v231, 16, 1
	v_bfe_u32 v126, v232, 16, 1
	v_bfe_u32 v127, v233, 16, 1
	v_add3_u32 v226, v226, v120, s28
	v_add3_u32 v227, v227, v121, s28
	v_add3_u32 v228, v228, v122, s28
	v_add3_u32 v229, v229, v123, s28
	v_add3_u32 v230, v230, v124, s28
	v_add3_u32 v231, v231, v125, s28
	v_add3_u32 v232, v232, v126, s28
	v_add3_u32 v233, v233, v127, s28
	v_perm_b32 v242, v227, v226, s29
	v_perm_b32 v243, v229, v228, s29
	v_perm_b32 v244, v231, v230, s29
	v_perm_b32 v245, v233, v232, s29
	s_nop 0
	global_store_dwordx4 v110, v[242:245], s[6:7]
	ds_read_b32 v226, v118
	ds_read_b32 v227, v118 offset:512
	ds_read_b32 v228, v118 offset:1024
	ds_read_b32 v229, v118 offset:1536
	ds_read_b32 v230, v118 offset:2048
	ds_read_b32 v231, v118 offset:2560
	ds_read_b32 v232, v118 offset:3072
	ds_read_b32 v233, v118 offset:3584
	s_waitcnt lgkmcnt(0)
	v_bfe_u32 v120, v226, 16, 1
	v_bfe_u32 v121, v227, 16, 1
	v_bfe_u32 v122, v228, 16, 1
	v_bfe_u32 v123, v229, 16, 1
	v_bfe_u32 v124, v230, 16, 1
	v_bfe_u32 v125, v231, 16, 1
	v_bfe_u32 v126, v232, 16, 1
	v_bfe_u32 v127, v233, 16, 1
	v_add3_u32 v226, v226, v120, s28
	v_add3_u32 v227, v227, v121, s28
	v_add3_u32 v228, v228, v122, s28
	v_add3_u32 v229, v229, v123, s28
	v_add3_u32 v230, v230, v124, s28
	v_add3_u32 v231, v231, v125, s28
	v_add3_u32 v232, v232, v126, s28
	v_add3_u32 v233, v233, v127, s28
	v_perm_b32 v242, v227, v226, s29
	v_perm_b32 v243, v229, v228, s29
	v_perm_b32 v244, v231, v230, s29
	v_perm_b32 v245, v233, v232, s29
	s_nop 0
	global_store_dwordx4 v111, v[242:245], s[6:7]
	s_add_i32 s26, s23, 24
	s_add_i32 s27, s23, 40
	s_waitcnt vmcnt(16)
	v_mul_f32_e32 v176, v218, v176
	v_mul_f32_e32 v177, v218, v177
	v_mul_f32_e32 v178, v218, v178
	v_mul_f32_e32 v179, v218, v179
	ds_write_b128 v210, v[176:179]
	v_mul_f32_e32 v180, v219, v180
	v_mul_f32_e32 v181, v219, v181
	v_mul_f32_e32 v182, v219, v182
	v_mul_f32_e32 v183, v219, v183
	ds_write_b128 v210, v[180:183] offset:1024
	v_mul_f32_e32 v184, v220, v184
	v_mul_f32_e32 v185, v220, v185
	v_mul_f32_e32 v186, v220, v186
	v_mul_f32_e32 v187, v220, v187
	ds_write_b128 v210, v[184:187] offset:2048
	v_mul_f32_e32 v188, v221, v188
	v_mul_f32_e32 v189, v221, v189
	v_mul_f32_e32 v190, v221, v190
	v_mul_f32_e32 v191, v221, v191
	ds_write_b128 v210, v[188:191] offset:3072
	v_mul_f32_e32 v192, v222, v192
	v_mul_f32_e32 v193, v222, v193
	v_mul_f32_e32 v194, v222, v194
	v_mul_f32_e32 v195, v222, v195
	ds_write_b128 v210, v[192:195] offset:4096
	v_mul_f32_e32 v196, v223, v196
	v_mul_f32_e32 v197, v223, v197
	v_mul_f32_e32 v198, v223, v198
	v_mul_f32_e32 v199, v223, v199
	ds_write_b128 v210, v[196:199] offset:5120
	v_mul_f32_e32 v200, v224, v200
	v_mul_f32_e32 v201, v224, v201
	v_mul_f32_e32 v202, v224, v202
	v_mul_f32_e32 v203, v224, v203
	ds_write_b128 v210, v[200:203] offset:6144
	v_mul_f32_e32 v204, v225, v204
	v_mul_f32_e32 v205, v225, v205
	v_mul_f32_e32 v206, v225, v206
	v_mul_f32_e32 v207, v225, v207
	ds_write_b128 v210, v[204:207] offset:7168
	s_waitcnt lgkmcnt(0)
	s_barrier
; #define GAS __attribute__((address_space(1)))
; #define LAS __attribute__((address_space(3)))
; #define LDS_WAIT() asm volatile("s_waitcnt lgkmcnt(0)" ::: "memory")
; __device__ __forceinline__ unsigned pk2(float lo, float hi) { return f2bf(lo) | (f2bf(hi) << 16); }
; __device__ __forceinline__ int nat_dim(int p) { return (p >> 1) + 64 * (p & 1); }
; __device__ __forceinline__ int src_col_in(int c) {
;     if (c < 5120) { const int blk = c >> 7, p = c & 127; const bool rope = blk < 16 || ((((blk - 16) >> 2) & 1) == 0); const int d = rope ? (p >> 1) + 64 * (p & 1) : p; return blk * 128 + d; }
; template <int MAP, bool KS, bool KPERM = false>
; __device__ __forceinline__ void p0_transpose_item(const float* W, int K, int Nsrc, int nblk, bf16* WT, const float* ksA, const float* ksB, int ksplit, LAS float* scr, int item, int lane) {
;     const int kb = item / nblk, nb = item % nblk, k0 = 64 * kb, n0 = 32 * nb;
;     const int nr = n0 + (lane & 31); const int sc = MAP == 1 ? src_col_in(nr) : (MAP == 2 ? nat_dim(nr) : nr);
;     float v[32];
; #pragma unroll
;     for (int i = 0; i < 32; ++i) { const int k = k0 + 2 * i + (lane >> 5); const int ksrc = KPERM ? ((k & ~127) + nat_dim(k & 127)) : k;
;         v[i] = sc >= 0 ? W[(size_t)ksrc * Nsrc + sc] : 0.f; }
; #pragma unroll
;     for (int i = 0; i < 32; ++i) { const int kk = 2 * i + (lane >> 5); const int k = k0 + kk;
;         if (KS) v[i] *= (k < ksplit ? ksA[k] : ksB[k - ksplit]);
;         scr[kk * 33 + (lane & 31)] = v[i]; }
;     LDS_WAIT(); asm volatile("" ::: "memory");
;     const int c = lane & 7;
; #pragma unroll
;     for (int j = 0; j < 4; ++j) { const int n = (lane >> 3) + 8 * j; const LAS float* s = scr + (8 * c) * 33 + n;
;         v4u o; o.x = pk2(s[0 * 33], s[1 * 33]); o.y = pk2(s[2 * 33], s[3 * 33]); o.z = pk2(s[4 * 33], s[5 * 33]); o.w = pk2(s[6 * 33], s[7 * 33]);
;         *(GAS v4u*)(WT + (size_t)(n0 + n) * K + k0 + 8 * c) = o; }
;     LDS_WAIT(); asm volatile("" ::: "memory");
	s_lshl_b32 s20, s27, 7
	s_cmp_lt_u32 s27, 40
	s_cselect_b32 s21, 0, 0x830
	s_cmp_lt_u32 s27, 72
	s_cselect_b32 s21, s21, 0xfffff030
	s_add_i32 s20, s20, s21
	s_lshl_b32 s20, s20, 2
	s_add_u32 s8, s16, s20
	s_addc_u32 s9, s17, 0
	global_load_dwordx4 v[176:179], v208, s[8:9]
	s_add_u32 s8, s8, 0x16280
	s_addc_u32 s9, s9, 0
	global_load_dwordx4 v[180:183], v208, s[8:9]
	s_add_u32 s8, s8, 0x16280
	s_addc_u32 s9, s9, 0
	global_load_dwordx4 v[184:187], v208, s[8:9]
	s_add_u32 s8, s8, 0x16280
	s_addc_u32 s9, s9, 0
	global_load_dwordx4 v[188:191], v208, s[8:9]
	s_add_u32 s8, s8, 0x16280
	s_addc_u32 s9, s9, 0
	global_load_dwordx4 v[192:195], v208, s[8:9]
	s_add_u32 s8, s8, 0x16280
	s_addc_u32 s9, s9, 0
	global_load_dwordx4 v[196:199], v208, s[8:9]
	s_add_u32 s8, s8, 0x16280
	s_addc_u32 s9, s9, 0
	global_load_dwordx4 v[200:203], v208, s[8:9]
	s_add_u32 s8, s8, 0x16280
	s_addc_u32 s9, s9, 0
	global_load_dwordx4 v[204:207], v208, s[8:9]
	s_mul_i32 s20, s26, 0x100000
	s_add_u32 s6, s18, s20
	s_addc_u32 s7, s19, 0
	s_cmp_lt_u32 s26, 16
	s_cselect_b32 s20, 1, 0
	s_sub_i32 s21, s26, 16
	s_bitcmp0_b32 s21, 2
	s_cselect_b32 s21, 1, 0
	s_cmp_lt_u32 s26, 40
	s_cselect_b32 s21, s21, 0
	s_or_b32 s20, s20, s21
	s_cmp_lg_u32 s20, 0
	s_cselect_b64 s[20:21], -1, 0
	v_cndmask_b32_e64 v108, v100, v104, s[20:21]
	v_cndmask_b32_e64 v109, v101, v105, s[20:21]
	v_cndmask_b32_e64 v110, v102, v106, s[20:21]
	v_cndmask_b32_e64 v111, v103, v107, s[20:21]
	ds_read_b32 v226, v113
	ds_read_b32 v227, v113 offset:512
	ds_read_b32 v228, v113 offset:1024
	ds_read_b32 v229, v113 offset:1536
	ds_read_b32 v230, v113 offset:2048
	ds_read_b32 v231, v113 offset:2560
	ds_read_b32 v232, v113 offset:3072
	ds_read_b32 v233, v113 offset:3584
	s_waitcnt lgkmcnt(0)
	v_bfe_u32 v120, v226, 16, 1
	v_bfe_u32 v121, v227, 16, 1
	v_bfe_u32 v122, v228, 16, 1
	v_bfe_u32 v123, v229, 16, 1
	v_bfe_u32 v124, v230, 16, 1
	v_bfe_u32 v125, v231, 16, 1
	v_bfe_u32 v126, v232, 16, 1
	v_bfe_u32 v127, v233, 16, 1
	v_add3_u32 v226, v226, v120, s28
	v_add3_u32 v227, v227, v121, s28
	v_add3_u32 v228, v228, v122, s28
	v_add3_u32 v229, v229, v123, s28
	v_add3_u32 v230, v230, v124, s28
	v_add3_u32 v231, v231, v125, s28
	v_add3_u32 v232, v232, v126, s28
	v_add3_u32 v233, v233, v127, s28
	v_perm_b32 v242, v227, v226, s29
	v_perm_b32 v243, v229, v228, s29
	v_perm_b32 v244, v231, v230, s29
	v_perm_b32 v245, v233, v232, s29
	s_nop 0
	global_store_dwordx4 v108, v[242:245], s[6:7]
	ds_read_b32 v226, v115
	ds_read_b32 v227, v115 offset:512
	ds_read_b32 v228, v115 offset:1024
	ds_read_b32 v229, v115 offset:1536
	ds_read_b32 v230, v115 offset:2048
	ds_read_b32 v231, v115 offset:2560
	ds_read_b32 v232, v115 offset:3072
	ds_read_b32 v233, v115 offset:3584
	s_waitcnt lgkmcnt(0)
	v_bfe_u32 v120, v226, 16, 1
	v_bfe_u32 v121, v227, 16, 1
	v_bfe_u32 v122, v228, 16, 1
	v_bfe_u32 v123, v229, 16, 1
	v_bfe_u32 v124, v230, 16, 1
	v_bfe_u32 v125, v231, 16, 1
	v_bfe_u32 v126, v232, 16, 1
	v_bfe_u32 v127, v233, 16, 1
	v_add3_u32 v226, v226, v120, s28
	v_add3_u32 v227, v227, v121, s28
	v_add3_u32 v228, v228, v122, s28
	v_add3_u32 v229, v229, v123, s28
	v_add3_u32 v230, v230, v124, s28
	v_add3_u32 v231, v231, v125, s28
	v_add3_u32 v232, v232, v126, s28
	v_add3_u32 v233, v233, v127, s28
	v_perm_b32 v242, v227, v226, s29
	v_perm_b32 v243, v229, v228, s29
	v_perm_b32 v244, v231, v230, s29
	v_perm_b32 v245, v233, v232, s29
	s_nop 0
	global_store_dwordx4 v109, v[242:245], s[6:7]
	ds_read_b32 v226, v117
	ds_read_b32 v227, v117 offset:512
	ds_read_b32 v228, v117 offset:1024
	ds_read_b32 v229, v117 offset:1536
	ds_read_b32 v230, v117 offset:2048
	ds_read_b32 v231, v117 offset:2560
	ds_read_b32 v232, v117 offset:3072
	ds_read_b32 v233, v117 offset:3584
	s_waitcnt lgkmcnt(0)
	v_bfe_u32 v120, v226, 16, 1
	v_bfe_u32 v121, v227, 16, 1
	v_bfe_u32 v122, v228, 16, 1
	v_bfe_u32 v123, v229, 16, 1
	v_bfe_u32 v124, v230, 16, 1
	v_bfe_u32 v125, v231, 16, 1
	v_bfe_u32 v126, v232, 16, 1
	v_bfe_u32 v127, v233, 16, 1
	v_add3_u32 v226, v226, v120, s28
	v_add3_u32 v227, v227, v121, s28
	v_add3_u32 v228, v228, v122, s28
	v_add3_u32 v229, v229, v123, s28
	v_add3_u32 v230, v230, v124, s28
	v_add3_u32 v231, v231, v125, s28
	v_add3_u32 v232, v232, v126, s28
	v_add3_u32 v233, v233, v127, s28
	v_perm_b32 v242, v227, v226, s29
	v_perm_b32 v243, v229, v228, s29
	v_perm_b32 v244, v231, v230, s29
	v_perm_b32 v245, v233, v232, s29
	s_nop 0
	global_store_dwordx4 v110, v[242:245], s[6:7]
	ds_read_b32 v226, v119
	ds_read_b32 v227, v119 offset:512
	ds_read_b32 v228, v119 offset:1024
	ds_read_b32 v229, v119 offset:1536
	ds_read_b32 v230, v119 offset:2048
	ds_read_b32 v231, v119 offset:2560
	ds_read_b32 v232, v119 offset:3072
	ds_read_b32 v233, v119 offset:3584
	s_waitcnt lgkmcnt(0)
	v_bfe_u32 v120, v226, 16, 1
	v_bfe_u32 v121, v227, 16, 1
	v_bfe_u32 v122, v228, 16, 1
	v_bfe_u32 v123, v229, 16, 1
	v_bfe_u32 v124, v230, 16, 1
	v_bfe_u32 v125, v231, 16, 1
	v_bfe_u32 v126, v232, 16, 1
	v_bfe_u32 v127, v233, 16, 1
	v_add3_u32 v226, v226, v120, s28
	v_add3_u32 v227, v227, v121, s28
	v_add3_u32 v228, v228, v122, s28
	v_add3_u32 v229, v229, v123, s28
	v_add3_u32 v230, v230, v124, s28
	v_add3_u32 v231, v231, v125, s28
	v_add3_u32 v232, v232, v126, s28
	v_add3_u32 v233, v233, v127, s28
	v_perm_b32 v242, v227, v226, s29
	v_perm_b32 v243, v229, v228, s29
	v_perm_b32 v244, v231, v230, s29
	v_perm_b32 v245, v233, v232, s29
	s_nop 0
	global_store_dwordx4 v111, v[242:245], s[6:7]
	s_add_i32 s26, s23, 32
	s_add_i32 s27, s23, 48
	s_waitcnt vmcnt(16)
	v_mul_f32_e32 v144, v218, v144
	v_mul_f32_e32 v145, v218, v145
	v_mul_f32_e32 v146, v218, v146
	v_mul_f32_e32 v147, v218, v147
	ds_write_b128 v209, v[144:147]
	v_mul_f32_e32 v148, v219, v148
	v_mul_f32_e32 v149, v219, v149
	v_mul_f32_e32 v150, v219, v150
	v_mul_f32_e32 v151, v219, v151
	ds_write_b128 v209, v[148:151] offset:1024
	v_mul_f32_e32 v152, v220, v152
	v_mul_f32_e32 v153, v220, v153
	v_mul_f32_e32 v154, v220, v154
	v_mul_f32_e32 v155, v220, v155
	ds_write_b128 v209, v[152:155] offset:2048
	v_mul_f32_e32 v156, v221, v156
	v_mul_f32_e32 v157, v221, v157
	v_mul_f32_e32 v158, v221, v158
	v_mul_f32_e32 v159, v221, v159
	ds_write_b128 v209, v[156:159] offset:3072
	v_mul_f32_e32 v160, v222, v160
	v_mul_f32_e32 v161, v222, v161
	v_mul_f32_e32 v162, v222, v162
	v_mul_f32_e32 v163, v222, v163
	ds_write_b128 v209, v[160:163] offset:4096
	v_mul_f32_e32 v164, v223, v164
	v_mul_f32_e32 v165, v223, v165
	v_mul_f32_e32 v166, v223, v166
	v_mul_f32_e32 v167, v223, v167
	ds_write_b128 v209, v[164:167] offset:5120
	v_mul_f32_e32 v168, v224, v168
	v_mul_f32_e32 v169, v224, v169
	v_mul_f32_e32 v170, v224, v170
	v_mul_f32_e32 v171, v224, v171
	ds_write_b128 v209, v[168:171] offset:6144
	v_mul_f32_e32 v172, v225, v172
	v_mul_f32_e32 v173, v225, v173
	v_mul_f32_e32 v174, v225, v174
	v_mul_f32_e32 v175, v225, v175
	ds_write_b128 v209, v[172:175] offset:7168
	s_waitcnt lgkmcnt(0)
	s_barrier
; #define GAS __attribute__((address_space(1)))
; #define LAS __attribute__((address_space(3)))
; #define LDS_WAIT() asm volatile("s_waitcnt lgkmcnt(0)" ::: "memory")
; __device__ __forceinline__ unsigned pk2(float lo, float hi) { return f2bf(lo) | (f2bf(hi) << 16); }
; __device__ __forceinline__ int nat_dim(int p) { return (p >> 1) + 64 * (p & 1); }
; __device__ __forceinline__ int src_col_in(int c) {
;     if (c < 5120) { const int blk = c >> 7, p = c & 127; const bool rope = blk < 16 || ((((blk - 16) >> 2) & 1) == 0); const int d = rope ? (p >> 1) + 64 * (p & 1) : p; return blk * 128 + d; }
; template <int MAP, bool KS, bool KPERM = false>
; __device__ __forceinline__ void p0_transpose_item(const float* W, int K, int Nsrc, int nblk, bf16* WT, const float* ksA, const float* ksB, int ksplit, LAS float* scr, int item, int lane) {
;     const int kb = item / nblk, nb = item % nblk, k0 = 64 * kb, n0 = 32 * nb;
;     const int nr = n0 + (lane & 31); const int sc = MAP == 1 ? src_col_in(nr) : (MAP == 2 ? nat_dim(nr) : nr);
;     float v[32];
; #pragma unroll
;     for (int i = 0; i < 32; ++i) { const int k = k0 + 2 * i + (lane >> 5); const int ksrc = KPERM ? ((k & ~127) + nat_dim(k & 127)) : k;
;         v[i] = sc >= 0 ? W[(size_t)ksrc * Nsrc + sc] : 0.f; }
; #pragma unroll
;     for (int i = 0; i < 32; ++i) { const int kk = 2 * i + (lane >> 5); const int k = k0 + kk;
;         if (KS) v[i] *= (k < ksplit ? ksA[k] : ksB[k - ksplit]);
;         scr[kk * 33 + (lane & 31)] = v[i]; }
;     LDS_WAIT(); asm volatile("" ::: "memory");
;     const int c = lane & 7;
; #pragma unroll
;     for (int j = 0; j < 4; ++j) { const int n = (lane >> 3) + 8 * j; const LAS float* s = scr + (8 * c) * 33 + n;
;         v4u o; o.x = pk2(s[0 * 33], s[1 * 33]); o.y = pk2(s[2 * 33], s[3 * 33]); o.z = pk2(s[4 * 33], s[5 * 33]); o.w = pk2(s[6 * 33], s[7 * 33]);
;         *(GAS v4u*)(WT + (size_t)(n0 + n) * K + k0 + 8 * c) = o; }
;     LDS_WAIT(); asm volatile("" ::: "memory");
	s_lshl_b32 s20, s27, 7
	s_cmp_lt_u32 s27, 40
	s_cselect_b32 s21, 0, 0x830
	s_cmp_lt_u32 s27, 72
	s_cselect_b32 s21, s21, 0xfffff030
	s_add_i32 s20, s20, s21
	s_lshl_b32 s20, s20, 2
	s_add_u32 s8, s16, s20
	s_addc_u32 s9, s17, 0
	global_load_dwordx4 v[144:147], v208, s[8:9]
	s_add_u32 s8, s8, 0x16280
	s_addc_u32 s9, s9, 0
	global_load_dwordx4 v[148:151], v208, s[8:9]
	s_add_u32 s8, s8, 0x16280
	s_addc_u32 s9, s9, 0
	global_load_dwordx4 v[152:155], v208, s[8:9]
	s_add_u32 s8, s8, 0x16280
	s_addc_u32 s9, s9, 0
	global_load_dwordx4 v[156:159], v208, s[8:9]
	s_add_u32 s8, s8, 0x16280
	s_addc_u32 s9, s9, 0
	global_load_dwordx4 v[160:163], v208, s[8:9]
	s_add_u32 s8, s8, 0x16280
	s_addc_u32 s9, s9, 0
	global_load_dwordx4 v[164:167], v208, s[8:9]
	s_add_u32 s8, s8, 0x16280
	s_addc_u32 s9, s9, 0
	global_load_dwordx4 v[168:171], v208, s[8:9]
	s_add_u32 s8, s8, 0x16280
	s_addc_u32 s9, s9, 0
	global_load_dwordx4 v[172:175], v208, s[8:9]
	s_mul_i32 s20, s26, 0x100000
	s_add_u32 s6, s18, s20
	s_addc_u32 s7, s19, 0
	s_cmp_lt_u32 s26, 16
	s_cselect_b32 s20, 1, 0
	s_sub_i32 s21, s26, 16
	s_bitcmp0_b32 s21, 2
	s_cselect_b32 s21, 1, 0
	s_cmp_lt_u32 s26, 40
	s_cselect_b32 s21, s21, 0
	s_or_b32 s20, s20, s21
	s_cmp_lg_u32 s20, 0
	s_cselect_b64 s[20:21], -1, 0
	v_cndmask_b32_e64 v108, v100, v104, s[20:21]
	v_cndmask_b32_e64 v109, v101, v105, s[20:21]
	v_cndmask_b32_e64 v110, v102, v106, s[20:21]
	v_cndmask_b32_e64 v111, v103, v107, s[20:21]
	ds_read_b32 v226, v112
	ds_read_b32 v227, v112 offset:512
	ds_read_b32 v228, v112 offset:1024
	ds_read_b32 v229, v112 offset:1536
	ds_read_b32 v230, v112 offset:2048
	ds_read_b32 v231, v112 offset:2560
	ds_read_b32 v232, v112 offset:3072
	ds_read_b32 v233, v112 offset:3584
	s_waitcnt lgkmcnt(0)
	v_bfe_u32 v120, v226, 16, 1
	v_bfe_u32 v121, v227, 16, 1
	v_bfe_u32 v122, v228, 16, 1
	v_bfe_u32 v123, v229, 16, 1
	v_bfe_u32 v124, v230, 16, 1
	v_bfe_u32 v125, v231, 16, 1
	v_bfe_u32 v126, v232, 16, 1
	v_bfe_u32 v127, v233, 16, 1
	v_add3_u32 v226, v226, v120, s28
	v_add3_u32 v227, v227, v121, s28
	v_add3_u32 v228, v228, v122, s28
	v_add3_u32 v229, v229, v123, s28
	v_add3_u32 v230, v230, v124, s28
	v_add3_u32 v231, v231, v125, s28
	v_add3_u32 v232, v232, v126, s28
	v_add3_u32 v233, v233, v127, s28
	v_perm_b32 v242, v227, v226, s29
	v_perm_b32 v243, v229, v228, s29
	v_perm_b32 v244, v231, v230, s29
	v_perm_b32 v245, v233, v232, s29
	s_nop 0
	global_store_dwordx4 v108, v[242:245], s[6:7]
	ds_read_b32 v226, v114
	ds_read_b32 v227, v114 offset:512
	ds_read_b32 v228, v114 offset:1024
	ds_read_b32 v229, v114 offset:1536
	ds_read_b32 v230, v114 offset:2048
	ds_read_b32 v231, v114 offset:2560
	ds_read_b32 v232, v114 offset:3072
	ds_read_b32 v233, v114 offset:3584
	s_waitcnt lgkmcnt(0)
	v_bfe_u32 v120, v226, 16, 1
	v_bfe_u32 v121, v227, 16, 1
	v_bfe_u32 v122, v228, 16, 1
	v_bfe_u32 v123, v229, 16, 1
	v_bfe_u32 v124, v230, 16, 1
	v_bfe_u32 v125, v231, 16, 1
	v_bfe_u32 v126, v232, 16, 1
	v_bfe_u32 v127, v233, 16, 1
	v_add3_u32 v226, v226, v120, s28
	v_add3_u32 v227, v227, v121, s28
	v_add3_u32 v228, v228, v122, s28
	v_add3_u32 v229, v229, v123, s28
	v_add3_u32 v230, v230, v124, s28
	v_add3_u32 v231, v231, v125, s28
	v_add3_u32 v232, v232, v126, s28
	v_add3_u32 v233, v233, v127, s28
	v_perm_b32 v242, v227, v226, s29
	v_perm_b32 v243, v229, v228, s29
	v_perm_b32 v244, v231, v230, s29
	v_perm_b32 v245, v233, v232, s29
	s_nop 0
	global_store_dwordx4 v109, v[242:245], s[6:7]
	ds_read_b32 v226, v116
	ds_read_b32 v227, v116 offset:512
	ds_read_b32 v228, v116 offset:1024
	ds_read_b32 v229, v116 offset:1536
	ds_read_b32 v230, v116 offset:2048
	ds_read_b32 v231, v116 offset:2560
	ds_read_b32 v232, v116 offset:3072
	ds_read_b32 v233, v116 offset:3584
	s_waitcnt lgkmcnt(0)
	v_bfe_u32 v120, v226, 16, 1
	v_bfe_u32 v121, v227, 16, 1
	v_bfe_u32 v122, v228, 16, 1
	v_bfe_u32 v123, v229, 16, 1
	v_bfe_u32 v124, v230, 16, 1
	v_bfe_u32 v125, v231, 16, 1
	v_bfe_u32 v126, v232, 16, 1
	v_bfe_u32 v127, v233, 16, 1
	v_add3_u32 v226, v226, v120, s28
	v_add3_u32 v227, v227, v121, s28
	v_add3_u32 v228, v228, v122, s28
	v_add3_u32 v229, v229, v123, s28
	v_add3_u32 v230, v230, v124, s28
	v_add3_u32 v231, v231, v125, s28
	v_add3_u32 v232, v232, v126, s28
	v_add3_u32 v233, v233, v127, s28
	v_perm_b32 v242, v227, v226, s29
	v_perm_b32 v243, v229, v228, s29
	v_perm_b32 v244, v231, v230, s29
	v_perm_b32 v245, v233, v232, s29
	s_nop 0
	global_store_dwordx4 v110, v[242:245], s[6:7]
	ds_read_b32 v226, v118
	ds_read_b32 v227, v118 offset:512
	ds_read_b32 v228, v118 offset:1024
	ds_read_b32 v229, v118 offset:1536
	ds_read_b32 v230, v118 offset:2048
	ds_read_b32 v231, v118 offset:2560
	ds_read_b32 v232, v118 offset:3072
	ds_read_b32 v233, v118 offset:3584
	s_waitcnt lgkmcnt(0)
	v_bfe_u32 v120, v226, 16, 1
	v_bfe_u32 v121, v227, 16, 1
	v_bfe_u32 v122, v228, 16, 1
	v_bfe_u32 v123, v229, 16, 1
	v_bfe_u32 v124, v230, 16, 1
	v_bfe_u32 v125, v231, 16, 1
	v_bfe_u32 v126, v232, 16, 1
	v_bfe_u32 v127, v233, 16, 1
	v_add3_u32 v226, v226, v120, s28
	v_add3_u32 v227, v227, v121, s28
	v_add3_u32 v228, v228, v122, s28
	v_add3_u32 v229, v229, v123, s28
	v_add3_u32 v230, v230, v124, s28
	v_add3_u32 v231, v231, v125, s28
	v_add3_u32 v232, v232, v126, s28
	v_add3_u32 v233, v233, v127, s28
	v_perm_b32 v242, v227, v226, s29
	v_perm_b32 v243, v229, v228, s29
	v_perm_b32 v244, v231, v230, s29
	v_perm_b32 v245, v233, v232, s29
	s_nop 0
	global_store_dwordx4 v111, v[242:245], s[6:7]
	s_add_i32 s26, s23, 40
	s_add_i32 s27, s23, 56
	s_waitcnt vmcnt(16)
	v_mul_f32_e32 v176, v218, v176
	v_mul_f32_e32 v177, v218, v177
	v_mul_f32_e32 v178, v218, v178
	v_mul_f32_e32 v179, v218, v179
	ds_write_b128 v210, v[176:179]
	v_mul_f32_e32 v180, v219, v180
	v_mul_f32_e32 v181, v219, v181
	v_mul_f32_e32 v182, v219, v182
	v_mul_f32_e32 v183, v219, v183
	ds_write_b128 v210, v[180:183] offset:1024
	v_mul_f32_e32 v184, v220, v184
	v_mul_f32_e32 v185, v220, v185
	v_mul_f32_e32 v186, v220, v186
	v_mul_f32_e32 v187, v220, v187
	ds_write_b128 v210, v[184:187] offset:2048
	v_mul_f32_e32 v188, v221, v188
	v_mul_f32_e32 v189, v221, v189
	v_mul_f32_e32 v190, v221, v190
	v_mul_f32_e32 v191, v221, v191
	ds_write_b128 v210, v[188:191] offset:3072
	v_mul_f32_e32 v192, v222, v192
	v_mul_f32_e32 v193, v222, v193
	v_mul_f32_e32 v194, v222, v194
	v_mul_f32_e32 v195, v222, v195
	ds_write_b128 v210, v[192:195] offset:4096
	v_mul_f32_e32 v196, v223, v196
	v_mul_f32_e32 v197, v223, v197
	v_mul_f32_e32 v198, v223, v198
	v_mul_f32_e32 v199, v223, v199
	ds_write_b128 v210, v[196:199] offset:5120
	v_mul_f32_e32 v200, v224, v200
	v_mul_f32_e32 v201, v224, v201
	v_mul_f32_e32 v202, v224, v202
	v_mul_f32_e32 v203, v224, v203
	ds_write_b128 v210, v[200:203] offset:6144
	v_mul_f32_e32 v204, v225, v204
	v_mul_f32_e32 v205, v225, v205
	v_mul_f32_e32 v206, v225, v206
	v_mul_f32_e32 v207, v225, v207
	ds_write_b128 v210, v[204:207] offset:7168
	s_waitcnt lgkmcnt(0)
	s_barrier
; #define GAS __attribute__((address_space(1)))
; #define LAS __attribute__((address_space(3)))
; #define LDS_WAIT() asm volatile("s_waitcnt lgkmcnt(0)" ::: "memory")
; __device__ __forceinline__ unsigned pk2(float lo, float hi) { return f2bf(lo) | (f2bf(hi) << 16); }
; __device__ __forceinline__ int nat_dim(int p) { return (p >> 1) + 64 * (p & 1); }
; __device__ __forceinline__ int src_col_in(int c) {
;     if (c < 5120) { const int blk = c >> 7, p = c & 127; const bool rope = blk < 16 || ((((blk - 16) >> 2) & 1) == 0); const int d = rope ? (p >> 1) + 64 * (p & 1) : p; return blk * 128 + d; }
; template <int MAP, bool KS, bool KPERM = false>
; __device__ __forceinline__ void p0_transpose_item(const float* W, int K, int Nsrc, int nblk, bf16* WT, const float* ksA, const float* ksB, int ksplit, LAS float* scr, int item, int lane) {
;     const int kb = item / nblk, nb = item % nblk, k0 = 64 * kb, n0 = 32 * nb;
;     const int nr = n0 + (lane & 31); const int sc = MAP == 1 ? src_col_in(nr) : (MAP == 2 ? nat_dim(nr) : nr);
;     float v[32];
; #pragma unroll
;     for (int i = 0; i < 32; ++i) { const int k = k0 + 2 * i + (lane >> 5); const int ksrc = KPERM ? ((k & ~127) + nat_dim(k & 127)) : k;
;         v[i] = sc >= 0 ? W[(size_t)ksrc * Nsrc + sc] : 0.f; }
; #pragma unroll
;     for (int i = 0; i < 32; ++i) { const int kk = 2 * i + (lane >> 5); const int k = k0 + kk;
;         if (KS) v[i] *= (k < ksplit ? ksA[k] : ksB[k - ksplit]);
;         scr[kk * 33 + (lane & 31)] = v[i]; }
;     LDS_WAIT(); asm volatile("" ::: "memory");
;     const int c = lane & 7;
; #pragma unroll
;     for (int j = 0; j < 4; ++j) { const int n = (lane >> 3) + 8 * j; const LAS float* s = scr + (8 * c) * 33 + n;
;         v4u o; o.x = pk2(s[0 * 33], s[1 * 33]); o.y = pk2(s[2 * 33], s[3 * 33]); o.z = pk2(s[4 * 33], s[5 * 33]); o.w = pk2(s[6 * 33], s[7 * 33]);
;         *(GAS v4u*)(WT + (size_t)(n0 + n) * K + k0 + 8 * c) = o; }
;     LDS_WAIT(); asm volatile("" ::: "memory");
	s_lshl_b32 s20, s27, 7
	s_cmp_lt_u32 s27, 40
	s_cselect_b32 s21, 0, 0x830
	s_cmp_lt_u32 s27, 72
	s_cselect_b32 s21, s21, 0xfffff030
	s_add_i32 s20, s20, s21
	s_lshl_b32 s20, s20, 2
	s_add_u32 s8, s16, s20
	s_addc_u32 s9, s17, 0
	global_load_dwordx4 v[176:179], v208, s[8:9]
	s_add_u32 s8, s8, 0x16280
	s_addc_u32 s9, s9, 0
	global_load_dwordx4 v[180:183], v208, s[8:9]
	s_add_u32 s8, s8, 0x16280
	s_addc_u32 s9, s9, 0
	global_load_dwordx4 v[184:187], v208, s[8:9]
	s_add_u32 s8, s8, 0x16280
	s_addc_u32 s9, s9, 0
	global_load_dwordx4 v[188:191], v208, s[8:9]
	s_add_u32 s8, s8, 0x16280
	s_addc_u32 s9, s9, 0
	global_load_dwordx4 v[192:195], v208, s[8:9]
	s_add_u32 s8, s8, 0x16280
	s_addc_u32 s9, s9, 0
	global_load_dwordx4 v[196:199], v208, s[8:9]
	s_add_u32 s8, s8, 0x16280
	s_addc_u32 s9, s9, 0
	global_load_dwordx4 v[200:203], v208, s[8:9]
	s_add_u32 s8, s8, 0x16280
	s_addc_u32 s9, s9, 0
	global_load_dwordx4 v[204:207], v208, s[8:9]
	s_mul_i32 s20, s26, 0x100000
	s_add_u32 s6, s18, s20
	s_addc_u32 s7, s19, 0
	s_cmp_lt_u32 s26, 16
	s_cselect_b32 s20, 1, 0
	s_sub_i32 s21, s26, 16
	s_bitcmp0_b32 s21, 2
	s_cselect_b32 s21, 1, 0
	s_cmp_lt_u32 s26, 40
	s_cselect_b32 s21, s21, 0
	s_or_b32 s20, s20, s21
	s_cmp_lg_u32 s20, 0
	s_cselect_b64 s[20:21], -1, 0
	v_cndmask_b32_e64 v108, v100, v104, s[20:21]
	v_cndmask_b32_e64 v109, v101, v105, s[20:21]
	v_cndmask_b32_e64 v110, v102, v106, s[20:21]
	v_cndmask_b32_e64 v111, v103, v107, s[20:21]
	ds_read_b32 v226, v113
	ds_read_b32 v227, v113 offset:512
	ds_read_b32 v228, v113 offset:1024
	ds_read_b32 v229, v113 offset:1536
	ds_read_b32 v230, v113 offset:2048
	ds_read_b32 v231, v113 offset:2560
	ds_read_b32 v232, v113 offset:3072
	ds_read_b32 v233, v113 offset:3584
	s_waitcnt lgkmcnt(0)
	v_bfe_u32 v120, v226, 16, 1
	v_bfe_u32 v121, v227, 16, 1
	v_bfe_u32 v122, v228, 16, 1
	v_bfe_u32 v123, v229, 16, 1
	v_bfe_u32 v124, v230, 16, 1
	v_bfe_u32 v125, v231, 16, 1
	v_bfe_u32 v126, v232, 16, 1
	v_bfe_u32 v127, v233, 16, 1
	v_add3_u32 v226, v226, v120, s28
	v_add3_u32 v227, v227, v121, s28
	v_add3_u32 v228, v228, v122, s28
	v_add3_u32 v229, v229, v123, s28
	v_add3_u32 v230, v230, v124, s28
	v_add3_u32 v231, v231, v125, s28
	v_add3_u32 v232, v232, v126, s28
	v_add3_u32 v233, v233, v127, s28
	v_perm_b32 v242, v227, v226, s29
	v_perm_b32 v243, v229, v228, s29
	v_perm_b32 v244, v231, v230, s29
	v_perm_b32 v245, v233, v232, s29
	s_nop 0
	global_store_dwordx4 v108, v[242:245], s[6:7]
	ds_read_b32 v226, v115
	ds_read_b32 v227, v115 offset:512
	ds_read_b32 v228, v115 offset:1024
	ds_read_b32 v229, v115 offset:1536
	ds_read_b32 v230, v115 offset:2048
	ds_read_b32 v231, v115 offset:2560
	ds_read_b32 v232, v115 offset:3072
	ds_read_b32 v233, v115 offset:3584
	s_waitcnt lgkmcnt(0)
	v_bfe_u32 v120, v226, 16, 1
	v_bfe_u32 v121, v227, 16, 1
	v_bfe_u32 v122, v228, 16, 1
	v_bfe_u32 v123, v229, 16, 1
	v_bfe_u32 v124, v230, 16, 1
	v_bfe_u32 v125, v231, 16, 1
	v_bfe_u32 v126, v232, 16, 1
	v_bfe_u32 v127, v233, 16, 1
	v_add3_u32 v226, v226, v120, s28
	v_add3_u32 v227, v227, v121, s28
	v_add3_u32 v228, v228, v122, s28
	v_add3_u32 v229, v229, v123, s28
	v_add3_u32 v230, v230, v124, s28
	v_add3_u32 v231, v231, v125, s28
	v_add3_u32 v232, v232, v126, s28
	v_add3_u32 v233, v233, v127, s28
	v_perm_b32 v242, v227, v226, s29
	v_perm_b32 v243, v229, v228, s29
	v_perm_b32 v244, v231, v230, s29
	v_perm_b32 v245, v233, v232, s29
	s_nop 0
	global_store_dwordx4 v109, v[242:245], s[6:7]
	ds_read_b32 v226, v117
	ds_read_b32 v227, v117 offset:512
	ds_read_b32 v228, v117 offset:1024
	ds_read_b32 v229, v117 offset:1536
	ds_read_b32 v230, v117 offset:2048
	ds_read_b32 v231, v117 offset:2560
	ds_read_b32 v232, v117 offset:3072
	ds_read_b32 v233, v117 offset:3584
	s_waitcnt lgkmcnt(0)
	v_bfe_u32 v120, v226, 16, 1
	v_bfe_u32 v121, v227, 16, 1
	v_bfe_u32 v122, v228, 16, 1
	v_bfe_u32 v123, v229, 16, 1
	v_bfe_u32 v124, v230, 16, 1
	v_bfe_u32 v125, v231, 16, 1
	v_bfe_u32 v126, v232, 16, 1
	v_bfe_u32 v127, v233, 16, 1
	v_add3_u32 v226, v226, v120, s28
	v_add3_u32 v227, v227, v121, s28
	v_add3_u32 v228, v228, v122, s28
	v_add3_u32 v229, v229, v123, s28
	v_add3_u32 v230, v230, v124, s28
	v_add3_u32 v231, v231, v125, s28
	v_add3_u32 v232, v232, v126, s28
	v_add3_u32 v233, v233, v127, s28
	v_perm_b32 v242, v227, v226, s29
	v_perm_b32 v243, v229, v228, s29
	v_perm_b32 v244, v231, v230, s29
	v_perm_b32 v245, v233, v232, s29
	s_nop 0
	global_store_dwordx4 v110, v[242:245], s[6:7]
	ds_read_b32 v226, v119
	ds_read_b32 v227, v119 offset:512
	ds_read_b32 v228, v119 offset:1024
	ds_read_b32 v229, v119 offset:1536
	ds_read_b32 v230, v119 offset:2048
	ds_read_b32 v231, v119 offset:2560
	ds_read_b32 v232, v119 offset:3072
	ds_read_b32 v233, v119 offset:3584
	s_waitcnt lgkmcnt(0)
	v_bfe_u32 v120, v226, 16, 1
	v_bfe_u32 v121, v227, 16, 1
	v_bfe_u32 v122, v228, 16, 1
	v_bfe_u32 v123, v229, 16, 1
	v_bfe_u32 v124, v230, 16, 1
	v_bfe_u32 v125, v231, 16, 1
	v_bfe_u32 v126, v232, 16, 1
	v_bfe_u32 v127, v233, 16, 1
	v_add3_u32 v226, v226, v120, s28
	v_add3_u32 v227, v227, v121, s28
	v_add3_u32 v228, v228, v122, s28
	v_add3_u32 v229, v229, v123, s28
	v_add3_u32 v230, v230, v124, s28
	v_add3_u32 v231, v231, v125, s28
	v_add3_u32 v232, v232, v126, s28
	v_add3_u32 v233, v233, v127, s28
	v_perm_b32 v242, v227, v226, s29
	v_perm_b32 v243, v229, v228, s29
	v_perm_b32 v244, v231, v230, s29
	v_perm_b32 v245, v233, v232, s29
	s_nop 0
	global_store_dwordx4 v111, v[242:245], s[6:7]
	s_add_i32 s26, s23, 48
	s_add_i32 s27, s23, 64
	s_waitcnt vmcnt(16)
	v_mul_f32_e32 v144, v218, v144
	v_mul_f32_e32 v145, v218, v145
	v_mul_f32_e32 v146, v218, v146
	v_mul_f32_e32 v147, v218, v147
	ds_write_b128 v209, v[144:147]
	v_mul_f32_e32 v148, v219, v148
	v_mul_f32_e32 v149, v219, v149
	v_mul_f32_e32 v150, v219, v150
	v_mul_f32_e32 v151, v219, v151
	ds_write_b128 v209, v[148:151] offset:1024
	v_mul_f32_e32 v152, v220, v152
	v_mul_f32_e32 v153, v220, v153
	v_mul_f32_e32 v154, v220, v154
	v_mul_f32_e32 v155, v220, v155
	ds_write_b128 v209, v[152:155] offset:2048
	v_mul_f32_e32 v156, v221, v156
	v_mul_f32_e32 v157, v221, v157
	v_mul_f32_e32 v158, v221, v158
	v_mul_f32_e32 v159, v221, v159
	ds_write_b128 v209, v[156:159] offset:3072
	v_mul_f32_e32 v160, v222, v160
	v_mul_f32_e32 v161, v222, v161
	v_mul_f32_e32 v162, v222, v162
	v_mul_f32_e32 v163, v222, v163
	ds_write_b128 v209, v[160:163] offset:4096
	v_mul_f32_e32 v164, v223, v164
	v_mul_f32_e32 v165, v223, v165
	v_mul_f32_e32 v166, v223, v166
	v_mul_f32_e32 v167, v223, v167
	ds_write_b128 v209, v[164:167] offset:5120
	v_mul_f32_e32 v168, v224, v168
	v_mul_f32_e32 v169, v224, v169
	v_mul_f32_e32 v170, v224, v170
	v_mul_f32_e32 v171, v224, v171
	ds_write_b128 v209, v[168:171] offset:6144
	v_mul_f32_e32 v172, v225, v172
	v_mul_f32_e32 v173, v225, v173
	v_mul_f32_e32 v174, v225, v174
	v_mul_f32_e32 v175, v225, v175
	ds_write_b128 v209, v[172:175] offset:7168
	s_waitcnt lgkmcnt(0)
	s_barrier
; #define GAS __attribute__((address_space(1)))
; #define LAS __attribute__((address_space(3)))
; #define LDS_WAIT() asm volatile("s_waitcnt lgkmcnt(0)" ::: "memory")
; __device__ __forceinline__ unsigned pk2(float lo, float hi) { return f2bf(lo) | (f2bf(hi) << 16); }
; __device__ __forceinline__ int nat_dim(int p) { return (p >> 1) + 64 * (p & 1); }
; __device__ __forceinline__ int src_col_in(int c) {
;     if (c < 5120) { const int blk = c >> 7, p = c & 127; const bool rope = blk < 16 || ((((blk - 16) >> 2) & 1) == 0); const int d = rope ? (p >> 1) + 64 * (p & 1) : p; return blk * 128 + d; }
; template <int MAP, bool KS, bool KPERM = false>
; __device__ __forceinline__ void p0_transpose_item(const float* W, int K, int Nsrc, int nblk, bf16* WT, const float* ksA, const float* ksB, int ksplit, LAS float* scr, int item, int lane) {
;     const int kb = item / nblk, nb = item % nblk, k0 = 64 * kb, n0 = 32 * nb;
;     const int nr = n0 + (lane & 31); const int sc = MAP == 1 ? src_col_in(nr) : (MAP == 2 ? nat_dim(nr) : nr);
;     float v[32];
; #pragma unroll
;     for (int i = 0; i < 32; ++i) { const int k = k0 + 2 * i + (lane >> 5); const int ksrc = KPERM ? ((k & ~127) + nat_dim(k & 127)) : k;
;         v[i] = sc >= 0 ? W[(size_t)ksrc * Nsrc + sc] : 0.f; }
; #pragma unroll
;     for (int i = 0; i < 32; ++i) { const int kk = 2 * i + (lane >> 5); const int k = k0 + kk;
;         if (KS) v[i] *= (k < ksplit ? ksA[k] : ksB[k - ksplit]);
;         scr[kk * 33 + (lane & 31)] = v[i]; }
;     LDS_WAIT(); asm volatile("" ::: "memory");
;     const int c = lane & 7;
; #pragma unroll
;     for (int j = 0; j < 4; ++j) { const int n = (lane >> 3) + 8 * j; const LAS float* s = scr + (8 * c) * 33 + n;
;         v4u o; o.x = pk2(s[0 * 33], s[1 * 33]); o.y = pk2(s[2 * 33], s[3 * 33]); o.z = pk2(s[4 * 33], s[5 * 33]); o.w = pk2(s[6 * 33], s[7 * 33]);
;         *(GAS v4u*)(WT + (size_t)(n0 + n) * K + k0 + 8 * c) = o; }
;     LDS_WAIT(); asm volatile("" ::: "memory");
	s_lshl_b32 s20, s27, 7
	s_cmp_lt_u32 s27, 40
	s_cselect_b32 s21, 0, 0x830
	s_cmp_lt_u32 s27, 72
	s_cselect_b32 s21, s21, 0xfffff030
	s_add_i32 s20, s20, s21
	s_lshl_b32 s20, s20, 2
	s_add_u32 s8, s16, s20
	s_addc_u32 s9, s17, 0
	global_load_dwordx4 v[144:147], v208, s[8:9]
	s_add_u32 s8, s8, 0x16280
	s_addc_u32 s9, s9, 0
	global_load_dwordx4 v[148:151], v208, s[8:9]
	s_add_u32 s8, s8, 0x16280
	s_addc_u32 s9, s9, 0
	global_load_dwordx4 v[152:155], v208, s[8:9]
	s_add_u32 s8, s8, 0x16280
	s_addc_u32 s9, s9, 0
	global_load_dwordx4 v[156:159], v208, s[8:9]
	s_add_u32 s8, s8, 0x16280
	s_addc_u32 s9, s9, 0
	global_load_dwordx4 v[160:163], v208, s[8:9]
	s_add_u32 s8, s8, 0x16280
	s_addc_u32 s9, s9, 0
	global_load_dwordx4 v[164:167], v208, s[8:9]
	s_add_u32 s8, s8, 0x16280
	s_addc_u32 s9, s9, 0
	global_load_dwordx4 v[168:171], v208, s[8:9]
	s_add_u32 s8, s8, 0x16280
	s_addc_u32 s9, s9, 0
	global_load_dwordx4 v[172:175], v208, s[8:9]
	s_mul_i32 s20, s26, 0x100000
	s_add_u32 s6, s18, s20
	s_addc_u32 s7, s19, 0
	s_cmp_lt_u32 s26, 16
	s_cselect_b32 s20, 1, 0
	s_sub_i32 s21, s26, 16
	s_bitcmp0_b32 s21, 2
	s_cselect_b32 s21, 1, 0
	s_cmp_lt_u32 s26, 40
	s_cselect_b32 s21, s21, 0
	s_or_b32 s20, s20, s21
	s_cmp_lg_u32 s20, 0
	s_cselect_b64 s[20:21], -1, 0
	v_cndmask_b32_e64 v108, v100, v104, s[20:21]
	v_cndmask_b32_e64 v109, v101, v105, s[20:21]
	v_cndmask_b32_e64 v110, v102, v106, s[20:21]
	v_cndmask_b32_e64 v111, v103, v107, s[20:21]
	ds_read_b32 v226, v112
	ds_read_b32 v227, v112 offset:512
	ds_read_b32 v228, v112 offset:1024
	ds_read_b32 v229, v112 offset:1536
	ds_read_b32 v230, v112 offset:2048
	ds_read_b32 v231, v112 offset:2560
	ds_read_b32 v232, v112 offset:3072
	ds_read_b32 v233, v112 offset:3584
	s_waitcnt lgkmcnt(0)
	v_bfe_u32 v120, v226, 16, 1
	v_bfe_u32 v121, v227, 16, 1
	v_bfe_u32 v122, v228, 16, 1
	v_bfe_u32 v123, v229, 16, 1
	v_bfe_u32 v124, v230, 16, 1
	v_bfe_u32 v125, v231, 16, 1
	v_bfe_u32 v126, v232, 16, 1
	v_bfe_u32 v127, v233, 16, 1
	v_add3_u32 v226, v226, v120, s28
	v_add3_u32 v227, v227, v121, s28
	v_add3_u32 v228, v228, v122, s28
	v_add3_u32 v229, v229, v123, s28
	v_add3_u32 v230, v230, v124, s28
	v_add3_u32 v231, v231, v125, s28
	v_add3_u32 v232, v232, v126, s28
	v_add3_u32 v233, v233, v127, s28
	v_perm_b32 v242, v227, v226, s29
	v_perm_b32 v243, v229, v228, s29
	v_perm_b32 v244, v231, v230, s29
	v_perm_b32 v245, v233, v232, s29
	s_nop 0
	global_store_dwordx4 v108, v[242:245], s[6:7]
	ds_read_b32 v226, v114
	ds_read_b32 v227, v114 offset:512
	ds_read_b32 v228, v114 offset:1024
	ds_read_b32 v229, v114 offset:1536
	ds_read_b32 v230, v114 offset:2048
	ds_read_b32 v231, v114 offset:2560
	ds_read_b32 v232, v114 offset:3072
	ds_read_b32 v233, v114 offset:3584
	s_waitcnt lgkmcnt(0)
	v_bfe_u32 v120, v226, 16, 1
	v_bfe_u32 v121, v227, 16, 1
	v_bfe_u32 v122, v228, 16, 1
	v_bfe_u32 v123, v229, 16, 1
	v_bfe_u32 v124, v230, 16, 1
	v_bfe_u32 v125, v231, 16, 1
	v_bfe_u32 v126, v232, 16, 1
	v_bfe_u32 v127, v233, 16, 1
	v_add3_u32 v226, v226, v120, s28
	v_add3_u32 v227, v227, v121, s28
	v_add3_u32 v228, v228, v122, s28
	v_add3_u32 v229, v229, v123, s28
	v_add3_u32 v230, v230, v124, s28
	v_add3_u32 v231, v231, v125, s28
	v_add3_u32 v232, v232, v126, s28
	v_add3_u32 v233, v233, v127, s28
	v_perm_b32 v242, v227, v226, s29
	v_perm_b32 v243, v229, v228, s29
	v_perm_b32 v244, v231, v230, s29
	v_perm_b32 v245, v233, v232, s29
	s_nop 0
	global_store_dwordx4 v109, v[242:245], s[6:7]
	ds_read_b32 v226, v116
	ds_read_b32 v227, v116 offset:512
	ds_read_b32 v228, v116 offset:1024
	ds_read_b32 v229, v116 offset:1536
	ds_read_b32 v230, v116 offset:2048
	ds_read_b32 v231, v116 offset:2560
	ds_read_b32 v232, v116 offset:3072
	ds_read_b32 v233, v116 offset:3584
	s_waitcnt lgkmcnt(0)
	v_bfe_u32 v120, v226, 16, 1
	v_bfe_u32 v121, v227, 16, 1
	v_bfe_u32 v122, v228, 16, 1
	v_bfe_u32 v123, v229, 16, 1
	v_bfe_u32 v124, v230, 16, 1
	v_bfe_u32 v125, v231, 16, 1
	v_bfe_u32 v126, v232, 16, 1
	v_bfe_u32 v127, v233, 16, 1
	v_add3_u32 v226, v226, v120, s28
	v_add3_u32 v227, v227, v121, s28
	v_add3_u32 v228, v228, v122, s28
	v_add3_u32 v229, v229, v123, s28
	v_add3_u32 v230, v230, v124, s28
	v_add3_u32 v231, v231, v125, s28
	v_add3_u32 v232, v232, v126, s28
	v_add3_u32 v233, v233, v127, s28
	v_perm_b32 v242, v227, v226, s29
	v_perm_b32 v243, v229, v228, s29
	v_perm_b32 v244, v231, v230, s29
	v_perm_b32 v245, v233, v232, s29
	s_nop 0
	global_store_dwordx4 v110, v[242:245], s[6:7]
	ds_read_b32 v226, v118
	ds_read_b32 v227, v118 offset:512
	ds_read_b32 v228, v118 offset:1024
	ds_read_b32 v229, v118 offset:1536
	ds_read_b32 v230, v118 offset:2048
	ds_read_b32 v231, v118 offset:2560
	ds_read_b32 v232, v118 offset:3072
	ds_read_b32 v233, v118 offset:3584
	s_waitcnt lgkmcnt(0)
	v_bfe_u32 v120, v226, 16, 1
	v_bfe_u32 v121, v227, 16, 1
	v_bfe_u32 v122, v228, 16, 1
	v_bfe_u32 v123, v229, 16, 1
	v_bfe_u32 v124, v230, 16, 1
	v_bfe_u32 v125, v231, 16, 1
	v_bfe_u32 v126, v232, 16, 1
	v_bfe_u32 v127, v233, 16, 1
	v_add3_u32 v226, v226, v120, s28
	v_add3_u32 v227, v227, v121, s28
	v_add3_u32 v228, v228, v122, s28
	v_add3_u32 v229, v229, v123, s28
	v_add3_u32 v230, v230, v124, s28
	v_add3_u32 v231, v231, v125, s28
	v_add3_u32 v232, v232, v126, s28
	v_add3_u32 v233, v233, v127, s28
	v_perm_b32 v242, v227, v226, s29
	v_perm_b32 v243, v229, v228, s29
	v_perm_b32 v244, v231, v230, s29
	v_perm_b32 v245, v233, v232, s29
	s_nop 0
	global_store_dwordx4 v111, v[242:245], s[6:7]
	s_add_i32 s26, s23, 56
	s_add_i32 s27, s23, 72
	s_waitcnt vmcnt(16)
	v_mul_f32_e32 v176, v218, v176
	v_mul_f32_e32 v177, v218, v177
	v_mul_f32_e32 v178, v218, v178
	v_mul_f32_e32 v179, v218, v179
	ds_write_b128 v210, v[176:179]
	v_mul_f32_e32 v180, v219, v180
	v_mul_f32_e32 v181, v219, v181
	v_mul_f32_e32 v182, v219, v182
	v_mul_f32_e32 v183, v219, v183
	ds_write_b128 v210, v[180:183] offset:1024
	v_mul_f32_e32 v184, v220, v184
	v_mul_f32_e32 v185, v220, v185
	v_mul_f32_e32 v186, v220, v186
	v_mul_f32_e32 v187, v220, v187
	ds_write_b128 v210, v[184:187] offset:2048
	v_mul_f32_e32 v188, v221, v188
	v_mul_f32_e32 v189, v221, v189
	v_mul_f32_e32 v190, v221, v190
	v_mul_f32_e32 v191, v221, v191
	ds_write_b128 v210, v[188:191] offset:3072
	v_mul_f32_e32 v192, v222, v192
	v_mul_f32_e32 v193, v222, v193
	v_mul_f32_e32 v194, v222, v194
	v_mul_f32_e32 v195, v222, v195
	ds_write_b128 v210, v[192:195] offset:4096
	v_mul_f32_e32 v196, v223, v196
	v_mul_f32_e32 v197, v223, v197
	v_mul_f32_e32 v198, v223, v198
	v_mul_f32_e32 v199, v223, v199
	ds_write_b128 v210, v[196:199] offset:5120
	v_mul_f32_e32 v200, v224, v200
	v_mul_f32_e32 v201, v224, v201
	v_mul_f32_e32 v202, v224, v202
	v_mul_f32_e32 v203, v224, v203
	ds_write_b128 v210, v[200:203] offset:6144
	v_mul_f32_e32 v204, v225, v204
	v_mul_f32_e32 v205, v225, v205
	v_mul_f32_e32 v206, v225, v206
	v_mul_f32_e32 v207, v225, v207
	ds_write_b128 v210, v[204:207] offset:7168
	s_waitcnt lgkmcnt(0)
	s_barrier
; #define GAS __attribute__((address_space(1)))
; #define LAS __attribute__((address_space(3)))
; #define LDS_WAIT() asm volatile("s_waitcnt lgkmcnt(0)" ::: "memory")
; __device__ __forceinline__ unsigned pk2(float lo, float hi) { return f2bf(lo) | (f2bf(hi) << 16); }
; __device__ __forceinline__ int nat_dim(int p) { return (p >> 1) + 64 * (p & 1); }
; __device__ __forceinline__ int src_col_in(int c) {
;     if (c < 5120) { const int blk = c >> 7, p = c & 127; const bool rope = blk < 16 || ((((blk - 16) >> 2) & 1) == 0); const int d = rope ? (p >> 1) + 64 * (p & 1) : p; return blk * 128 + d; }
; template <int MAP, bool KS, bool KPERM = false>
; __device__ __forceinline__ void p0_transpose_item(const float* W, int K, int Nsrc, int nblk, bf16* WT, const float* ksA, const float* ksB, int ksplit, LAS float* scr, int item, int lane) {
;     const int kb = item / nblk, nb = item % nblk, k0 = 64 * kb, n0 = 32 * nb;
;     const int nr = n0 + (lane & 31); const int sc = MAP == 1 ? src_col_in(nr) : (MAP == 2 ? nat_dim(nr) : nr);
;     float v[32];
; #pragma unroll
;     for (int i = 0; i < 32; ++i) { const int k = k0 + 2 * i + (lane >> 5); const int ksrc = KPERM ? ((k & ~127) + nat_dim(k & 127)) : k;
;         v[i] = sc >= 0 ? W[(size_t)ksrc * Nsrc + sc] : 0.f; }
; #pragma unroll
;     for (int i = 0; i < 32; ++i) { const int kk = 2 * i + (lane >> 5); const int k = k0 + kk;
;         if (KS) v[i] *= (k < ksplit ? ksA[k] : ksB[k - ksplit]);
;         scr[kk * 33 + (lane & 31)] = v[i]; }
;     LDS_WAIT(); asm volatile("" ::: "memory");
;     const int c = lane & 7;
; #pragma unroll
;     for (int j = 0; j < 4; ++j) { const int n = (lane >> 3) + 8 * j; const LAS float* s = scr + (8 * c) * 33 + n;
;         v4u o; o.x = pk2(s[0 * 33], s[1 * 33]); o.y = pk2(s[2 * 33], s[3 * 33]); o.z = pk2(s[4 * 33], s[5 * 33]); o.w = pk2(s[6 * 33], s[7 * 33]);
;         *(GAS v4u*)(WT + (size_t)(n0 + n) * K + k0 + 8 * c) = o; }
;     LDS_WAIT(); asm volatile("" ::: "memory");
	s_lshl_b32 s20, s27, 7
	s_cmp_lt_u32 s27, 40
	s_cselect_b32 s21, 0, 0x830
	s_cmp_lt_u32 s27, 72
	s_cselect_b32 s21, s21, 0xfffff030
	s_add_i32 s20, s20, s21
	s_lshl_b32 s20, s20, 2
	s_add_u32 s8, s16, s20
	s_addc_u32 s9, s17, 0
	global_load_dwordx4 v[176:179], v208, s[8:9]
	s_add_u32 s8, s8, 0x16280
	s_addc_u32 s9, s9, 0
	global_load_dwordx4 v[180:183], v208, s[8:9]
	s_add_u32 s8, s8, 0x16280
	s_addc_u32 s9, s9, 0
	global_load_dwordx4 v[184:187], v208, s[8:9]
	s_add_u32 s8, s8, 0x16280
	s_addc_u32 s9, s9, 0
	global_load_dwordx4 v[188:191], v208, s[8:9]
	s_add_u32 s8, s8, 0x16280
	s_addc_u32 s9, s9, 0
	global_load_dwordx4 v[192:195], v208, s[8:9]
	s_add_u32 s8, s8, 0x16280
	s_addc_u32 s9, s9, 0
	global_load_dwordx4 v[196:199], v208, s[8:9]
	s_add_u32 s8, s8, 0x16280
	s_addc_u32 s9, s9, 0
	global_load_dwordx4 v[200:203], v208, s[8:9]
	s_add_u32 s8, s8, 0x16280
	s_addc_u32 s9, s9, 0
	global_load_dwordx4 v[204:207], v208, s[8:9]
	s_mul_i32 s20, s26, 0x100000
	s_add_u32 s6, s18, s20
	s_addc_u32 s7, s19, 0
	s_cmp_lt_u32 s26, 16
	s_cselect_b32 s20, 1, 0
	s_sub_i32 s21, s26, 16
	s_bitcmp0_b32 s21, 2
	s_cselect_b32 s21, 1, 0
	s_cmp_lt_u32 s26, 40
	s_cselect_b32 s21, s21, 0
	s_or_b32 s20, s20, s21
	s_cmp_lg_u32 s20, 0
	s_cselect_b64 s[20:21], -1, 0
	v_cndmask_b32_e64 v108, v100, v104, s[20:21]
	v_cndmask_b32_e64 v109, v101, v105, s[20:21]
	v_cndmask_b32_e64 v110, v102, v106, s[20:21]
	v_cndmask_b32_e64 v111, v103, v107, s[20:21]
	ds_read_b32 v226, v113
	ds_read_b32 v227, v113 offset:512
	ds_read_b32 v228, v113 offset:1024
	ds_read_b32 v229, v113 offset:1536
	ds_read_b32 v230, v113 offset:2048
	ds_read_b32 v231, v113 offset:2560
	ds_read_b32 v232, v113 offset:3072
	ds_read_b32 v233, v113 offset:3584
	s_waitcnt lgkmcnt(0)
	v_bfe_u32 v120, v226, 16, 1
	v_bfe_u32 v121, v227, 16, 1
	v_bfe_u32 v122, v228, 16, 1
	v_bfe_u32 v123, v229, 16, 1
	v_bfe_u32 v124, v230, 16, 1
	v_bfe_u32 v125, v231, 16, 1
	v_bfe_u32 v126, v232, 16, 1
	v_bfe_u32 v127, v233, 16, 1
	v_add3_u32 v226, v226, v120, s28
	v_add3_u32 v227, v227, v121, s28
	v_add3_u32 v228, v228, v122, s28
	v_add3_u32 v229, v229, v123, s28
	v_add3_u32 v230, v230, v124, s28
	v_add3_u32 v231, v231, v125, s28
	v_add3_u32 v232, v232, v126, s28
	v_add3_u32 v233, v233, v127, s28
	v_perm_b32 v242, v227, v226, s29
	v_perm_b32 v243, v229, v228, s29
	v_perm_b32 v244, v231, v230, s29
	v_perm_b32 v245, v233, v232, s29
	s_nop 0
	global_store_dwordx4 v108, v[242:245], s[6:7]
	ds_read_b32 v226, v115
	ds_read_b32 v227, v115 offset:512
	ds_read_b32 v228, v115 offset:1024
	ds_read_b32 v229, v115 offset:1536
	ds_read_b32 v230, v115 offset:2048
	ds_read_b32 v231, v115 offset:2560
	ds_read_b32 v232, v115 offset:3072
	ds_read_b32 v233, v115 offset:3584
	s_waitcnt lgkmcnt(0)
	v_bfe_u32 v120, v226, 16, 1
	v_bfe_u32 v121, v227, 16, 1
	v_bfe_u32 v122, v228, 16, 1
	v_bfe_u32 v123, v229, 16, 1
	v_bfe_u32 v124, v230, 16, 1
	v_bfe_u32 v125, v231, 16, 1
	v_bfe_u32 v126, v232, 16, 1
	v_bfe_u32 v127, v233, 16, 1
	v_add3_u32 v226, v226, v120, s28
	v_add3_u32 v227, v227, v121, s28
	v_add3_u32 v228, v228, v122, s28
	v_add3_u32 v229, v229, v123, s28
	v_add3_u32 v230, v230, v124, s28
	v_add3_u32 v231, v231, v125, s28
	v_add3_u32 v232, v232, v126, s28
	v_add3_u32 v233, v233, v127, s28
	v_perm_b32 v242, v227, v226, s29
	v_perm_b32 v243, v229, v228, s29
	v_perm_b32 v244, v231, v230, s29
	v_perm_b32 v245, v233, v232, s29
	s_nop 0
	global_store_dwordx4 v109, v[242:245], s[6:7]
	ds_read_b32 v226, v117
	ds_read_b32 v227, v117 offset:512
	ds_read_b32 v228, v117 offset:1024
	ds_read_b32 v229, v117 offset:1536
	ds_read_b32 v230, v117 offset:2048
	ds_read_b32 v231, v117 offset:2560
	ds_read_b32 v232, v117 offset:3072
	ds_read_b32 v233, v117 offset:3584
	s_waitcnt lgkmcnt(0)
	v_bfe_u32 v120, v226, 16, 1
	v_bfe_u32 v121, v227, 16, 1
	v_bfe_u32 v122, v228, 16, 1
	v_bfe_u32 v123, v229, 16, 1
	v_bfe_u32 v124, v230, 16, 1
	v_bfe_u32 v125, v231, 16, 1
	v_bfe_u32 v126, v232, 16, 1
	v_bfe_u32 v127, v233, 16, 1
	v_add3_u32 v226, v226, v120, s28
	v_add3_u32 v227, v227, v121, s28
	v_add3_u32 v228, v228, v122, s28
	v_add3_u32 v229, v229, v123, s28
	v_add3_u32 v230, v230, v124, s28
	v_add3_u32 v231, v231, v125, s28
	v_add3_u32 v232, v232, v126, s28
	v_add3_u32 v233, v233, v127, s28
	v_perm_b32 v242, v227, v226, s29
	v_perm_b32 v243, v229, v228, s29
	v_perm_b32 v244, v231, v230, s29
	v_perm_b32 v245, v233, v232, s29
	s_nop 0
	global_store_dwordx4 v110, v[242:245], s[6:7]
	ds_read_b32 v226, v119
	ds_read_b32 v227, v119 offset:512
	ds_read_b32 v228, v119 offset:1024
	ds_read_b32 v229, v119 offset:1536
	ds_read_b32 v230, v119 offset:2048
	ds_read_b32 v231, v119 offset:2560
	ds_read_b32 v232, v119 offset:3072
	ds_read_b32 v233, v119 offset:3584
	s_waitcnt lgkmcnt(0)
	v_bfe_u32 v120, v226, 16, 1
	v_bfe_u32 v121, v227, 16, 1
	v_bfe_u32 v122, v228, 16, 1
	v_bfe_u32 v123, v229, 16, 1
	v_bfe_u32 v124, v230, 16, 1
	v_bfe_u32 v125, v231, 16, 1
	v_bfe_u32 v126, v232, 16, 1
	v_bfe_u32 v127, v233, 16, 1
	v_add3_u32 v226, v226, v120, s28
	v_add3_u32 v227, v227, v121, s28
	v_add3_u32 v228, v228, v122, s28
	v_add3_u32 v229, v229, v123, s28
	v_add3_u32 v230, v230, v124, s28
	v_add3_u32 v231, v231, v125, s28
	v_add3_u32 v232, v232, v126, s28
	v_add3_u32 v233, v233, v127, s28
	v_perm_b32 v242, v227, v226, s29
	v_perm_b32 v243, v229, v228, s29
	v_perm_b32 v244, v231, v230, s29
	v_perm_b32 v245, v233, v232, s29
	s_nop 0
	global_store_dwordx4 v111, v[242:245], s[6:7]
	s_add_i32 s26, s23, 64
	s_add_i32 s27, s23, 80
	s_waitcnt vmcnt(16)
	v_mul_f32_e32 v144, v218, v144
	v_mul_f32_e32 v145, v218, v145
	v_mul_f32_e32 v146, v218, v146
	v_mul_f32_e32 v147, v218, v147
	ds_write_b128 v209, v[144:147]
	v_mul_f32_e32 v148, v219, v148
	v_mul_f32_e32 v149, v219, v149
	v_mul_f32_e32 v150, v219, v150
	v_mul_f32_e32 v151, v219, v151
	ds_write_b128 v209, v[148:151] offset:1024
	v_mul_f32_e32 v152, v220, v152
	v_mul_f32_e32 v153, v220, v153
	v_mul_f32_e32 v154, v220, v154
	v_mul_f32_e32 v155, v220, v155
	ds_write_b128 v209, v[152:155] offset:2048
	v_mul_f32_e32 v156, v221, v156
	v_mul_f32_e32 v157, v221, v157
	v_mul_f32_e32 v158, v221, v158
	v_mul_f32_e32 v159, v221, v159
	ds_write_b128 v209, v[156:159] offset:3072
	v_mul_f32_e32 v160, v222, v160
	v_mul_f32_e32 v161, v222, v161
	v_mul_f32_e32 v162, v222, v162
	v_mul_f32_e32 v163, v222, v163
	ds_write_b128 v209, v[160:163] offset:4096
	v_mul_f32_e32 v164, v223, v164
	v_mul_f32_e32 v165, v223, v165
	v_mul_f32_e32 v166, v223, v166
	v_mul_f32_e32 v167, v223, v167
	ds_write_b128 v209, v[164:167] offset:5120
	v_mul_f32_e32 v168, v224, v168
	v_mul_f32_e32 v169, v224, v169
	v_mul_f32_e32 v170, v224, v170
	v_mul_f32_e32 v171, v224, v171
	ds_write_b128 v209, v[168:171] offset:6144
	v_mul_f32_e32 v172, v225, v172
	v_mul_f32_e32 v173, v225, v173
	v_mul_f32_e32 v174, v225, v174
	v_mul_f32_e32 v175, v225, v175
	ds_write_b128 v209, v[172:175] offset:7168
	s_waitcnt lgkmcnt(0)
	s_barrier
; #define GAS __attribute__((address_space(1)))
; #define LAS __attribute__((address_space(3)))
; #define LDS_WAIT() asm volatile("s_waitcnt lgkmcnt(0)" ::: "memory")
; __device__ __forceinline__ unsigned pk2(float lo, float hi) { return f2bf(lo) | (f2bf(hi) << 16); }
; __device__ __forceinline__ int nat_dim(int p) { return (p >> 1) + 64 * (p & 1); }
; __device__ __forceinline__ int src_col_in(int c) {
;     if (c < 5120) { const int blk = c >> 7, p = c & 127; const bool rope = blk < 16 || ((((blk - 16) >> 2) & 1) == 0); const int d = rope ? (p >> 1) + 64 * (p & 1) : p; return blk * 128 + d; }
; template <int MAP, bool KS, bool KPERM = false>
; __device__ __forceinline__ void p0_transpose_item(const float* W, int K, int Nsrc, int nblk, bf16* WT, const float* ksA, const float* ksB, int ksplit, LAS float* scr, int item, int lane) {
;     const int kb = item / nblk, nb = item % nblk, k0 = 64 * kb, n0 = 32 * nb;
;     const int nr = n0 + (lane & 31); const int sc = MAP == 1 ? src_col_in(nr) : (MAP == 2 ? nat_dim(nr) : nr);
;     float v[32];
; #pragma unroll
;     for (int i = 0; i < 32; ++i) { const int k = k0 + 2 * i + (lane >> 5); const int ksrc = KPERM ? ((k & ~127) + nat_dim(k & 127)) : k;
;         v[i] = sc >= 0 ? W[(size_t)ksrc * Nsrc + sc] : 0.f; }
; #pragma unroll
;     for (int i = 0; i < 32; ++i) { const int kk = 2 * i + (lane >> 5); const int k = k0 + kk;
;         if (KS) v[i] *= (k < ksplit ? ksA[k] : ksB[k - ksplit]);
;         scr[kk * 33 + (lane & 31)] = v[i]; }
;     LDS_WAIT(); asm volatile("" ::: "memory");
;     const int c = lane & 7;
; #pragma unroll
;     for (int j = 0; j < 4; ++j) { const int n = (lane >> 3) + 8 * j; const LAS float* s = scr + (8 * c) * 33 + n;
;         v4u o; o.x = pk2(s[0 * 33], s[1 * 33]); o.y = pk2(s[2 * 33], s[3 * 33]); o.z = pk2(s[4 * 33], s[5 * 33]); o.w = pk2(s[6 * 33], s[7 * 33]);
;         *(GAS v4u*)(WT + (size_t)(n0 + n) * K + k0 + 8 * c) = o; }
;     LDS_WAIT(); asm volatile("" ::: "memory");
	s_lshl_b32 s20, s27, 7
	s_cmp_lt_u32 s27, 40
	s_cselect_b32 s21, 0, 0x830
	s_cmp_lt_u32 s27, 72
	s_cselect_b32 s21, s21, 0xfffff030
	s_add_i32 s20, s20, s21
	s_lshl_b32 s20, s20, 2
	s_add_u32 s8, s16, s20
	s_addc_u32 s9, s17, 0
	global_load_dwordx4 v[144:147], v208, s[8:9]
	s_add_u32 s8, s8, 0x16280
	s_addc_u32 s9, s9, 0
	global_load_dwordx4 v[148:151], v208, s[8:9]
	s_add_u32 s8, s8, 0x16280
	s_addc_u32 s9, s9, 0
	global_load_dwordx4 v[152:155], v208, s[8:9]
	s_add_u32 s8, s8, 0x16280
	s_addc_u32 s9, s9, 0
	global_load_dwordx4 v[156:159], v208, s[8:9]
	s_add_u32 s8, s8, 0x16280
	s_addc_u32 s9, s9, 0
	global_load_dwordx4 v[160:163], v208, s[8:9]
	s_add_u32 s8, s8, 0x16280
	s_addc_u32 s9, s9, 0
	global_load_dwordx4 v[164:167], v208, s[8:9]
	s_add_u32 s8, s8, 0x16280
	s_addc_u32 s9, s9, 0
	global_load_dwordx4 v[168:171], v208, s[8:9]
	s_add_u32 s8, s8, 0x16280
	s_addc_u32 s9, s9, 0
	global_load_dwordx4 v[172:175], v208, s[8:9]
	s_mul_i32 s20, s26, 0x100000
	s_add_u32 s6, s18, s20
	s_addc_u32 s7, s19, 0
	s_cmp_lt_u32 s26, 16
	s_cselect_b32 s20, 1, 0
	s_sub_i32 s21, s26, 16
	s_bitcmp0_b32 s21, 2
	s_cselect_b32 s21, 1, 0
	s_cmp_lt_u32 s26, 40
	s_cselect_b32 s21, s21, 0
	s_or_b32 s20, s20, s21
	s_cmp_lg_u32 s20, 0
	s_cselect_b64 s[20:21], -1, 0
	v_cndmask_b32_e64 v108, v100, v104, s[20:21]
	v_cndmask_b32_e64 v109, v101, v105, s[20:21]
	v_cndmask_b32_e64 v110, v102, v106, s[20:21]
	v_cndmask_b32_e64 v111, v103, v107, s[20:21]
	ds_read_b32 v226, v112
	ds_read_b32 v227, v112 offset:512
	ds_read_b32 v228, v112 offset:1024
	ds_read_b32 v229, v112 offset:1536
	ds_read_b32 v230, v112 offset:2048
	ds_read_b32 v231, v112 offset:2560
	ds_read_b32 v232, v112 offset:3072
	ds_read_b32 v233, v112 offset:3584
	s_waitcnt lgkmcnt(0)
	v_bfe_u32 v120, v226, 16, 1
	v_bfe_u32 v121, v227, 16, 1
	v_bfe_u32 v122, v228, 16, 1
	v_bfe_u32 v123, v229, 16, 1
	v_bfe_u32 v124, v230, 16, 1
	v_bfe_u32 v125, v231, 16, 1
	v_bfe_u32 v126, v232, 16, 1
	v_bfe_u32 v127, v233, 16, 1
	v_add3_u32 v226, v226, v120, s28
	v_add3_u32 v227, v227, v121, s28
	v_add3_u32 v228, v228, v122, s28
	v_add3_u32 v229, v229, v123, s28
	v_add3_u32 v230, v230, v124, s28
	v_add3_u32 v231, v231, v125, s28
	v_add3_u32 v232, v232, v126, s28
	v_add3_u32 v233, v233, v127, s28
	v_perm_b32 v242, v227, v226, s29
	v_perm_b32 v243, v229, v228, s29
	v_perm_b32 v244, v231, v230, s29
	v_perm_b32 v245, v233, v232, s29
	s_nop 0
	global_store_dwordx4 v108, v[242:245], s[6:7]
	ds_read_b32 v226, v114
	ds_read_b32 v227, v114 offset:512
	ds_read_b32 v228, v114 offset:1024
	ds_read_b32 v229, v114 offset:1536
	ds_read_b32 v230, v114 offset:2048
	ds_read_b32 v231, v114 offset:2560
	ds_read_b32 v232, v114 offset:3072
	ds_read_b32 v233, v114 offset:3584
	s_waitcnt lgkmcnt(0)
	v_bfe_u32 v120, v226, 16, 1
	v_bfe_u32 v121, v227, 16, 1
	v_bfe_u32 v122, v228, 16, 1
	v_bfe_u32 v123, v229, 16, 1
	v_bfe_u32 v124, v230, 16, 1
	v_bfe_u32 v125, v231, 16, 1
	v_bfe_u32 v126, v232, 16, 1
	v_bfe_u32 v127, v233, 16, 1
	v_add3_u32 v226, v226, v120, s28
	v_add3_u32 v227, v227, v121, s28
	v_add3_u32 v228, v228, v122, s28
	v_add3_u32 v229, v229, v123, s28
	v_add3_u32 v230, v230, v124, s28
	v_add3_u32 v231, v231, v125, s28
	v_add3_u32 v232, v232, v126, s28
	v_add3_u32 v233, v233, v127, s28
	v_perm_b32 v242, v227, v226, s29
	v_perm_b32 v243, v229, v228, s29
	v_perm_b32 v244, v231, v230, s29
	v_perm_b32 v245, v233, v232, s29
	s_nop 0
	global_store_dwordx4 v109, v[242:245], s[6:7]
	ds_read_b32 v226, v116
	ds_read_b32 v227, v116 offset:512
	ds_read_b32 v228, v116 offset:1024
	ds_read_b32 v229, v116 offset:1536
	ds_read_b32 v230, v116 offset:2048
	ds_read_b32 v231, v116 offset:2560
	ds_read_b32 v232, v116 offset:3072
	ds_read_b32 v233, v116 offset:3584
	s_waitcnt lgkmcnt(0)
	v_bfe_u32 v120, v226, 16, 1
	v_bfe_u32 v121, v227, 16, 1
	v_bfe_u32 v122, v228, 16, 1
	v_bfe_u32 v123, v229, 16, 1
	v_bfe_u32 v124, v230, 16, 1
	v_bfe_u32 v125, v231, 16, 1
	v_bfe_u32 v126, v232, 16, 1
	v_bfe_u32 v127, v233, 16, 1
	v_add3_u32 v226, v226, v120, s28
	v_add3_u32 v227, v227, v121, s28
	v_add3_u32 v228, v228, v122, s28
	v_add3_u32 v229, v229, v123, s28
	v_add3_u32 v230, v230, v124, s28
	v_add3_u32 v231, v231, v125, s28
	v_add3_u32 v232, v232, v126, s28
	v_add3_u32 v233, v233, v127, s28
	v_perm_b32 v242, v227, v226, s29
	v_perm_b32 v243, v229, v228, s29
	v_perm_b32 v244, v231, v230, s29
	v_perm_b32 v245, v233, v232, s29
	s_nop 0
	global_store_dwordx4 v110, v[242:245], s[6:7]
	ds_read_b32 v226, v118
	ds_read_b32 v227, v118 offset:512
	ds_read_b32 v228, v118 offset:1024
	ds_read_b32 v229, v118 offset:1536
	ds_read_b32 v230, v118 offset:2048
	ds_read_b32 v231, v118 offset:2560
	ds_read_b32 v232, v118 offset:3072
	ds_read_b32 v233, v118 offset:3584
	s_waitcnt lgkmcnt(0)
	v_bfe_u32 v120, v226, 16, 1
	v_bfe_u32 v121, v227, 16, 1
	v_bfe_u32 v122, v228, 16, 1
	v_bfe_u32 v123, v229, 16, 1
	v_bfe_u32 v124, v230, 16, 1
	v_bfe_u32 v125, v231, 16, 1
	v_bfe_u32 v126, v232, 16, 1
	v_bfe_u32 v127, v233, 16, 1
	v_add3_u32 v226, v226, v120, s28
	v_add3_u32 v227, v227, v121, s28
	v_add3_u32 v228, v228, v122, s28
	v_add3_u32 v229, v229, v123, s28
	v_add3_u32 v230, v230, v124, s28
	v_add3_u32 v231, v231, v125, s28
	v_add3_u32 v232, v232, v126, s28
	v_add3_u32 v233, v233, v127, s28
	v_perm_b32 v242, v227, v226, s29
	v_perm_b32 v243, v229, v228, s29
	v_perm_b32 v244, v231, v230, s29
	v_perm_b32 v245, v233, v232, s29
	s_nop 0
	global_store_dwordx4 v111, v[242:245], s[6:7]
	s_add_i32 s26, s23, 72
	s_add_i32 s27, s23, 88
	s_waitcnt vmcnt(16)
	v_mul_f32_e32 v176, v218, v176
	v_mul_f32_e32 v177, v218, v177
	v_mul_f32_e32 v178, v218, v178
	v_mul_f32_e32 v179, v218, v179
	ds_write_b128 v210, v[176:179]
	v_mul_f32_e32 v180, v219, v180
	v_mul_f32_e32 v181, v219, v181
	v_mul_f32_e32 v182, v219, v182
	v_mul_f32_e32 v183, v219, v183
	ds_write_b128 v210, v[180:183] offset:1024
	v_mul_f32_e32 v184, v220, v184
	v_mul_f32_e32 v185, v220, v185
	v_mul_f32_e32 v186, v220, v186
	v_mul_f32_e32 v187, v220, v187
	ds_write_b128 v210, v[184:187] offset:2048
	v_mul_f32_e32 v188, v221, v188
	v_mul_f32_e32 v189, v221, v189
	v_mul_f32_e32 v190, v221, v190
	v_mul_f32_e32 v191, v221, v191
	ds_write_b128 v210, v[188:191] offset:3072
	v_mul_f32_e32 v192, v222, v192
	v_mul_f32_e32 v193, v222, v193
	v_mul_f32_e32 v194, v222, v194
	v_mul_f32_e32 v195, v222, v195
	ds_write_b128 v210, v[192:195] offset:4096
	v_mul_f32_e32 v196, v223, v196
	v_mul_f32_e32 v197, v223, v197
	v_mul_f32_e32 v198, v223, v198
	v_mul_f32_e32 v199, v223, v199
	ds_write_b128 v210, v[196:199] offset:5120
	v_mul_f32_e32 v200, v224, v200
	v_mul_f32_e32 v201, v224, v201
	v_mul_f32_e32 v202, v224, v202
	v_mul_f32_e32 v203, v224, v203
	ds_write_b128 v210, v[200:203] offset:6144
	v_mul_f32_e32 v204, v225, v204
	v_mul_f32_e32 v205, v225, v205
	v_mul_f32_e32 v206, v225, v206
	v_mul_f32_e32 v207, v225, v207
	ds_write_b128 v210, v[204:207] offset:7168
	s_waitcnt lgkmcnt(0)
	s_barrier
; #define GAS __attribute__((address_space(1)))
; #define LAS __attribute__((address_space(3)))
; #define LDS_WAIT() asm volatile("s_waitcnt lgkmcnt(0)" ::: "memory")
; __device__ __forceinline__ unsigned pk2(float lo, float hi) { return f2bf(lo) | (f2bf(hi) << 16); }
; __device__ __forceinline__ int nat_dim(int p) { return (p >> 1) + 64 * (p & 1); }
; template <int MAP, bool KS, bool KPERM = false>
; __device__ __forceinline__ void p0_transpose_item(const float* W, int K, int Nsrc, int nblk, bf16* WT, const float* ksA, const float* ksB, int ksplit, LAS float* scr, int item, int lane) {
;     const int kb = item / nblk, nb = item % nblk, k0 = 64 * kb, n0 = 32 * nb;
;     const int nr = n0 + (lane & 31); const int sc = MAP == 1 ? src_col_in(nr) : (MAP == 2 ? nat_dim(nr) : nr);
;     float v[32];
; #pragma unroll
;     for (int i = 0; i < 32; ++i) { const int k = k0 + 2 * i + (lane >> 5); const int ksrc = KPERM ? ((k & ~127) + nat_dim(k & 127)) : k;
;         v[i] = sc >= 0 ? W[(size_t)ksrc * Nsrc + sc] : 0.f; }
; #pragma unroll
;     for (int i = 0; i < 32; ++i) { const int kk = 2 * i + (lane >> 5); const int k = k0 + kk;
;         if (KS) v[i] *= (k < ksplit ? ksA[k] : ksB[k - ksplit]);
;         scr[kk * 33 + (lane & 31)] = v[i]; }
;     LDS_WAIT(); asm volatile("" ::: "memory");
;     const int c = lane & 7;
; #pragma unroll
;     for (int j = 0; j < 4; ++j) { const int n = (lane >> 3) + 8 * j; const LAS float* s = scr + (8 * c) * 33 + n;
;         v4u o; o.x = pk2(s[0 * 33], s[1 * 33]); o.y = pk2(s[2 * 33], s[3 * 33]); o.z = pk2(s[4 * 33], s[5 * 33]); o.w = pk2(s[6 * 33], s[7 * 33]);
;         *(GAS v4u*)(WT + (size_t)(n0 + n) * K + k0 + 8 * c) = o; }
;     LDS_WAIT(); asm volatile("" ::: "memory");
	s_mul_i32 s20, s26, 0x100000
	s_add_u32 s6, s18, s20
	s_addc_u32 s7, s19, 0
	s_cmp_lt_u32 s26, 16
	s_cselect_b32 s20, 1, 0
	s_sub_i32 s21, s26, 16
	s_bitcmp0_b32 s21, 2
	s_cselect_b32 s21, 1, 0
	s_cmp_lt_u32 s26, 40
	s_cselect_b32 s21, s21, 0
	s_or_b32 s20, s20, s21
	s_cmp_lg_u32 s20, 0
	s_cselect_b64 s[20:21], -1, 0
	v_cndmask_b32_e64 v108, v100, v104, s[20:21]
	v_cndmask_b32_e64 v109, v101, v105, s[20:21]
	v_cndmask_b32_e64 v110, v102, v106, s[20:21]
	v_cndmask_b32_e64 v111, v103, v107, s[20:21]
	ds_read_b32 v226, v113
	ds_read_b32 v227, v113 offset:512
	ds_read_b32 v228, v113 offset:1024
	ds_read_b32 v229, v113 offset:1536
	ds_read_b32 v230, v113 offset:2048
	ds_read_b32 v231, v113 offset:2560
	ds_read_b32 v232, v113 offset:3072
	ds_read_b32 v233, v113 offset:3584
	s_waitcnt lgkmcnt(0)
	v_bfe_u32 v120, v226, 16, 1
	v_bfe_u32 v121, v227, 16, 1
	v_bfe_u32 v122, v228, 16, 1
	v_bfe_u32 v123, v229, 16, 1
	v_bfe_u32 v124, v230, 16, 1
	v_bfe_u32 v125, v231, 16, 1
	v_bfe_u32 v126, v232, 16, 1
	v_bfe_u32 v127, v233, 16, 1
	v_add3_u32 v226, v226, v120, s28
	v_add3_u32 v227, v227, v121, s28
	v_add3_u32 v228, v228, v122, s28
	v_add3_u32 v229, v229, v123, s28
	v_add3_u32 v230, v230, v124, s28
	v_add3_u32 v231, v231, v125, s28
	v_add3_u32 v232, v232, v126, s28
	v_add3_u32 v233, v233, v127, s28
	v_perm_b32 v242, v227, v226, s29
	v_perm_b32 v243, v229, v228, s29
	v_perm_b32 v244, v231, v230, s29
	v_perm_b32 v245, v233, v232, s29
	s_nop 0
	global_store_dwordx4 v108, v[242:245], s[6:7]
	ds_read_b32 v226, v115
	ds_read_b32 v227, v115 offset:512
	ds_read_b32 v228, v115 offset:1024
	ds_read_b32 v229, v115 offset:1536
	ds_read_b32 v230, v115 offset:2048
	ds_read_b32 v231, v115 offset:2560
	ds_read_b32 v232, v115 offset:3072
	ds_read_b32 v233, v115 offset:3584
	s_waitcnt lgkmcnt(0)
	v_bfe_u32 v120, v226, 16, 1
	v_bfe_u32 v121, v227, 16, 1
	v_bfe_u32 v122, v228, 16, 1
	v_bfe_u32 v123, v229, 16, 1
	v_bfe_u32 v124, v230, 16, 1
	v_bfe_u32 v125, v231, 16, 1
	v_bfe_u32 v126, v232, 16, 1
	v_bfe_u32 v127, v233, 16, 1
	v_add3_u32 v226, v226, v120, s28
	v_add3_u32 v227, v227, v121, s28
	v_add3_u32 v228, v228, v122, s28
	v_add3_u32 v229, v229, v123, s28
	v_add3_u32 v230, v230, v124, s28
	v_add3_u32 v231, v231, v125, s28
	v_add3_u32 v232, v232, v126, s28
	v_add3_u32 v233, v233, v127, s28
	v_perm_b32 v242, v227, v226, s29
	v_perm_b32 v243, v229, v228, s29
	v_perm_b32 v244, v231, v230, s29
	v_perm_b32 v245, v233, v232, s29
	s_nop 0
	global_store_dwordx4 v109, v[242:245], s[6:7]
	ds_read_b32 v226, v117
	ds_read_b32 v227, v117 offset:512
	ds_read_b32 v228, v117 offset:1024
	ds_read_b32 v229, v117 offset:1536
	ds_read_b32 v230, v117 offset:2048
	ds_read_b32 v231, v117 offset:2560
	ds_read_b32 v232, v117 offset:3072
	ds_read_b32 v233, v117 offset:3584
	s_waitcnt lgkmcnt(0)
	v_bfe_u32 v120, v226, 16, 1
	v_bfe_u32 v121, v227, 16, 1
	v_bfe_u32 v122, v228, 16, 1
	v_bfe_u32 v123, v229, 16, 1
	v_bfe_u32 v124, v230, 16, 1
	v_bfe_u32 v125, v231, 16, 1
	v_bfe_u32 v126, v232, 16, 1
	v_bfe_u32 v127, v233, 16, 1
	v_add3_u32 v226, v226, v120, s28
	v_add3_u32 v227, v227, v121, s28
	v_add3_u32 v228, v228, v122, s28
	v_add3_u32 v229, v229, v123, s28
	v_add3_u32 v230, v230, v124, s28
	v_add3_u32 v231, v231, v125, s28
	v_add3_u32 v232, v232, v126, s28
	v_add3_u32 v233, v233, v127, s28
	v_perm_b32 v242, v227, v226, s29
	v_perm_b32 v243, v229, v228, s29
	v_perm_b32 v244, v231, v230, s29
	v_perm_b32 v245, v233, v232, s29
	s_nop 0
	global_store_dwordx4 v110, v[242:245], s[6:7]
	ds_read_b32 v226, v119
	ds_read_b32 v227, v119 offset:512
	ds_read_b32 v228, v119 offset:1024
	ds_read_b32 v229, v119 offset:1536
	ds_read_b32 v230, v119 offset:2048
	ds_read_b32 v231, v119 offset:2560
	ds_read_b32 v232, v119 offset:3072
	ds_read_b32 v233, v119 offset:3584
	s_waitcnt lgkmcnt(0)
	v_bfe_u32 v120, v226, 16, 1
	v_bfe_u32 v121, v227, 16, 1
	v_bfe_u32 v122, v228, 16, 1
	v_bfe_u32 v123, v229, 16, 1
	v_bfe_u32 v124, v230, 16, 1
	v_bfe_u32 v125, v231, 16, 1
	v_bfe_u32 v126, v232, 16, 1
	v_bfe_u32 v127, v233, 16, 1
	v_add3_u32 v226, v226, v120, s28
	v_add3_u32 v227, v227, v121, s28
	v_add3_u32 v228, v228, v122, s28
	v_add3_u32 v229, v229, v123, s28
	v_add3_u32 v230, v230, v124, s28
	v_add3_u32 v231, v231, v125, s28
	v_add3_u32 v232, v232, v126, s28
	v_add3_u32 v233, v233, v127, s28
	v_perm_b32 v242, v227, v226, s29
	v_perm_b32 v243, v229, v228, s29
	v_perm_b32 v244, v231, v230, s29
	v_perm_b32 v245, v233, v232, s29
	s_nop 0
	global_store_dwordx4 v111, v[242:245], s[6:7]
	s_add_i32 s26, s23, 80
	s_add_i32 s27, s23, 96
	s_waitcnt vmcnt(8)
	v_mul_f32_e32 v144, v218, v144
	v_mul_f32_e32 v145, v218, v145
	v_mul_f32_e32 v146, v218, v146
	v_mul_f32_e32 v147, v218, v147
	ds_write_b128 v209, v[144:147]
	v_mul_f32_e32 v148, v219, v148
	v_mul_f32_e32 v149, v219, v149
	v_mul_f32_e32 v150, v219, v150
	v_mul_f32_e32 v151, v219, v151
	ds_write_b128 v209, v[148:151] offset:1024
	v_mul_f32_e32 v152, v220, v152
	v_mul_f32_e32 v153, v220, v153
	v_mul_f32_e32 v154, v220, v154
	v_mul_f32_e32 v155, v220, v155
	ds_write_b128 v209, v[152:155] offset:2048
	v_mul_f32_e32 v156, v221, v156
	v_mul_f32_e32 v157, v221, v157
	v_mul_f32_e32 v158, v221, v158
	v_mul_f32_e32 v159, v221, v159
	ds_write_b128 v209, v[156:159] offset:3072
	v_mul_f32_e32 v160, v222, v160
	v_mul_f32_e32 v161, v222, v161
	v_mul_f32_e32 v162, v222, v162
	v_mul_f32_e32 v163, v222, v163
	ds_write_b128 v209, v[160:163] offset:4096
	v_mul_f32_e32 v164, v223, v164
	v_mul_f32_e32 v165, v223, v165
	v_mul_f32_e32 v166, v223, v166
	v_mul_f32_e32 v167, v223, v167
	ds_write_b128 v209, v[164:167] offset:5120
	v_mul_f32_e32 v168, v224, v168
	v_mul_f32_e32 v169, v224, v169
	v_mul_f32_e32 v170, v224, v170
	v_mul_f32_e32 v171, v224, v171
	ds_write_b128 v209, v[168:171] offset:6144
	v_mul_f32_e32 v172, v225, v172
	v_mul_f32_e32 v173, v225, v173
	v_mul_f32_e32 v174, v225, v174
	v_mul_f32_e32 v175, v225, v175
	ds_write_b128 v209, v[172:175] offset:7168
	s_waitcnt lgkmcnt(0)
	s_barrier
; #define GAS __attribute__((address_space(1)))
; #define LAS __attribute__((address_space(3)))
; #define LDS_WAIT() asm volatile("s_waitcnt lgkmcnt(0)" ::: "memory")
; __device__ __forceinline__ unsigned pk2(float lo, float hi) { return f2bf(lo) | (f2bf(hi) << 16); }
; template <int MAP, bool KS, bool KPERM = false>
; __device__ __forceinline__ void p0_transpose_item(const float* W, int K, int Nsrc, int nblk, bf16* WT, const float* ksA, const float* ksB, int ksplit, LAS float* scr, int item, int lane) {
;     ...
;     for (int i = 0; i < 32; ++i) { const int kk = 2 * i + (lane >> 5); const int k = k0 + kk;
;         if (KS) v[i] *= (k < ksplit ? ksA[k] : ksB[k - ksplit]);
;         scr[kk * 33 + (lane & 31)] = v[i]; }
;     LDS_WAIT(); asm volatile("" ::: "memory");
;     const int c = lane & 7;
; #pragma unroll
;     for (int j = 0; j < 4; ++j) { const int n = (lane >> 3) + 8 * j; const LAS float* s = scr + (8 * c) * 33 + n;
;         v4u o; o.x = pk2(s[0 * 33], s[1 * 33]); o.y = pk2(s[2 * 33], s[3 * 33]); o.z = pk2(s[4 * 33], s[5 * 33]); o.w = pk2(s[6 * 33], s[7 * 33]);
;         *(GAS v4u*)(WT + (size_t)(n0 + n) * K + k0 + 8 * c) = o; }
;     LDS_WAIT(); asm volatile("" ::: "memory");
	s_mul_i32 s20, s26, 0x100000
	s_add_u32 s6, s18, s20
	s_addc_u32 s7, s19, 0
	s_cmp_lt_u32 s26, 16
	s_cselect_b32 s20, 1, 0
	s_sub_i32 s21, s26, 16
	s_bitcmp0_b32 s21, 2
	s_cselect_b32 s21, 1, 0
	s_cmp_lt_u32 s26, 40
	s_cselect_b32 s21, s21, 0
	s_or_b32 s20, s20, s21
	s_cmp_lg_u32 s20, 0
	s_cselect_b64 s[20:21], -1, 0
	v_cndmask_b32_e64 v108, v100, v104, s[20:21]
	v_cndmask_b32_e64 v109, v101, v105, s[20:21]
	v_cndmask_b32_e64 v110, v102, v106, s[20:21]
	v_cndmask_b32_e64 v111, v103, v107, s[20:21]
	ds_read_b32 v226, v112
	ds_read_b32 v227, v112 offset:512
	ds_read_b32 v228, v112 offset:1024
	ds_read_b32 v229, v112 offset:1536
	ds_read_b32 v230, v112 offset:2048
	ds_read_b32 v231, v112 offset:2560
	ds_read_b32 v232, v112 offset:3072
	ds_read_b32 v233, v112 offset:3584
	s_waitcnt lgkmcnt(0)
	v_bfe_u32 v120, v226, 16, 1
	v_bfe_u32 v121, v227, 16, 1
	v_bfe_u32 v122, v228, 16, 1
	v_bfe_u32 v123, v229, 16, 1
	v_bfe_u32 v124, v230, 16, 1
	v_bfe_u32 v125, v231, 16, 1
	v_bfe_u32 v126, v232, 16, 1
	v_bfe_u32 v127, v233, 16, 1
	v_add3_u32 v226, v226, v120, s28
	v_add3_u32 v227, v227, v121, s28
	v_add3_u32 v228, v228, v122, s28
	v_add3_u32 v229, v229, v123, s28
	v_add3_u32 v230, v230, v124, s28
	v_add3_u32 v231, v231, v125, s28
	v_add3_u32 v232, v232, v126, s28
	v_add3_u32 v233, v233, v127, s28
	v_perm_b32 v242, v227, v226, s29
	v_perm_b32 v243, v229, v228, s29
	v_perm_b32 v244, v231, v230, s29
	v_perm_b32 v245, v233, v232, s29
	s_nop 0
	global_store_dwordx4 v108, v[242:245], s[6:7]
	ds_read_b32 v226, v114
	ds_read_b32 v227, v114 offset:512
	ds_read_b32 v228, v114 offset:1024
	ds_read_b32 v229, v114 offset:1536
	ds_read_b32 v230, v114 offset:2048
	ds_read_b32 v231, v114 offset:2560
	ds_read_b32 v232, v114 offset:3072
	ds_read_b32 v233, v114 offset:3584
	s_waitcnt lgkmcnt(0)
	v_bfe_u32 v120, v226, 16, 1
	v_bfe_u32 v121, v227, 16, 1
	v_bfe_u32 v122, v228, 16, 1
	v_bfe_u32 v123, v229, 16, 1
	v_bfe_u32 v124, v230, 16, 1
	v_bfe_u32 v125, v231, 16, 1
	v_bfe_u32 v126, v232, 16, 1
	v_bfe_u32 v127, v233, 16, 1
	v_add3_u32 v226, v226, v120, s28
	v_add3_u32 v227, v227, v121, s28
	v_add3_u32 v228, v228, v122, s28
	v_add3_u32 v229, v229, v123, s28
	v_add3_u32 v230, v230, v124, s28
	v_add3_u32 v231, v231, v125, s28
	v_add3_u32 v232, v232, v126, s28
	v_add3_u32 v233, v233, v127, s28
	v_perm_b32 v242, v227, v226, s29
	v_perm_b32 v243, v229, v228, s29
	v_perm_b32 v244, v231, v230, s29
	v_perm_b32 v245, v233, v232, s29
	s_nop 0
	global_store_dwordx4 v109, v[242:245], s[6:7]
	ds_read_b32 v226, v116
	ds_read_b32 v227, v116 offset:512
	ds_read_b32 v228, v116 offset:1024
	ds_read_b32 v229, v116 offset:1536
	ds_read_b32 v230, v116 offset:2048
	ds_read_b32 v231, v116 offset:2560
	ds_read_b32 v232, v116 offset:3072
	ds_read_b32 v233, v116 offset:3584
	s_waitcnt lgkmcnt(0)
	v_bfe_u32 v120, v226, 16, 1
	v_bfe_u32 v121, v227, 16, 1
	v_bfe_u32 v122, v228, 16, 1
	v_bfe_u32 v123, v229, 16, 1
	v_bfe_u32 v124, v230, 16, 1
	v_bfe_u32 v125, v231, 16, 1
	v_bfe_u32 v126, v232, 16, 1
	v_bfe_u32 v127, v233, 16, 1
	v_add3_u32 v226, v226, v120, s28
	v_add3_u32 v227, v227, v121, s28
	v_add3_u32 v228, v228, v122, s28
	v_add3_u32 v229, v229, v123, s28
	v_add3_u32 v230, v230, v124, s28
	v_add3_u32 v231, v231, v125, s28
	v_add3_u32 v232, v232, v126, s28
	v_add3_u32 v233, v233, v127, s28
	v_perm_b32 v242, v227, v226, s29
	v_perm_b32 v243, v229, v228, s29
	v_perm_b32 v244, v231, v230, s29
	v_perm_b32 v245, v233, v232, s29
	s_nop 0
	global_store_dwordx4 v110, v[242:245], s[6:7]
	ds_read_b32 v226, v118
	ds_read_b32 v227, v118 offset:512
	ds_read_b32 v228, v118 offset:1024
	ds_read_b32 v229, v118 offset:1536
	ds_read_b32 v230, v118 offset:2048
	ds_read_b32 v231, v118 offset:2560
	ds_read_b32 v232, v118 offset:3072
	ds_read_b32 v233, v118 offset:3584
	s_waitcnt lgkmcnt(0)
	v_bfe_u32 v120, v226, 16, 1
	v_bfe_u32 v121, v227, 16, 1
	v_bfe_u32 v122, v228, 16, 1
	v_bfe_u32 v123, v229, 16, 1
	v_bfe_u32 v124, v230, 16, 1
	v_bfe_u32 v125, v231, 16, 1
	v_bfe_u32 v126, v232, 16, 1
	v_bfe_u32 v127, v233, 16, 1
	v_add3_u32 v226, v226, v120, s28
	v_add3_u32 v227, v227, v121, s28
	v_add3_u32 v228, v228, v122, s28
	v_add3_u32 v229, v229, v123, s28
	v_add3_u32 v230, v230, v124, s28
	v_add3_u32 v231, v231, v125, s28
	v_add3_u32 v232, v232, v126, s28
	v_add3_u32 v233, v233, v127, s28
	v_perm_b32 v242, v227, v226, s29
	v_perm_b32 v243, v229, v228, s29
	v_perm_b32 v244, v231, v230, s29
	v_perm_b32 v245, v233, v232, s29
	s_nop 0
	global_store_dwordx4 v111, v[242:245], s[6:7]
	s_waitcnt lgkmcnt(0)
	s_barrier
;     const int pr = item >> 1, kb = 2 * (pr / nblk) + (item & 1), nb = pr % nblk, k0 = 64 * kb, n0 = 32 * nb;
;     const int nr = n0 + (lane & 31); const int sc = MAP == 1 ? src_col_in(nr) : nr;
;     float v[32];
; #pragma unroll
;     for (int i = 0; i < 32; ++i) v[i] = sc >= 0 ? W[(size_t)(k0 + 2 * i + (lane >> 5)) * Nsrc + sc] : 0.f;
; #pragma unroll
;     for (int i = 0; i < 32; ++i) { const int k = k0 + 2 * i + (lane >> 5); float x = v[i] * wscale; if (KS) x *= (k < ksplit ? ksA[k] : ksB[k - ksplit]); scr[(2 * i + (lane >> 5)) * 33 + (lane & 31)] = x; }
; __global__ void __launch_bounds__(NWAVES * 64, 2) hybrid_fwd(Args args) {
;     ...
;         for (int it = gw; it < DEPTH * I_L; it += NGW) {
;             const int l = it / I_L; int r = it % I_L;
;             if (r < I_IN) { if (l >= PROJ_F8_FROM) p0_transpose_item_f8<true, 1>(args.in[2] + (size_t)l * DM * NSRC, DM, NSRC, NPROJ / 32, (unsigned char*)(ws + WS_WIN + l * SZ_WIN), WUP8_SCALE, args.in[1] + l * DM, args.in[1] + l * DM, DM, scr, r, lane);
	v_lshrrev_b32_e32 v246, 5, v249
	v_lshl_add_u32 v246, v250, 4, v246
	v_and_b32_e32 v247, 31, v249
	v_lshlrev_b32_e32 v247, 4, v247
	s_mov_b32 s20, 0xb140
	v_mad_u32_u24 v208, v246, s20, v247
	v_lshrrev_b32_e32 v246, 3, v249
	v_lshl_add_u32 v246, v250, 4, v246
	v_and_b32_e32 v247, 7, v249
	v_lshlrev_b32_e32 v247, 4, v247
	v_lshl_add_u32 v100, v246, 12, v247
	v_and_b32_e32 v248, 63, v246
	v_lshlrev_b32_e32 v248, 1, v248
	v_lshrrev_b32_e32 v246, 6, v246
	v_or_b32_e32 v248, v248, v246
	v_lshl_add_u32 v104, v248, 12, v247
	v_lshrrev_b32_e32 v246, 3, v249
	v_lshl_add_u32 v246, v250, 4, v246
	v_add_u32_e32 v246, 8, v246
	v_and_b32_e32 v247, 7, v249
	v_lshlrev_b32_e32 v247, 4, v247
	v_lshl_add_u32 v101, v246, 12, v247
	v_and_b32_e32 v248, 63, v246
	v_lshlrev_b32_e32 v248, 1, v248
	v_lshrrev_b32_e32 v246, 6, v246
	v_or_b32_e32 v248, v248, v246
	v_lshl_add_u32 v105, v248, 12, v247
	s_lshr_b32 s22, s15, 3
	s_and_b32 s23, s15, 7
	v_readlane_b32 s16, v253, 7
	v_readlane_b32 s17, v253, 8
	v_readlane_b32 s18, v253, 41
	v_readlane_b32 s19, v253, 42
	s_add_u32 s16, s16, 0xb140000
	s_addc_u32 s17, s17, 0
	s_mul_i32 s20, s22, 0x58a000
	s_add_u32 s16, s16, s20
	s_addc_u32 s17, s17, 0
	s_add_u32 s18, s18, 0x5c00000
	s_addc_u32 s19, s19, 0
	s_lshl_b32 s20, s22, 7
	s_add_u32 s18, s18, s20
	s_addc_u32 s19, s19, 0
	v_readlane_b32 s10, v253, 5
	v_readlane_b32 s11, v253, 6
	s_lshl_b32 s20, s22, 9
	s_add_i32 s20, s20, 0x4000
	s_add_u32 s10, s10, s20
	s_addc_u32 s11, s11, 0
	s_mov_b32 s44, 0xc3e00000
	v_mov_b32_e32 v246, 0x43e00000
	s_mov_b32 s28, 0x7fff
	s_mov_b32 s29, 0x07060302
	s_mov_b32 s24, s23
	s_add_i32 s25, s23, 8
	s_lshl_b32 s20, s24, 7
	s_cmp_lt_u32 s24, 40
	s_cselect_b32 s21, 0, 0x830
	s_cmp_lt_u32 s24, 72
	s_cselect_b32 s21, s21, 0xfffff030
	s_add_i32 s20, s20, s21
	s_lshl_b32 s20, s20, 2
	s_add_u32 s8, s16, s20
	s_addc_u32 s9, s17, 0
	global_load_dwordx4 v[144:147], v208, s[8:9]
	s_add_u32 s8, s8, 0x16280
	s_addc_u32 s9, s9, 0
	global_load_dwordx4 v[148:151], v208, s[8:9]
	s_add_u32 s8, s8, 0x16280
	s_addc_u32 s9, s9, 0
	global_load_dwordx4 v[152:155], v208, s[8:9]
	s_add_u32 s8, s8, 0x16280
	s_addc_u32 s9, s9, 0
	global_load_dwordx4 v[156:159], v208, s[8:9]
	s_add_u32 s8, s8, 0x16280
	s_addc_u32 s9, s9, 0
	global_load_dwordx4 v[160:163], v208, s[8:9]
	s_add_u32 s8, s8, 0x16280
	s_addc_u32 s9, s9, 0
	global_load_dwordx4 v[164:167], v208, s[8:9]
	s_add_u32 s8, s8, 0x16280
	s_addc_u32 s9, s9, 0
	global_load_dwordx4 v[168:171], v208, s[8:9]
	s_add_u32 s8, s8, 0x16280
	s_addc_u32 s9, s9, 0
	global_load_dwordx4 v[172:175], v208, s[8:9]
	s_lshl_b32 s20, s25, 7
	s_cmp_lt_u32 s25, 40
	s_cselect_b32 s21, 0, 0x830
	s_cmp_lt_u32 s25, 72
	s_cselect_b32 s21, s21, 0xfffff030
	s_add_i32 s20, s20, s21
	s_lshl_b32 s20, s20, 2
	s_add_u32 s8, s16, s20
	s_addc_u32 s9, s17, 0
	global_load_dwordx4 v[176:179], v208, s[8:9]
	s_add_u32 s8, s8, 0x16280
	s_addc_u32 s9, s9, 0
	global_load_dwordx4 v[180:183], v208, s[8:9]
	s_add_u32 s8, s8, 0x16280
	s_addc_u32 s9, s9, 0
	global_load_dwordx4 v[184:187], v208, s[8:9]
	s_add_u32 s8, s8, 0x16280
	s_addc_u32 s9, s9, 0
	global_load_dwordx4 v[188:191], v208, s[8:9]
	s_add_u32 s8, s8, 0x16280
	s_addc_u32 s9, s9, 0
	global_load_dwordx4 v[192:195], v208, s[8:9]
	s_add_u32 s8, s8, 0x16280
	s_addc_u32 s9, s9, 0
	global_load_dwordx4 v[196:199], v208, s[8:9]
	s_add_u32 s8, s8, 0x16280
	s_addc_u32 s9, s9, 0
	global_load_dwordx4 v[200:203], v208, s[8:9]
	s_add_u32 s8, s8, 0x16280
	s_addc_u32 s9, s9, 0
	global_load_dwordx4 v[204:207], v208, s[8:9]
	global_load_dword v218, v217, s[10:11] offset:0
	global_load_dword v219, v217, s[10:11] offset:8
	global_load_dword v220, v217, s[10:11] offset:16
	global_load_dword v221, v217, s[10:11] offset:24
	global_load_dword v222, v217, s[10:11] offset:32
	global_load_dword v223, v217, s[10:11] offset:40
	global_load_dword v224, v217, s[10:11] offset:48
	global_load_dword v225, v217, s[10:11] offset:56
	s_waitcnt vmcnt(0)
	v_mul_f32_e32 v218, 0x42800000, v218
	v_mul_f32_e32 v219, 0x42800000, v219
	v_mul_f32_e32 v220, 0x42800000, v220
	v_mul_f32_e32 v221, 0x42800000, v221
	v_mul_f32_e32 v222, 0x42800000, v222
	v_mul_f32_e32 v223, 0x42800000, v223
	v_mul_f32_e32 v224, 0x42800000, v224
	v_mul_f32_e32 v225, 0x42800000, v225
	s_add_i32 s26, s23, 0
	s_add_i32 s27, s23, 16
	s_waitcnt vmcnt(8)
	v_mul_f32_e32 v144, v218, v144
	v_mul_f32_e32 v145, v218, v145
	v_mul_f32_e32 v146, v218, v146
	v_mul_f32_e32 v147, v218, v147
	ds_write_b128 v209, v[144:147]
	v_mul_f32_e32 v148, v219, v148
	v_mul_f32_e32 v149, v219, v149
	v_mul_f32_e32 v150, v219, v150
	v_mul_f32_e32 v151, v219, v151
	ds_write_b128 v209, v[148:151] offset:1024
	v_mul_f32_e32 v152, v220, v152
	v_mul_f32_e32 v153, v220, v153
	v_mul_f32_e32 v154, v220, v154
	v_mul_f32_e32 v155, v220, v155
	ds_write_b128 v209, v[152:155] offset:2048
	v_mul_f32_e32 v156, v221, v156
	v_mul_f32_e32 v157, v221, v157
	v_mul_f32_e32 v158, v221, v158
	v_mul_f32_e32 v159, v221, v159
	ds_write_b128 v209, v[156:159] offset:3072
	v_mul_f32_e32 v160, v222, v160
	v_mul_f32_e32 v161, v222, v161
	v_mul_f32_e32 v162, v222, v162
	v_mul_f32_e32 v163, v222, v163
	ds_write_b128 v209, v[160:163] offset:4096
	v_mul_f32_e32 v164, v223, v164
	v_mul_f32_e32 v165, v223, v165
	v_mul_f32_e32 v166, v223, v166
	v_mul_f32_e32 v167, v223, v167
	ds_write_b128 v209, v[164:167] offset:5120
	v_mul_f32_e32 v168, v224, v168
	v_mul_f32_e32 v169, v224, v169
	v_mul_f32_e32 v170, v224, v170
	v_mul_f32_e32 v171, v224, v171
	ds_write_b128 v209, v[168:171] offset:6144
	v_mul_f32_e32 v172, v225, v172
	v_mul_f32_e32 v173, v225, v173
	v_mul_f32_e32 v174, v225, v174
	v_mul_f32_e32 v175, v225, v175
	ds_write_b128 v209, v[172:175] offset:7168
	s_waitcnt lgkmcnt(0)
	s_barrier
; #define GAS __attribute__((address_space(1)))
; #define LAS __attribute__((address_space(3)))
; #define LDS_WAIT() asm volatile("s_waitcnt lgkmcnt(0)" ::: "memory")
;     const int pr = item >> 1, kb = 2 * (pr / nblk) + (item & 1), nb = pr % nblk, k0 = 64 * kb, n0 = 32 * nb;
;     const int nr = n0 + (lane & 31); const int sc = MAP == 1 ? src_col_in(nr) : nr;
;     float v[32];
; #pragma unroll
;     for (int i = 0; i < 32; ++i) v[i] = sc >= 0 ? W[(size_t)(k0 + 2 * i + (lane >> 5)) * Nsrc + sc] : 0.f;
; #pragma unroll
;     for (int i = 0; i < 32; ++i) { const int k = k0 + 2 * i + (lane >> 5); float x = v[i] * wscale; if (KS) x *= (k < ksplit ? ksA[k] : ksB[k - ksplit]); scr[(2 * i + (lane >> 5)) * 33 + (lane & 31)] = x; }
;     LDS_WAIT(); asm volatile("" ::: "memory");
;     const int c = lane & 7;
; #pragma unroll
;     for (int j = 0; j < 4; ++j) { const int n = (lane >> 3) + 8 * j; const LAS float* s = scr + (8 * c) * 33 + n;
;         const unsigned long long o = (unsigned long long)pg8::pk4_fp8(s[0 * 33], s[1 * 33], s[2 * 33], s[3 * 33]) | ((unsigned long long)pg8::pk4_fp8(s[4 * 33], s[5 * 33], s[6 * 33], s[7 * 33]) << 32);
;         *(GAS unsigned long long*)(WT + (size_t)(n0 + n) * K + k0 + 8 * c) = o; }
;     LDS_WAIT(); asm volatile("" ::: "memory");
	s_lshl_b32 s20, s27, 7
	s_cmp_lt_u32 s27, 40
	s_cselect_b32 s21, 0, 0x830
	s_cmp_lt_u32 s27, 72
	s_cselect_b32 s21, s21, 0xfffff030
	s_add_i32 s20, s20, s21
	s_lshl_b32 s20, s20, 2
	s_add_u32 s8, s16, s20
	s_addc_u32 s9, s17, 0
	global_load_dwordx4 v[144:147], v208, s[8:9]
	s_add_u32 s8, s8, 0x16280
	s_addc_u32 s9, s9, 0
	global_load_dwordx4 v[148:151], v208, s[8:9]
	s_add_u32 s8, s8, 0x16280
	s_addc_u32 s9, s9, 0
	global_load_dwordx4 v[152:155], v208, s[8:9]
	s_add_u32 s8, s8, 0x16280
	s_addc_u32 s9, s9, 0
	global_load_dwordx4 v[156:159], v208, s[8:9]
	s_add_u32 s8, s8, 0x16280
	s_addc_u32 s9, s9, 0
	global_load_dwordx4 v[160:163], v208, s[8:9]
	s_add_u32 s8, s8, 0x16280
	s_addc_u32 s9, s9, 0
	global_load_dwordx4 v[164:167], v208, s[8:9]
	s_add_u32 s8, s8, 0x16280
	s_addc_u32 s9, s9, 0
	global_load_dwordx4 v[168:171], v208, s[8:9]
	s_add_u32 s8, s8, 0x16280
	s_addc_u32 s9, s9, 0
	global_load_dwordx4 v[172:175], v208, s[8:9]
	s_mul_i32 s20, s26, 0x80000
	s_add_u32 s6, s18, s20
	s_addc_u32 s7, s19, 0
	s_cmp_lt_u32 s26, 16
	s_cselect_b32 s20, 1, 0
	s_sub_i32 s21, s26, 16
	s_bitcmp0_b32 s21, 2
	s_cselect_b32 s21, 1, 0
	s_cmp_lt_u32 s26, 40
	s_cselect_b32 s21, s21, 0
	s_or_b32 s20, s20, s21
	s_cmp_lg_u32 s20, 0
	s_cselect_b64 s[20:21], -1, 0
	v_cndmask_b32_e64 v108, v100, v104, s[20:21]
	v_cndmask_b32_e64 v109, v101, v105, s[20:21]
	ds_read_b32 v226, v211
	ds_read_b32 v227, v211 offset:512
	ds_read_b32 v228, v211 offset:1024
	ds_read_b32 v229, v211 offset:1536
	ds_read_b32 v230, v211 offset:2048
	ds_read_b32 v231, v211 offset:2560
	ds_read_b32 v232, v211 offset:3072
	ds_read_b32 v233, v211 offset:3584
	ds_read_b32 v234, v211 offset:4096
	ds_read_b32 v235, v211 offset:4608
	ds_read_b32 v236, v211 offset:5120
	ds_read_b32 v237, v211 offset:5632
	ds_read_b32 v238, v211 offset:6144
	ds_read_b32 v239, v211 offset:6656
	ds_read_b32 v240, v211 offset:7168
	ds_read_b32 v241, v211 offset:7680
	s_waitcnt lgkmcnt(0)
	v_max_f32_e32 v226, v226, v226
	v_max_f32_e32 v227, v227, v227
	v_max_f32_e32 v228, v228, v228
	v_max_f32_e32 v229, v229, v229
	v_max_f32_e32 v230, v230, v230
	v_max_f32_e32 v231, v231, v231
	v_max_f32_e32 v232, v232, v232
	v_max_f32_e32 v233, v233, v233
	v_max_f32_e32 v234, v234, v234
	v_max_f32_e32 v235, v235, v235
	v_max_f32_e32 v236, v236, v236
	v_max_f32_e32 v237, v237, v237
	v_max_f32_e32 v238, v238, v238
	v_max_f32_e32 v239, v239, v239
	v_max_f32_e32 v240, v240, v240
	v_max_f32_e32 v241, v241, v241
	v_med3_f32 v226, v226, s44, v246
	v_med3_f32 v227, v227, s44, v246
	v_med3_f32 v228, v228, s44, v246
	v_med3_f32 v229, v229, s44, v246
	v_med3_f32 v230, v230, s44, v246
	v_med3_f32 v231, v231, s44, v246
	v_med3_f32 v232, v232, s44, v246
	v_med3_f32 v233, v233, s44, v246
	v_med3_f32 v234, v234, s44, v246
	v_med3_f32 v235, v235, s44, v246
	v_med3_f32 v236, v236, s44, v246
	v_med3_f32 v237, v237, s44, v246
	v_med3_f32 v238, v238, s44, v246
	v_med3_f32 v239, v239, s44, v246
	v_med3_f32 v240, v240, s44, v246
	v_med3_f32 v241, v241, s44, v246
	v_mov_b32_e32 v242, 0
	v_mov_b32_e32 v243, 0
	v_mov_b32_e32 v244, 0
	v_mov_b32_e32 v245, 0
	v_cvt_pk_fp8_f32 v242, v226, v227
	v_cvt_pk_fp8_f32 v243, v230, v231
	v_cvt_pk_fp8_f32 v244, v234, v235
	v_cvt_pk_fp8_f32 v245, v238, v239
	v_cvt_pk_fp8_f32 v242, v228, v229 op_sel:[0,0,1]
	v_cvt_pk_fp8_f32 v243, v232, v233 op_sel:[0,0,1]
	v_cvt_pk_fp8_f32 v244, v236, v237 op_sel:[0,0,1]
	v_cvt_pk_fp8_f32 v245, v240, v241 op_sel:[0,0,1]
	s_nop 0
	global_store_dwordx4 v108, v[242:245], s[6:7]
	ds_read_b32 v226, v213
	ds_read_b32 v227, v213 offset:512
	ds_read_b32 v228, v213 offset:1024
	ds_read_b32 v229, v213 offset:1536
	ds_read_b32 v230, v213 offset:2048
	ds_read_b32 v231, v213 offset:2560
	ds_read_b32 v232, v213 offset:3072
	ds_read_b32 v233, v213 offset:3584
	ds_read_b32 v234, v213 offset:4096
	ds_read_b32 v235, v213 offset:4608
	ds_read_b32 v236, v213 offset:5120
	ds_read_b32 v237, v213 offset:5632
	ds_read_b32 v238, v213 offset:6144
	ds_read_b32 v239, v213 offset:6656
	ds_read_b32 v240, v213 offset:7168
	ds_read_b32 v241, v213 offset:7680
	s_waitcnt lgkmcnt(0)
	v_max_f32_e32 v226, v226, v226
	v_max_f32_e32 v227, v227, v227
	v_max_f32_e32 v228, v228, v228
	v_max_f32_e32 v229, v229, v229
	v_max_f32_e32 v230, v230, v230
	v_max_f32_e32 v231, v231, v231
	v_max_f32_e32 v232, v232, v232
	v_max_f32_e32 v233, v233, v233
	v_max_f32_e32 v234, v234, v234
	v_max_f32_e32 v235, v235, v235
	v_max_f32_e32 v236, v236, v236
	v_max_f32_e32 v237, v237, v237
	v_max_f32_e32 v238, v238, v238
	v_max_f32_e32 v239, v239, v239
	v_max_f32_e32 v240, v240, v240
	v_max_f32_e32 v241, v241, v241
	v_med3_f32 v226, v226, s44, v246
	v_med3_f32 v227, v227, s44, v246
	v_med3_f32 v228, v228, s44, v246
	v_med3_f32 v229, v229, s44, v246
	v_med3_f32 v230, v230, s44, v246
	v_med3_f32 v231, v231, s44, v246
	v_med3_f32 v232, v232, s44, v246
	v_med3_f32 v233, v233, s44, v246
	v_med3_f32 v234, v234, s44, v246
	v_med3_f32 v235, v235, s44, v246
	v_med3_f32 v236, v236, s44, v246
	v_med3_f32 v237, v237, s44, v246
	v_med3_f32 v238, v238, s44, v246
	v_med3_f32 v239, v239, s44, v246
	v_med3_f32 v240, v240, s44, v246
	v_med3_f32 v241, v241, s44, v246
	v_mov_b32_e32 v242, 0
	v_mov_b32_e32 v243, 0
	v_mov_b32_e32 v244, 0
	v_mov_b32_e32 v245, 0
	v_cvt_pk_fp8_f32 v242, v226, v227
	v_cvt_pk_fp8_f32 v243, v230, v231
	v_cvt_pk_fp8_f32 v244, v234, v235
	v_cvt_pk_fp8_f32 v245, v238, v239
	v_cvt_pk_fp8_f32 v242, v228, v229 op_sel:[0,0,1]
	v_cvt_pk_fp8_f32 v243, v232, v233 op_sel:[0,0,1]
	v_cvt_pk_fp8_f32 v244, v236, v237 op_sel:[0,0,1]
	v_cvt_pk_fp8_f32 v245, v240, v241 op_sel:[0,0,1]
	s_nop 0
	global_store_dwordx4 v109, v[242:245], s[6:7]
	s_add_i32 s26, s23, 8
	s_add_i32 s27, s23, 24
	s_waitcnt vmcnt(10)
; #define GAS __attribute__((address_space(1)))
; #define LAS __attribute__((address_space(3)))
; #define LDS_WAIT() asm volatile("s_waitcnt lgkmcnt(0)" ::: "memory")
;     const int pr = item >> 1, kb = 2 * (pr / nblk) + (item & 1), nb = pr % nblk, k0 = 64 * kb, n0 = 32 * nb;
;     const int nr = n0 + (lane & 31); const int sc = MAP == 1 ? src_col_in(nr) : nr;
;     float v[32];
; #pragma unroll
;     for (int i = 0; i < 32; ++i) v[i] = sc >= 0 ? W[(size_t)(k0 + 2 * i + (lane >> 5)) * Nsrc + sc] : 0.f;
; #pragma unroll
;     for (int i = 0; i < 32; ++i) { const int k = k0 + 2 * i + (lane >> 5); float x = v[i] * wscale; if (KS) x *= (k < ksplit ? ksA[k] : ksB[k - ksplit]); scr[(2 * i + (lane >> 5)) * 33 + (lane & 31)] = x; }
;     LDS_WAIT(); asm volatile("" ::: "memory");
;     const int c = lane & 7;
; #pragma unroll
;     for (int j = 0; j < 4; ++j) { const int n = (lane >> 3) + 8 * j; const LAS float* s = scr + (8 * c) * 33 + n;
;         const unsigned long long o = (unsigned long long)pg8::pk4_fp8(s[0 * 33], s[1 * 33], s[2 * 33], s[3 * 33]) | ((unsigned long long)pg8::pk4_fp8(s[4 * 33], s[5 * 33], s[6 * 33], s[7 * 33]) << 32);
;         *(GAS unsigned long long*)(WT + (size_t)(n0 + n) * K + k0 + 8 * c) = o; }
;     LDS_WAIT(); asm volatile("" ::: "memory");
	v_mul_f32_e32 v176, v218, v176
	v_mul_f32_e32 v177, v218, v177
	v_mul_f32_e32 v178, v218, v178
	v_mul_f32_e32 v179, v218, v179
	ds_write_b128 v210, v[176:179]
	v_mul_f32_e32 v180, v219, v180
	v_mul_f32_e32 v181, v219, v181
	v_mul_f32_e32 v182, v219, v182
	v_mul_f32_e32 v183, v219, v183
	ds_write_b128 v210, v[180:183] offset:1024
	v_mul_f32_e32 v184, v220, v184
	v_mul_f32_e32 v185, v220, v185
	v_mul_f32_e32 v186, v220, v186
	v_mul_f32_e32 v187, v220, v187
	ds_write_b128 v210, v[184:187] offset:2048
	v_mul_f32_e32 v188, v221, v188
	v_mul_f32_e32 v189, v221, v189
	v_mul_f32_e32 v190, v221, v190
	v_mul_f32_e32 v191, v221, v191
	ds_write_b128 v210, v[188:191] offset:3072
	v_mul_f32_e32 v192, v222, v192
	v_mul_f32_e32 v193, v222, v193
	v_mul_f32_e32 v194, v222, v194
	v_mul_f32_e32 v195, v222, v195
	ds_write_b128 v210, v[192:195] offset:4096
	v_mul_f32_e32 v196, v223, v196
	v_mul_f32_e32 v197, v223, v197
	v_mul_f32_e32 v198, v223, v198
	v_mul_f32_e32 v199, v223, v199
	ds_write_b128 v210, v[196:199] offset:5120
	v_mul_f32_e32 v200, v224, v200
	v_mul_f32_e32 v201, v224, v201
	v_mul_f32_e32 v202, v224, v202
	v_mul_f32_e32 v203, v224, v203
	ds_write_b128 v210, v[200:203] offset:6144
	v_mul_f32_e32 v204, v225, v204
	v_mul_f32_e32 v205, v225, v205
	v_mul_f32_e32 v206, v225, v206
	v_mul_f32_e32 v207, v225, v207
	ds_write_b128 v210, v[204:207] offset:7168
	s_waitcnt lgkmcnt(0)
	s_barrier
	s_lshl_b32 s20, s27, 7
	s_cmp_lt_u32 s27, 40
	s_cselect_b32 s21, 0, 0x830
	s_cmp_lt_u32 s27, 72
	s_cselect_b32 s21, s21, 0xfffff030
	s_add_i32 s20, s20, s21
	s_lshl_b32 s20, s20, 2
	s_add_u32 s8, s16, s20
	s_addc_u32 s9, s17, 0
	global_load_dwordx4 v[176:179], v208, s[8:9]
	s_add_u32 s8, s8, 0x16280
	s_addc_u32 s9, s9, 0
	global_load_dwordx4 v[180:183], v208, s[8:9]
	s_add_u32 s8, s8, 0x16280
	s_addc_u32 s9, s9, 0
	global_load_dwordx4 v[184:187], v208, s[8:9]
	s_add_u32 s8, s8, 0x16280
	s_addc_u32 s9, s9, 0
	global_load_dwordx4 v[188:191], v208, s[8:9]
	s_add_u32 s8, s8, 0x16280
	s_addc_u32 s9, s9, 0
	global_load_dwordx4 v[192:195], v208, s[8:9]
	s_add_u32 s8, s8, 0x16280
	s_addc_u32 s9, s9, 0
	global_load_dwordx4 v[196:199], v208, s[8:9]
	s_add_u32 s8, s8, 0x16280
	s_addc_u32 s9, s9, 0
	global_load_dwordx4 v[200:203], v208, s[8:9]
	s_add_u32 s8, s8, 0x16280
	s_addc_u32 s9, s9, 0
	global_load_dwordx4 v[204:207], v208, s[8:9]
	s_mul_i32 s20, s26, 0x80000
	s_add_u32 s6, s18, s20
	s_addc_u32 s7, s19, 0
	s_cmp_lt_u32 s26, 16
	s_cselect_b32 s20, 1, 0
	s_sub_i32 s21, s26, 16
	s_bitcmp0_b32 s21, 2
	s_cselect_b32 s21, 1, 0
	s_cmp_lt_u32 s26, 40
	s_cselect_b32 s21, s21, 0
	s_or_b32 s20, s20, s21
	s_cmp_lg_u32 s20, 0
	s_cselect_b64 s[20:21], -1, 0
	v_cndmask_b32_e64 v108, v100, v104, s[20:21]
	v_cndmask_b32_e64 v109, v101, v105, s[20:21]
	ds_read_b32 v226, v212
	ds_read_b32 v227, v212 offset:512
	ds_read_b32 v228, v212 offset:1024
	ds_read_b32 v229, v212 offset:1536
	ds_read_b32 v230, v212 offset:2048
	ds_read_b32 v231, v212 offset:2560
	ds_read_b32 v232, v212 offset:3072
	ds_read_b32 v233, v212 offset:3584
	ds_read_b32 v234, v212 offset:4096
	ds_read_b32 v235, v212 offset:4608
	ds_read_b32 v236, v212 offset:5120
	ds_read_b32 v237, v212 offset:5632
	ds_read_b32 v238, v212 offset:6144
	ds_read_b32 v239, v212 offset:6656
	ds_read_b32 v240, v212 offset:7168
	ds_read_b32 v241, v212 offset:7680
	s_waitcnt lgkmcnt(0)
	v_max_f32_e32 v226, v226, v226
	v_max_f32_e32 v227, v227, v227
	v_max_f32_e32 v228, v228, v228
	v_max_f32_e32 v229, v229, v229
	v_max_f32_e32 v230, v230, v230
	v_max_f32_e32 v231, v231, v231
	v_max_f32_e32 v232, v232, v232
	v_max_f32_e32 v233, v233, v233
	v_max_f32_e32 v234, v234, v234
	v_max_f32_e32 v235, v235, v235
	v_max_f32_e32 v236, v236, v236
	v_max_f32_e32 v237, v237, v237
	v_max_f32_e32 v238, v238, v238
	v_max_f32_e32 v239, v239, v239
	v_max_f32_e32 v240, v240, v240
	v_max_f32_e32 v241, v241, v241
	v_med3_f32 v226, v226, s44, v246
	v_med3_f32 v227, v227, s44, v246
	v_med3_f32 v228, v228, s44, v246
	v_med3_f32 v229, v229, s44, v246
	v_med3_f32 v230, v230, s44, v246
	v_med3_f32 v231, v231, s44, v246
	v_med3_f32 v232, v232, s44, v246
	v_med3_f32 v233, v233, s44, v246
	v_med3_f32 v234, v234, s44, v246
	v_med3_f32 v235, v235, s44, v246
	v_med3_f32 v236, v236, s44, v246
	v_med3_f32 v237, v237, s44, v246
	v_med3_f32 v238, v238, s44, v246
	v_med3_f32 v239, v239, s44, v246
	v_med3_f32 v240, v240, s44, v246
	v_med3_f32 v241, v241, s44, v246
	v_mov_b32_e32 v242, 0
	v_mov_b32_e32 v243, 0
	v_mov_b32_e32 v244, 0
	v_mov_b32_e32 v245, 0
	v_cvt_pk_fp8_f32 v242, v226, v227
	v_cvt_pk_fp8_f32 v243, v230, v231
	v_cvt_pk_fp8_f32 v244, v234, v235
	v_cvt_pk_fp8_f32 v245, v238, v239
	v_cvt_pk_fp8_f32 v242, v228, v229 op_sel:[0,0,1]
	v_cvt_pk_fp8_f32 v243, v232, v233 op_sel:[0,0,1]
	v_cvt_pk_fp8_f32 v244, v236, v237 op_sel:[0,0,1]
	v_cvt_pk_fp8_f32 v245, v240, v241 op_sel:[0,0,1]
	s_nop 0
	global_store_dwordx4 v108, v[242:245], s[6:7]
	ds_read_b32 v226, v214
	ds_read_b32 v227, v214 offset:512
	ds_read_b32 v228, v214 offset:1024
	ds_read_b32 v229, v214 offset:1536
	ds_read_b32 v230, v214 offset:2048
	ds_read_b32 v231, v214 offset:2560
	ds_read_b32 v232, v214 offset:3072
	ds_read_b32 v233, v214 offset:3584
	ds_read_b32 v234, v214 offset:4096
	ds_read_b32 v235, v214 offset:4608
	ds_read_b32 v236, v214 offset:5120
	ds_read_b32 v237, v214 offset:5632
	ds_read_b32 v238, v214 offset:6144
	ds_read_b32 v239, v214 offset:6656
	ds_read_b32 v240, v214 offset:7168
	ds_read_b32 v241, v214 offset:7680
	s_waitcnt lgkmcnt(0)
; #define GAS __attribute__((address_space(1)))
; #define LAS __attribute__((address_space(3)))
; #define LDS_WAIT() asm volatile("s_waitcnt lgkmcnt(0)" ::: "memory")
;     const int pr = item >> 1, kb = 2 * (pr / nblk) + (item & 1), nb = pr % nblk, k0 = 64 * kb, n0 = 32 * nb;
;     const int nr = n0 + (lane & 31); const int sc = MAP == 1 ? src_col_in(nr) : nr;
;     float v[32];
; #pragma unroll
;     for (int i = 0; i < 32; ++i) v[i] = sc >= 0 ? W[(size_t)(k0 + 2 * i + (lane >> 5)) * Nsrc + sc] : 0.f;
; #pragma unroll
;     for (int i = 0; i < 32; ++i) { const int k = k0 + 2 * i + (lane >> 5); float x = v[i] * wscale; if (KS) x *= (k < ksplit ? ksA[k] : ksB[k - ksplit]); scr[(2 * i + (lane >> 5)) * 33 + (lane & 31)] = x; }
;     LDS_WAIT(); asm volatile("" ::: "memory");
;     const int c = lane & 7;
; #pragma unroll
;     for (int j = 0; j < 4; ++j) { const int n = (lane >> 3) + 8 * j; const LAS float* s = scr + (8 * c) * 33 + n;
;         const unsigned long long o = (unsigned long long)pg8::pk4_fp8(s[0 * 33], s[1 * 33], s[2 * 33], s[3 * 33]) | ((unsigned long long)pg8::pk4_fp8(s[4 * 33], s[5 * 33], s[6 * 33], s[7 * 33]) << 32);
;         *(GAS unsigned long long*)(WT + (size_t)(n0 + n) * K + k0 + 8 * c) = o; }
;     LDS_WAIT(); asm volatile("" ::: "memory");
	v_max_f32_e32 v226, v226, v226
	v_max_f32_e32 v227, v227, v227
	v_max_f32_e32 v228, v228, v228
	v_max_f32_e32 v229, v229, v229
	v_max_f32_e32 v230, v230, v230
	v_max_f32_e32 v231, v231, v231
	v_max_f32_e32 v232, v232, v232
	v_max_f32_e32 v233, v233, v233
	v_max_f32_e32 v234, v234, v234
	v_max_f32_e32 v235, v235, v235
	v_max_f32_e32 v236, v236, v236
	v_max_f32_e32 v237, v237, v237
	v_max_f32_e32 v238, v238, v238
	v_max_f32_e32 v239, v239, v239
	v_max_f32_e32 v240, v240, v240
	v_max_f32_e32 v241, v241, v241
	v_med3_f32 v226, v226, s44, v246
	v_med3_f32 v227, v227, s44, v246
	v_med3_f32 v228, v228, s44, v246
	v_med3_f32 v229, v229, s44, v246
	v_med3_f32 v230, v230, s44, v246
	v_med3_f32 v231, v231, s44, v246
	v_med3_f32 v232, v232, s44, v246
	v_med3_f32 v233, v233, s44, v246
	v_med3_f32 v234, v234, s44, v246
	v_med3_f32 v235, v235, s44, v246
	v_med3_f32 v236, v236, s44, v246
	v_med3_f32 v237, v237, s44, v246
	v_med3_f32 v238, v238, s44, v246
	v_med3_f32 v239, v239, s44, v246
	v_med3_f32 v240, v240, s44, v246
	v_med3_f32 v241, v241, s44, v246
	v_mov_b32_e32 v242, 0
	v_mov_b32_e32 v243, 0
	v_mov_b32_e32 v244, 0
	v_mov_b32_e32 v245, 0
	v_cvt_pk_fp8_f32 v242, v226, v227
	v_cvt_pk_fp8_f32 v243, v230, v231
	v_cvt_pk_fp8_f32 v244, v234, v235
	v_cvt_pk_fp8_f32 v245, v238, v239
	v_cvt_pk_fp8_f32 v242, v228, v229 op_sel:[0,0,1]
	v_cvt_pk_fp8_f32 v243, v232, v233 op_sel:[0,0,1]
	v_cvt_pk_fp8_f32 v244, v236, v237 op_sel:[0,0,1]
	v_cvt_pk_fp8_f32 v245, v240, v241 op_sel:[0,0,1]
	s_nop 0
	global_store_dwordx4 v109, v[242:245], s[6:7]
	s_add_i32 s26, s23, 16
	s_add_i32 s27, s23, 32
	s_waitcnt vmcnt(12)
	v_mul_f32_e32 v144, v218, v144
	v_mul_f32_e32 v145, v218, v145
	v_mul_f32_e32 v146, v218, v146
	v_mul_f32_e32 v147, v218, v147
	ds_write_b128 v209, v[144:147]
	v_mul_f32_e32 v148, v219, v148
	v_mul_f32_e32 v149, v219, v149
	v_mul_f32_e32 v150, v219, v150
	v_mul_f32_e32 v151, v219, v151
	ds_write_b128 v209, v[148:151] offset:1024
	v_mul_f32_e32 v152, v220, v152
	v_mul_f32_e32 v153, v220, v153
	v_mul_f32_e32 v154, v220, v154
	v_mul_f32_e32 v155, v220, v155
	ds_write_b128 v209, v[152:155] offset:2048
	v_mul_f32_e32 v156, v221, v156
	v_mul_f32_e32 v157, v221, v157
	v_mul_f32_e32 v158, v221, v158
	v_mul_f32_e32 v159, v221, v159
	ds_write_b128 v209, v[156:159] offset:3072
	v_mul_f32_e32 v160, v222, v160
	v_mul_f32_e32 v161, v222, v161
	v_mul_f32_e32 v162, v222, v162
	v_mul_f32_e32 v163, v222, v163
	ds_write_b128 v209, v[160:163] offset:4096
	v_mul_f32_e32 v164, v223, v164
	v_mul_f32_e32 v165, v223, v165
	v_mul_f32_e32 v166, v223, v166
	v_mul_f32_e32 v167, v223, v167
	ds_write_b128 v209, v[164:167] offset:5120
	v_mul_f32_e32 v168, v224, v168
	v_mul_f32_e32 v169, v224, v169
	v_mul_f32_e32 v170, v224, v170
	v_mul_f32_e32 v171, v224, v171
	ds_write_b128 v209, v[168:171] offset:6144
	v_mul_f32_e32 v172, v225, v172
	v_mul_f32_e32 v173, v225, v173
	v_mul_f32_e32 v174, v225, v174
	v_mul_f32_e32 v175, v225, v175
	ds_write_b128 v209, v[172:175] offset:7168
	s_waitcnt lgkmcnt(0)
	s_barrier
	s_lshl_b32 s20, s27, 7
	s_cmp_lt_u32 s27, 40
	s_cselect_b32 s21, 0, 0x830
	s_cmp_lt_u32 s27, 72
	s_cselect_b32 s21, s21, 0xfffff030
	s_add_i32 s20, s20, s21
	s_lshl_b32 s20, s20, 2
	s_add_u32 s8, s16, s20
	s_addc_u32 s9, s17, 0
	global_load_dwordx4 v[144:147], v208, s[8:9]
	s_add_u32 s8, s8, 0x16280
	s_addc_u32 s9, s9, 0
	global_load_dwordx4 v[148:151], v208, s[8:9]
	s_add_u32 s8, s8, 0x16280
	s_addc_u32 s9, s9, 0
	global_load_dwordx4 v[152:155], v208, s[8:9]
	s_add_u32 s8, s8, 0x16280
	s_addc_u32 s9, s9, 0
	global_load_dwordx4 v[156:159], v208, s[8:9]
	s_add_u32 s8, s8, 0x16280
	s_addc_u32 s9, s9, 0
	global_load_dwordx4 v[160:163], v208, s[8:9]
	s_add_u32 s8, s8, 0x16280
	s_addc_u32 s9, s9, 0
	global_load_dwordx4 v[164:167], v208, s[8:9]
	s_add_u32 s8, s8, 0x16280
	s_addc_u32 s9, s9, 0
	global_load_dwordx4 v[168:171], v208, s[8:9]
	s_add_u32 s8, s8, 0x16280
	s_addc_u32 s9, s9, 0
	global_load_dwordx4 v[172:175], v208, s[8:9]
	s_mul_i32 s20, s26, 0x80000
	s_add_u32 s6, s18, s20
	s_addc_u32 s7, s19, 0
	s_cmp_lt_u32 s26, 16
	s_cselect_b32 s20, 1, 0
	s_sub_i32 s21, s26, 16
	s_bitcmp0_b32 s21, 2
	s_cselect_b32 s21, 1, 0
	s_cmp_lt_u32 s26, 40
	s_cselect_b32 s21, s21, 0
	s_or_b32 s20, s20, s21
	s_cmp_lg_u32 s20, 0
	s_cselect_b64 s[20:21], -1, 0
	v_cndmask_b32_e64 v108, v100, v104, s[20:21]
	v_cndmask_b32_e64 v109, v101, v105, s[20:21]
	ds_read_b32 v226, v211
	ds_read_b32 v227, v211 offset:512
	ds_read_b32 v228, v211 offset:1024
	ds_read_b32 v229, v211 offset:1536
	ds_read_b32 v230, v211 offset:2048
	ds_read_b32 v231, v211 offset:2560
	ds_read_b32 v232, v211 offset:3072
	ds_read_b32 v233, v211 offset:3584
	ds_read_b32 v234, v211 offset:4096
	ds_read_b32 v235, v211 offset:4608
	ds_read_b32 v236, v211 offset:5120
	ds_read_b32 v237, v211 offset:5632
	ds_read_b32 v238, v211 offset:6144
	ds_read_b32 v239, v211 offset:6656
	ds_read_b32 v240, v211 offset:7168
	ds_read_b32 v241, v211 offset:7680
	s_waitcnt lgkmcnt(0)
; #define GAS __attribute__((address_space(1)))
; #define LAS __attribute__((address_space(3)))
; #define LDS_WAIT() asm volatile("s_waitcnt lgkmcnt(0)" ::: "memory")
;     const int pr = item >> 1, kb = 2 * (pr / nblk) + (item & 1), nb = pr % nblk, k0 = 64 * kb, n0 = 32 * nb;
;     const int nr = n0 + (lane & 31); const int sc = MAP == 1 ? src_col_in(nr) : nr;
;     float v[32];
; #pragma unroll
;     for (int i = 0; i < 32; ++i) v[i] = sc >= 0 ? W[(size_t)(k0 + 2 * i + (lane >> 5)) * Nsrc + sc] : 0.f;
; #pragma unroll
;     for (int i = 0; i < 32; ++i) { const int k = k0 + 2 * i + (lane >> 5); float x = v[i] * wscale; if (KS) x *= (k < ksplit ? ksA[k] : ksB[k - ksplit]); scr[(2 * i + (lane >> 5)) * 33 + (lane & 31)] = x; }
;     LDS_WAIT(); asm volatile("" ::: "memory");
;     const int c = lane & 7;
; #pragma unroll
;     for (int j = 0; j < 4; ++j) { const int n = (lane >> 3) + 8 * j; const LAS float* s = scr + (8 * c) * 33 + n;
;         const unsigned long long o = (unsigned long long)pg8::pk4_fp8(s[0 * 33], s[1 * 33], s[2 * 33], s[3 * 33]) | ((unsigned long long)pg8::pk4_fp8(s[4 * 33], s[5 * 33], s[6 * 33], s[7 * 33]) << 32);
;         *(GAS unsigned long long*)(WT + (size_t)(n0 + n) * K + k0 + 8 * c) = o; }
;     LDS_WAIT(); asm volatile("" ::: "memory");
	v_max_f32_e32 v226, v226, v226
	v_max_f32_e32 v227, v227, v227
	v_max_f32_e32 v228, v228, v228
	v_max_f32_e32 v229, v229, v229
	v_max_f32_e32 v230, v230, v230
	v_max_f32_e32 v231, v231, v231
	v_max_f32_e32 v232, v232, v232
	v_max_f32_e32 v233, v233, v233
	v_max_f32_e32 v234, v234, v234
	v_max_f32_e32 v235, v235, v235
	v_max_f32_e32 v236, v236, v236
	v_max_f32_e32 v237, v237, v237
	v_max_f32_e32 v238, v238, v238
	v_max_f32_e32 v239, v239, v239
	v_max_f32_e32 v240, v240, v240
	v_max_f32_e32 v241, v241, v241
	v_med3_f32 v226, v226, s44, v246
	v_med3_f32 v227, v227, s44, v246
	v_med3_f32 v228, v228, s44, v246
	v_med3_f32 v229, v229, s44, v246
	v_med3_f32 v230, v230, s44, v246
	v_med3_f32 v231, v231, s44, v246
	v_med3_f32 v232, v232, s44, v246
	v_med3_f32 v233, v233, s44, v246
	v_med3_f32 v234, v234, s44, v246
	v_med3_f32 v235, v235, s44, v246
	v_med3_f32 v236, v236, s44, v246
	v_med3_f32 v237, v237, s44, v246
	v_med3_f32 v238, v238, s44, v246
	v_med3_f32 v239, v239, s44, v246
	v_med3_f32 v240, v240, s44, v246
	v_med3_f32 v241, v241, s44, v246
	v_mov_b32_e32 v242, 0
	v_mov_b32_e32 v243, 0
	v_mov_b32_e32 v244, 0
	v_mov_b32_e32 v245, 0
	v_cvt_pk_fp8_f32 v242, v226, v227
	v_cvt_pk_fp8_f32 v243, v230, v231
	v_cvt_pk_fp8_f32 v244, v234, v235
	v_cvt_pk_fp8_f32 v245, v238, v239
	v_cvt_pk_fp8_f32 v242, v228, v229 op_sel:[0,0,1]
	v_cvt_pk_fp8_f32 v243, v232, v233 op_sel:[0,0,1]
	v_cvt_pk_fp8_f32 v244, v236, v237 op_sel:[0,0,1]
	v_cvt_pk_fp8_f32 v245, v240, v241 op_sel:[0,0,1]
	s_nop 0
	global_store_dwordx4 v108, v[242:245], s[6:7]
	ds_read_b32 v226, v213
	ds_read_b32 v227, v213 offset:512
	ds_read_b32 v228, v213 offset:1024
	ds_read_b32 v229, v213 offset:1536
	ds_read_b32 v230, v213 offset:2048
	ds_read_b32 v231, v213 offset:2560
	ds_read_b32 v232, v213 offset:3072
	ds_read_b32 v233, v213 offset:3584
	ds_read_b32 v234, v213 offset:4096
	ds_read_b32 v235, v213 offset:4608
	ds_read_b32 v236, v213 offset:5120
	ds_read_b32 v237, v213 offset:5632
	ds_read_b32 v238, v213 offset:6144
	ds_read_b32 v239, v213 offset:6656
	ds_read_b32 v240, v213 offset:7168
	ds_read_b32 v241, v213 offset:7680
	s_waitcnt lgkmcnt(0)
	v_max_f32_e32 v226, v226, v226
	v_max_f32_e32 v227, v227, v227
	v_max_f32_e32 v228, v228, v228
	v_max_f32_e32 v229, v229, v229
	v_max_f32_e32 v230, v230, v230
	v_max_f32_e32 v231, v231, v231
	v_max_f32_e32 v232, v232, v232
	v_max_f32_e32 v233, v233, v233
	v_max_f32_e32 v234, v234, v234
	v_max_f32_e32 v235, v235, v235
	v_max_f32_e32 v236, v236, v236
	v_max_f32_e32 v237, v237, v237
	v_max_f32_e32 v238, v238, v238
	v_max_f32_e32 v239, v239, v239
	v_max_f32_e32 v240, v240, v240
	v_max_f32_e32 v241, v241, v241
	v_med3_f32 v226, v226, s44, v246
	v_med3_f32 v227, v227, s44, v246
	v_med3_f32 v228, v228, s44, v246
	v_med3_f32 v229, v229, s44, v246
	v_med3_f32 v230, v230, s44, v246
	v_med3_f32 v231, v231, s44, v246
	v_med3_f32 v232, v232, s44, v246
	v_med3_f32 v233, v233, s44, v246
	v_med3_f32 v234, v234, s44, v246
	v_med3_f32 v235, v235, s44, v246
	v_med3_f32 v236, v236, s44, v246
	v_med3_f32 v237, v237, s44, v246
	v_med3_f32 v238, v238, s44, v246
	v_med3_f32 v239, v239, s44, v246
	v_med3_f32 v240, v240, s44, v246
	v_med3_f32 v241, v241, s44, v246
	v_mov_b32_e32 v242, 0
	v_mov_b32_e32 v243, 0
	v_mov_b32_e32 v244, 0
	v_mov_b32_e32 v245, 0
	v_cvt_pk_fp8_f32 v242, v226, v227
	v_cvt_pk_fp8_f32 v243, v230, v231
	v_cvt_pk_fp8_f32 v244, v234, v235
	v_cvt_pk_fp8_f32 v245, v238, v239
	v_cvt_pk_fp8_f32 v242, v228, v229 op_sel:[0,0,1]
	v_cvt_pk_fp8_f32 v243, v232, v233 op_sel:[0,0,1]
	v_cvt_pk_fp8_f32 v244, v236, v237 op_sel:[0,0,1]
	v_cvt_pk_fp8_f32 v245, v240, v241 op_sel:[0,0,1]
	s_nop 0
	global_store_dwordx4 v109, v[242:245], s[6:7]
	s_add_i32 s26, s23, 24
	s_add_i32 s27, s23, 40
	s_waitcnt vmcnt(12)
	v_mul_f32_e32 v176, v218, v176
	v_mul_f32_e32 v177, v218, v177
	v_mul_f32_e32 v178, v218, v178
	v_mul_f32_e32 v179, v218, v179
	ds_write_b128 v210, v[176:179]
	v_mul_f32_e32 v180, v219, v180
	v_mul_f32_e32 v181, v219, v181
	v_mul_f32_e32 v182, v219, v182
	v_mul_f32_e32 v183, v219, v183
	ds_write_b128 v210, v[180:183] offset:1024
	v_mul_f32_e32 v184, v220, v184
	v_mul_f32_e32 v185, v220, v185
	v_mul_f32_e32 v186, v220, v186
	v_mul_f32_e32 v187, v220, v187
	ds_write_b128 v210, v[184:187] offset:2048
	v_mul_f32_e32 v188, v221, v188
	v_mul_f32_e32 v189, v221, v189
	v_mul_f32_e32 v190, v221, v190
	v_mul_f32_e32 v191, v221, v191
	ds_write_b128 v210, v[188:191] offset:3072
	v_mul_f32_e32 v192, v222, v192
	v_mul_f32_e32 v193, v222, v193
	v_mul_f32_e32 v194, v222, v194
	v_mul_f32_e32 v195, v222, v195
	ds_write_b128 v210, v[192:195] offset:4096
	v_mul_f32_e32 v196, v223, v196
	v_mul_f32_e32 v197, v223, v197
	v_mul_f32_e32 v198, v223, v198
	v_mul_f32_e32 v199, v223, v199
	ds_write_b128 v210, v[196:199] offset:5120
	v_mul_f32_e32 v200, v224, v200
	v_mul_f32_e32 v201, v224, v201
	v_mul_f32_e32 v202, v224, v202
	v_mul_f32_e32 v203, v224, v203
	ds_write_b128 v210, v[200:203] offset:6144
	v_mul_f32_e32 v204, v225, v204
	v_mul_f32_e32 v205, v225, v205
	v_mul_f32_e32 v206, v225, v206
	v_mul_f32_e32 v207, v225, v207
	ds_write_b128 v210, v[204:207] offset:7168
	s_waitcnt lgkmcnt(0)
	s_barrier
; #define GAS __attribute__((address_space(1)))
; #define LAS __attribute__((address_space(3)))
; #define LDS_WAIT() asm volatile("s_waitcnt lgkmcnt(0)" ::: "memory")
;     const int pr = item >> 1, kb = 2 * (pr / nblk) + (item & 1), nb = pr % nblk, k0 = 64 * kb, n0 = 32 * nb;
;     const int nr = n0 + (lane & 31); const int sc = MAP == 1 ? src_col_in(nr) : nr;
;     float v[32];
; #pragma unroll
;     for (int i = 0; i < 32; ++i) v[i] = sc >= 0 ? W[(size_t)(k0 + 2 * i + (lane >> 5)) * Nsrc + sc] : 0.f;
; #pragma unroll
;     for (int i = 0; i < 32; ++i) { const int k = k0 + 2 * i + (lane >> 5); float x = v[i] * wscale; if (KS) x *= (k < ksplit ? ksA[k] : ksB[k - ksplit]); scr[(2 * i + (lane >> 5)) * 33 + (lane & 31)] = x; }
;     LDS_WAIT(); asm volatile("" ::: "memory");
;     const int c = lane & 7;
; #pragma unroll
;     for (int j = 0; j < 4; ++j) { const int n = (lane >> 3) + 8 * j; const LAS float* s = scr + (8 * c) * 33 + n;
;         const unsigned long long o = (unsigned long long)pg8::pk4_fp8(s[0 * 33], s[1 * 33], s[2 * 33], s[3 * 33]) | ((unsigned long long)pg8::pk4_fp8(s[4 * 33], s[5 * 33], s[6 * 33], s[7 * 33]) << 32);
;         *(GAS unsigned long long*)(WT + (size_t)(n0 + n) * K + k0 + 8 * c) = o; }
;     LDS_WAIT(); asm volatile("" ::: "memory");
	s_lshl_b32 s20, s27, 7
	s_cmp_lt_u32 s27, 40
	s_cselect_b32 s21, 0, 0x830
	s_cmp_lt_u32 s27, 72
	s_cselect_b32 s21, s21, 0xfffff030
	s_add_i32 s20, s20, s21
	s_lshl_b32 s20, s20, 2
	s_add_u32 s8, s16, s20
	s_addc_u32 s9, s17, 0
	global_load_dwordx4 v[176:179], v208, s[8:9]
	s_add_u32 s8, s8, 0x16280
	s_addc_u32 s9, s9, 0
	global_load_dwordx4 v[180:183], v208, s[8:9]
	s_add_u32 s8, s8, 0x16280
	s_addc_u32 s9, s9, 0
	global_load_dwordx4 v[184:187], v208, s[8:9]
	s_add_u32 s8, s8, 0x16280
	s_addc_u32 s9, s9, 0
	global_load_dwordx4 v[188:191], v208, s[8:9]
	s_add_u32 s8, s8, 0x16280
	s_addc_u32 s9, s9, 0
	global_load_dwordx4 v[192:195], v208, s[8:9]
	s_add_u32 s8, s8, 0x16280
	s_addc_u32 s9, s9, 0
	global_load_dwordx4 v[196:199], v208, s[8:9]
	s_add_u32 s8, s8, 0x16280
	s_addc_u32 s9, s9, 0
	global_load_dwordx4 v[200:203], v208, s[8:9]
	s_add_u32 s8, s8, 0x16280
	s_addc_u32 s9, s9, 0
	global_load_dwordx4 v[204:207], v208, s[8:9]
	s_mul_i32 s20, s26, 0x80000
	s_add_u32 s6, s18, s20
	s_addc_u32 s7, s19, 0
	s_cmp_lt_u32 s26, 16
	s_cselect_b32 s20, 1, 0
	s_sub_i32 s21, s26, 16
	s_bitcmp0_b32 s21, 2
	s_cselect_b32 s21, 1, 0
	s_cmp_lt_u32 s26, 40
	s_cselect_b32 s21, s21, 0
	s_or_b32 s20, s20, s21
	s_cmp_lg_u32 s20, 0
	s_cselect_b64 s[20:21], -1, 0
	v_cndmask_b32_e64 v108, v100, v104, s[20:21]
	v_cndmask_b32_e64 v109, v101, v105, s[20:21]
	ds_read_b32 v226, v212
	ds_read_b32 v227, v212 offset:512
	ds_read_b32 v228, v212 offset:1024
	ds_read_b32 v229, v212 offset:1536
	ds_read_b32 v230, v212 offset:2048
	ds_read_b32 v231, v212 offset:2560
	ds_read_b32 v232, v212 offset:3072
	ds_read_b32 v233, v212 offset:3584
	ds_read_b32 v234, v212 offset:4096
	ds_read_b32 v235, v212 offset:4608
	ds_read_b32 v236, v212 offset:5120
	ds_read_b32 v237, v212 offset:5632
	ds_read_b32 v238, v212 offset:6144
	ds_read_b32 v239, v212 offset:6656
	ds_read_b32 v240, v212 offset:7168
	ds_read_b32 v241, v212 offset:7680
	s_waitcnt lgkmcnt(0)
	v_max_f32_e32 v226, v226, v226
	v_max_f32_e32 v227, v227, v227
	v_max_f32_e32 v228, v228, v228
	v_max_f32_e32 v229, v229, v229
	v_max_f32_e32 v230, v230, v230
	v_max_f32_e32 v231, v231, v231
	v_max_f32_e32 v232, v232, v232
	v_max_f32_e32 v233, v233, v233
	v_max_f32_e32 v234, v234, v234
	v_max_f32_e32 v235, v235, v235
	v_max_f32_e32 v236, v236, v236
	v_max_f32_e32 v237, v237, v237
	v_max_f32_e32 v238, v238, v238
	v_max_f32_e32 v239, v239, v239
	v_max_f32_e32 v240, v240, v240
	v_max_f32_e32 v241, v241, v241
	v_med3_f32 v226, v226, s44, v246
	v_med3_f32 v227, v227, s44, v246
	v_med3_f32 v228, v228, s44, v246
	v_med3_f32 v229, v229, s44, v246
	v_med3_f32 v230, v230, s44, v246
	v_med3_f32 v231, v231, s44, v246
	v_med3_f32 v232, v232, s44, v246
	v_med3_f32 v233, v233, s44, v246
	v_med3_f32 v234, v234, s44, v246
	v_med3_f32 v235, v235, s44, v246
	v_med3_f32 v236, v236, s44, v246
	v_med3_f32 v237, v237, s44, v246
	v_med3_f32 v238, v238, s44, v246
	v_med3_f32 v239, v239, s44, v246
	v_med3_f32 v240, v240, s44, v246
	v_med3_f32 v241, v241, s44, v246
	v_mov_b32_e32 v242, 0
	v_mov_b32_e32 v243, 0
	v_mov_b32_e32 v244, 0
	v_mov_b32_e32 v245, 0
	v_cvt_pk_fp8_f32 v242, v226, v227
	v_cvt_pk_fp8_f32 v243, v230, v231
	v_cvt_pk_fp8_f32 v244, v234, v235
	v_cvt_pk_fp8_f32 v245, v238, v239
	v_cvt_pk_fp8_f32 v242, v228, v229 op_sel:[0,0,1]
	v_cvt_pk_fp8_f32 v243, v232, v233 op_sel:[0,0,1]
	v_cvt_pk_fp8_f32 v244, v236, v237 op_sel:[0,0,1]
	v_cvt_pk_fp8_f32 v245, v240, v241 op_sel:[0,0,1]
	s_nop 0
	global_store_dwordx4 v108, v[242:245], s[6:7]
	ds_read_b32 v226, v214
	ds_read_b32 v227, v214 offset:512
	ds_read_b32 v228, v214 offset:1024
	ds_read_b32 v229, v214 offset:1536
	ds_read_b32 v230, v214 offset:2048
	ds_read_b32 v231, v214 offset:2560
	ds_read_b32 v232, v214 offset:3072
	ds_read_b32 v233, v214 offset:3584
	ds_read_b32 v234, v214 offset:4096
	ds_read_b32 v235, v214 offset:4608
	ds_read_b32 v236, v214 offset:5120
	ds_read_b32 v237, v214 offset:5632
	ds_read_b32 v238, v214 offset:6144
	ds_read_b32 v239, v214 offset:6656
	ds_read_b32 v240, v214 offset:7168
	ds_read_b32 v241, v214 offset:7680
	s_waitcnt lgkmcnt(0)
	v_max_f32_e32 v226, v226, v226
	v_max_f32_e32 v227, v227, v227
	v_max_f32_e32 v228, v228, v228
	v_max_f32_e32 v229, v229, v229
	v_max_f32_e32 v230, v230, v230
	v_max_f32_e32 v231, v231, v231
	v_max_f32_e32 v232, v232, v232
	v_max_f32_e32 v233, v233, v233
	v_max_f32_e32 v234, v234, v234
	v_max_f32_e32 v235, v235, v235
	v_max_f32_e32 v236, v236, v236
	v_max_f32_e32 v237, v237, v237
	v_max_f32_e32 v238, v238, v238
	v_max_f32_e32 v239, v239, v239
	v_max_f32_e32 v240, v240, v240
	v_max_f32_e32 v241, v241, v241
	v_med3_f32 v226, v226, s44, v246
	v_med3_f32 v227, v227, s44, v246
	v_med3_f32 v228, v228, s44, v246
	v_med3_f32 v229, v229, s44, v246
	v_med3_f32 v230, v230, s44, v246
	v_med3_f32 v231, v231, s44, v246
	v_med3_f32 v232, v232, s44, v246
	v_med3_f32 v233, v233, s44, v246
	v_med3_f32 v234, v234, s44, v246
	v_med3_f32 v235, v235, s44, v246
	v_med3_f32 v236, v236, s44, v246
	v_med3_f32 v237, v237, s44, v246
	v_med3_f32 v238, v238, s44, v246
	v_med3_f32 v239, v239, s44, v246
	v_med3_f32 v240, v240, s44, v246
	v_med3_f32 v241, v241, s44, v246
	v_mov_b32_e32 v242, 0
	v_mov_b32_e32 v243, 0
	v_mov_b32_e32 v244, 0
	v_mov_b32_e32 v245, 0
	v_cvt_pk_fp8_f32 v242, v226, v227
	v_cvt_pk_fp8_f32 v243, v230, v231
	v_cvt_pk_fp8_f32 v244, v234, v235
	v_cvt_pk_fp8_f32 v245, v238, v239
	v_cvt_pk_fp8_f32 v242, v228, v229 op_sel:[0,0,1]
	v_cvt_pk_fp8_f32 v243, v232, v233 op_sel:[0,0,1]
	v_cvt_pk_fp8_f32 v244, v236, v237 op_sel:[0,0,1]
	v_cvt_pk_fp8_f32 v245, v240, v241 op_sel:[0,0,1]
	s_nop 0
	global_store_dwordx4 v109, v[242:245], s[6:7]
	s_add_i32 s26, s23, 32
	s_add_i32 s27, s23, 48
	s_waitcnt vmcnt(12)
; #define GAS __attribute__((address_space(1)))
; #define LAS __attribute__((address_space(3)))
; #define LDS_WAIT() asm volatile("s_waitcnt lgkmcnt(0)" ::: "memory")
;     const int pr = item >> 1, kb = 2 * (pr / nblk) + (item & 1), nb = pr % nblk, k0 = 64 * kb, n0 = 32 * nb;
;     const int nr = n0 + (lane & 31); const int sc = MAP == 1 ? src_col_in(nr) : nr;
;     float v[32];
; #pragma unroll
;     for (int i = 0; i < 32; ++i) v[i] = sc >= 0 ? W[(size_t)(k0 + 2 * i + (lane >> 5)) * Nsrc + sc] : 0.f;
; #pragma unroll
;     for (int i = 0; i < 32; ++i) { const int k = k0 + 2 * i + (lane >> 5); float x = v[i] * wscale; if (KS) x *= (k < ksplit ? ksA[k] : ksB[k - ksplit]); scr[(2 * i + (lane >> 5)) * 33 + (lane & 31)] = x; }
;     LDS_WAIT(); asm volatile("" ::: "memory");
;     const int c = lane & 7;
; #pragma unroll
;     for (int j = 0; j < 4; ++j) { const int n = (lane >> 3) + 8 * j; const LAS float* s = scr + (8 * c) * 33 + n;
;         const unsigned long long o = (unsigned long long)pg8::pk4_fp8(s[0 * 33], s[1 * 33], s[2 * 33], s[3 * 33]) | ((unsigned long long)pg8::pk4_fp8(s[4 * 33], s[5 * 33], s[6 * 33], s[7 * 33]) << 32);
;         *(GAS unsigned long long*)(WT + (size_t)(n0 + n) * K + k0 + 8 * c) = o; }
;     LDS_WAIT(); asm volatile("" ::: "memory");
	v_mul_f32_e32 v144, v218, v144
	v_mul_f32_e32 v145, v218, v145
	v_mul_f32_e32 v146, v218, v146
	v_mul_f32_e32 v147, v218, v147
	ds_write_b128 v209, v[144:147]
	v_mul_f32_e32 v148, v219, v148
	v_mul_f32_e32 v149, v219, v149
	v_mul_f32_e32 v150, v219, v150
	v_mul_f32_e32 v151, v219, v151
	ds_write_b128 v209, v[148:151] offset:1024
	v_mul_f32_e32 v152, v220, v152
	v_mul_f32_e32 v153, v220, v153
	v_mul_f32_e32 v154, v220, v154
	v_mul_f32_e32 v155, v220, v155
	ds_write_b128 v209, v[152:155] offset:2048
	v_mul_f32_e32 v156, v221, v156
	v_mul_f32_e32 v157, v221, v157
	v_mul_f32_e32 v158, v221, v158
	v_mul_f32_e32 v159, v221, v159
	ds_write_b128 v209, v[156:159] offset:3072
	v_mul_f32_e32 v160, v222, v160
	v_mul_f32_e32 v161, v222, v161
	v_mul_f32_e32 v162, v222, v162
	v_mul_f32_e32 v163, v222, v163
	ds_write_b128 v209, v[160:163] offset:4096
	v_mul_f32_e32 v164, v223, v164
	v_mul_f32_e32 v165, v223, v165
	v_mul_f32_e32 v166, v223, v166
	v_mul_f32_e32 v167, v223, v167
	ds_write_b128 v209, v[164:167] offset:5120
	v_mul_f32_e32 v168, v224, v168
	v_mul_f32_e32 v169, v224, v169
	v_mul_f32_e32 v170, v224, v170
	v_mul_f32_e32 v171, v224, v171
	ds_write_b128 v209, v[168:171] offset:6144
	v_mul_f32_e32 v172, v225, v172
	v_mul_f32_e32 v173, v225, v173
	v_mul_f32_e32 v174, v225, v174
	v_mul_f32_e32 v175, v225, v175
	ds_write_b128 v209, v[172:175] offset:7168
	s_waitcnt lgkmcnt(0)
	s_barrier
	s_lshl_b32 s20, s27, 7
	s_cmp_lt_u32 s27, 40
	s_cselect_b32 s21, 0, 0x830
	s_cmp_lt_u32 s27, 72
	s_cselect_b32 s21, s21, 0xfffff030
	s_add_i32 s20, s20, s21
	s_lshl_b32 s20, s20, 2
	s_add_u32 s8, s16, s20
	s_addc_u32 s9, s17, 0
	global_load_dwordx4 v[144:147], v208, s[8:9]
	s_add_u32 s8, s8, 0x16280
	s_addc_u32 s9, s9, 0
	global_load_dwordx4 v[148:151], v208, s[8:9]
	s_add_u32 s8, s8, 0x16280
	s_addc_u32 s9, s9, 0
	global_load_dwordx4 v[152:155], v208, s[8:9]
	s_add_u32 s8, s8, 0x16280
	s_addc_u32 s9, s9, 0
	global_load_dwordx4 v[156:159], v208, s[8:9]
	s_add_u32 s8, s8, 0x16280
	s_addc_u32 s9, s9, 0
	global_load_dwordx4 v[160:163], v208, s[8:9]
	s_add_u32 s8, s8, 0x16280
	s_addc_u32 s9, s9, 0
	global_load_dwordx4 v[164:167], v208, s[8:9]
	s_add_u32 s8, s8, 0x16280
	s_addc_u32 s9, s9, 0
	global_load_dwordx4 v[168:171], v208, s[8:9]
	s_add_u32 s8, s8, 0x16280
	s_addc_u32 s9, s9, 0
	global_load_dwordx4 v[172:175], v208, s[8:9]
	s_mul_i32 s20, s26, 0x80000
	s_add_u32 s6, s18, s20
	s_addc_u32 s7, s19, 0
	s_cmp_lt_u32 s26, 16
	s_cselect_b32 s20, 1, 0
	s_sub_i32 s21, s26, 16
	s_bitcmp0_b32 s21, 2
	s_cselect_b32 s21, 1, 0
	s_cmp_lt_u32 s26, 40
	s_cselect_b32 s21, s21, 0
	s_or_b32 s20, s20, s21
	s_cmp_lg_u32 s20, 0
	s_cselect_b64 s[20:21], -1, 0
	v_cndmask_b32_e64 v108, v100, v104, s[20:21]
	v_cndmask_b32_e64 v109, v101, v105, s[20:21]
	ds_read_b32 v226, v211
	ds_read_b32 v227, v211 offset:512
	ds_read_b32 v228, v211 offset:1024
	ds_read_b32 v229, v211 offset:1536
	ds_read_b32 v230, v211 offset:2048
	ds_read_b32 v231, v211 offset:2560
	ds_read_b32 v232, v211 offset:3072
	ds_read_b32 v233, v211 offset:3584
	ds_read_b32 v234, v211 offset:4096
	ds_read_b32 v235, v211 offset:4608
	ds_read_b32 v236, v211 offset:5120
	ds_read_b32 v237, v211 offset:5632
	ds_read_b32 v238, v211 offset:6144
	ds_read_b32 v239, v211 offset:6656
	ds_read_b32 v240, v211 offset:7168
	ds_read_b32 v241, v211 offset:7680
	s_waitcnt lgkmcnt(0)
	v_max_f32_e32 v226, v226, v226
	v_max_f32_e32 v227, v227, v227
	v_max_f32_e32 v228, v228, v228
	v_max_f32_e32 v229, v229, v229
	v_max_f32_e32 v230, v230, v230
	v_max_f32_e32 v231, v231, v231
	v_max_f32_e32 v232, v232, v232
	v_max_f32_e32 v233, v233, v233
	v_max_f32_e32 v234, v234, v234
	v_max_f32_e32 v235, v235, v235
	v_max_f32_e32 v236, v236, v236
	v_max_f32_e32 v237, v237, v237
	v_max_f32_e32 v238, v238, v238
	v_max_f32_e32 v239, v239, v239
	v_max_f32_e32 v240, v240, v240
	v_max_f32_e32 v241, v241, v241
	v_med3_f32 v226, v226, s44, v246
	v_med3_f32 v227, v227, s44, v246
	v_med3_f32 v228, v228, s44, v246
	v_med3_f32 v229, v229, s44, v246
	v_med3_f32 v230, v230, s44, v246
	v_med3_f32 v231, v231, s44, v246
	v_med3_f32 v232, v232, s44, v246
	v_med3_f32 v233, v233, s44, v246
	v_med3_f32 v234, v234, s44, v246
	v_med3_f32 v235, v235, s44, v246
	v_med3_f32 v236, v236, s44, v246
	v_med3_f32 v237, v237, s44, v246
	v_med3_f32 v238, v238, s44, v246
	v_med3_f32 v239, v239, s44, v246
	v_med3_f32 v240, v240, s44, v246
	v_med3_f32 v241, v241, s44, v246
	v_mov_b32_e32 v242, 0
	v_mov_b32_e32 v243, 0
	v_mov_b32_e32 v244, 0
	v_mov_b32_e32 v245, 0
	v_cvt_pk_fp8_f32 v242, v226, v227
	v_cvt_pk_fp8_f32 v243, v230, v231
	v_cvt_pk_fp8_f32 v244, v234, v235
	v_cvt_pk_fp8_f32 v245, v238, v239
	v_cvt_pk_fp8_f32 v242, v228, v229 op_sel:[0,0,1]
	v_cvt_pk_fp8_f32 v243, v232, v233 op_sel:[0,0,1]
	v_cvt_pk_fp8_f32 v244, v236, v237 op_sel:[0,0,1]
	v_cvt_pk_fp8_f32 v245, v240, v241 op_sel:[0,0,1]
	s_nop 0
	global_store_dwordx4 v108, v[242:245], s[6:7]
	ds_read_b32 v226, v213
	ds_read_b32 v227, v213 offset:512
	ds_read_b32 v228, v213 offset:1024
	ds_read_b32 v229, v213 offset:1536
	ds_read_b32 v230, v213 offset:2048
	ds_read_b32 v231, v213 offset:2560
	ds_read_b32 v232, v213 offset:3072
	ds_read_b32 v233, v213 offset:3584
	ds_read_b32 v234, v213 offset:4096
	ds_read_b32 v235, v213 offset:4608
	ds_read_b32 v236, v213 offset:5120
	ds_read_b32 v237, v213 offset:5632
	ds_read_b32 v238, v213 offset:6144
	ds_read_b32 v239, v213 offset:6656
	ds_read_b32 v240, v213 offset:7168
	ds_read_b32 v241, v213 offset:7680
	s_waitcnt lgkmcnt(0)
; #define GAS __attribute__((address_space(1)))
; #define LAS __attribute__((address_space(3)))
; #define LDS_WAIT() asm volatile("s_waitcnt lgkmcnt(0)" ::: "memory")
;     const int pr = item >> 1, kb = 2 * (pr / nblk) + (item & 1), nb = pr % nblk, k0 = 64 * kb, n0 = 32 * nb;
;     const int nr = n0 + (lane & 31); const int sc = MAP == 1 ? src_col_in(nr) : nr;
;     float v[32];
; #pragma unroll
;     for (int i = 0; i < 32; ++i) v[i] = sc >= 0 ? W[(size_t)(k0 + 2 * i + (lane >> 5)) * Nsrc + sc] : 0.f;
; #pragma unroll
;     for (int i = 0; i < 32; ++i) { const int k = k0 + 2 * i + (lane >> 5); float x = v[i] * wscale; if (KS) x *= (k < ksplit ? ksA[k] : ksB[k - ksplit]); scr[(2 * i + (lane >> 5)) * 33 + (lane & 31)] = x; }
;     LDS_WAIT(); asm volatile("" ::: "memory");
;     const int c = lane & 7;
; #pragma unroll
;     for (int j = 0; j < 4; ++j) { const int n = (lane >> 3) + 8 * j; const LAS float* s = scr + (8 * c) * 33 + n;
;         const unsigned long long o = (unsigned long long)pg8::pk4_fp8(s[0 * 33], s[1 * 33], s[2 * 33], s[3 * 33]) | ((unsigned long long)pg8::pk4_fp8(s[4 * 33], s[5 * 33], s[6 * 33], s[7 * 33]) << 32);
;         *(GAS unsigned long long*)(WT + (size_t)(n0 + n) * K + k0 + 8 * c) = o; }
;     LDS_WAIT(); asm volatile("" ::: "memory");
	v_max_f32_e32 v226, v226, v226
	v_max_f32_e32 v227, v227, v227
	v_max_f32_e32 v228, v228, v228
	v_max_f32_e32 v229, v229, v229
	v_max_f32_e32 v230, v230, v230
	v_max_f32_e32 v231, v231, v231
	v_max_f32_e32 v232, v232, v232
	v_max_f32_e32 v233, v233, v233
	v_max_f32_e32 v234, v234, v234
	v_max_f32_e32 v235, v235, v235
	v_max_f32_e32 v236, v236, v236
	v_max_f32_e32 v237, v237, v237
	v_max_f32_e32 v238, v238, v238
	v_max_f32_e32 v239, v239, v239
	v_max_f32_e32 v240, v240, v240
	v_max_f32_e32 v241, v241, v241
	v_med3_f32 v226, v226, s44, v246
	v_med3_f32 v227, v227, s44, v246
	v_med3_f32 v228, v228, s44, v246
	v_med3_f32 v229, v229, s44, v246
	v_med3_f32 v230, v230, s44, v246
	v_med3_f32 v231, v231, s44, v246
	v_med3_f32 v232, v232, s44, v246
	v_med3_f32 v233, v233, s44, v246
	v_med3_f32 v234, v234, s44, v246
	v_med3_f32 v235, v235, s44, v246
	v_med3_f32 v236, v236, s44, v246
	v_med3_f32 v237, v237, s44, v246
	v_med3_f32 v238, v238, s44, v246
	v_med3_f32 v239, v239, s44, v246
	v_med3_f32 v240, v240, s44, v246
	v_med3_f32 v241, v241, s44, v246
	v_mov_b32_e32 v242, 0
	v_mov_b32_e32 v243, 0
	v_mov_b32_e32 v244, 0
	v_mov_b32_e32 v245, 0
	v_cvt_pk_fp8_f32 v242, v226, v227
	v_cvt_pk_fp8_f32 v243, v230, v231
	v_cvt_pk_fp8_f32 v244, v234, v235
	v_cvt_pk_fp8_f32 v245, v238, v239
	v_cvt_pk_fp8_f32 v242, v228, v229 op_sel:[0,0,1]
	v_cvt_pk_fp8_f32 v243, v232, v233 op_sel:[0,0,1]
	v_cvt_pk_fp8_f32 v244, v236, v237 op_sel:[0,0,1]
	v_cvt_pk_fp8_f32 v245, v240, v241 op_sel:[0,0,1]
	s_nop 0
	global_store_dwordx4 v109, v[242:245], s[6:7]
	s_add_i32 s26, s23, 40
	s_add_i32 s27, s23, 56
	s_waitcnt vmcnt(12)
	v_mul_f32_e32 v176, v218, v176
	v_mul_f32_e32 v177, v218, v177
	v_mul_f32_e32 v178, v218, v178
	v_mul_f32_e32 v179, v218, v179
	ds_write_b128 v210, v[176:179]
	v_mul_f32_e32 v180, v219, v180
	v_mul_f32_e32 v181, v219, v181
	v_mul_f32_e32 v182, v219, v182
	v_mul_f32_e32 v183, v219, v183
	ds_write_b128 v210, v[180:183] offset:1024
	v_mul_f32_e32 v184, v220, v184
	v_mul_f32_e32 v185, v220, v185
	v_mul_f32_e32 v186, v220, v186
	v_mul_f32_e32 v187, v220, v187
	ds_write_b128 v210, v[184:187] offset:2048
	v_mul_f32_e32 v188, v221, v188
	v_mul_f32_e32 v189, v221, v189
	v_mul_f32_e32 v190, v221, v190
	v_mul_f32_e32 v191, v221, v191
	ds_write_b128 v210, v[188:191] offset:3072
	v_mul_f32_e32 v192, v222, v192
	v_mul_f32_e32 v193, v222, v193
	v_mul_f32_e32 v194, v222, v194
	v_mul_f32_e32 v195, v222, v195
	ds_write_b128 v210, v[192:195] offset:4096
	v_mul_f32_e32 v196, v223, v196
	v_mul_f32_e32 v197, v223, v197
	v_mul_f32_e32 v198, v223, v198
	v_mul_f32_e32 v199, v223, v199
	ds_write_b128 v210, v[196:199] offset:5120
	v_mul_f32_e32 v200, v224, v200
	v_mul_f32_e32 v201, v224, v201
	v_mul_f32_e32 v202, v224, v202
	v_mul_f32_e32 v203, v224, v203
	ds_write_b128 v210, v[200:203] offset:6144
	v_mul_f32_e32 v204, v225, v204
	v_mul_f32_e32 v205, v225, v205
	v_mul_f32_e32 v206, v225, v206
	v_mul_f32_e32 v207, v225, v207
	ds_write_b128 v210, v[204:207] offset:7168
	s_waitcnt lgkmcnt(0)
	s_barrier
	s_lshl_b32 s20, s27, 7
	s_cmp_lt_u32 s27, 40
	s_cselect_b32 s21, 0, 0x830
	s_cmp_lt_u32 s27, 72
	s_cselect_b32 s21, s21, 0xfffff030
	s_add_i32 s20, s20, s21
	s_lshl_b32 s20, s20, 2
	s_add_u32 s8, s16, s20
	s_addc_u32 s9, s17, 0
	global_load_dwordx4 v[176:179], v208, s[8:9]
	s_add_u32 s8, s8, 0x16280
	s_addc_u32 s9, s9, 0
	global_load_dwordx4 v[180:183], v208, s[8:9]
	s_add_u32 s8, s8, 0x16280
	s_addc_u32 s9, s9, 0
	global_load_dwordx4 v[184:187], v208, s[8:9]
	s_add_u32 s8, s8, 0x16280
	s_addc_u32 s9, s9, 0
	global_load_dwordx4 v[188:191], v208, s[8:9]
	s_add_u32 s8, s8, 0x16280
	s_addc_u32 s9, s9, 0
	global_load_dwordx4 v[192:195], v208, s[8:9]
	s_add_u32 s8, s8, 0x16280
	s_addc_u32 s9, s9, 0
	global_load_dwordx4 v[196:199], v208, s[8:9]
	s_add_u32 s8, s8, 0x16280
	s_addc_u32 s9, s9, 0
	global_load_dwordx4 v[200:203], v208, s[8:9]
	s_add_u32 s8, s8, 0x16280
	s_addc_u32 s9, s9, 0
	global_load_dwordx4 v[204:207], v208, s[8:9]
	s_mul_i32 s20, s26, 0x80000
	s_add_u32 s6, s18, s20
	s_addc_u32 s7, s19, 0
	s_cmp_lt_u32 s26, 16
	s_cselect_b32 s20, 1, 0
	s_sub_i32 s21, s26, 16
	s_bitcmp0_b32 s21, 2
	s_cselect_b32 s21, 1, 0
	s_cmp_lt_u32 s26, 40
	s_cselect_b32 s21, s21, 0
	s_or_b32 s20, s20, s21
	s_cmp_lg_u32 s20, 0
	s_cselect_b64 s[20:21], -1, 0
	v_cndmask_b32_e64 v108, v100, v104, s[20:21]
	v_cndmask_b32_e64 v109, v101, v105, s[20:21]
	ds_read_b32 v226, v212
	ds_read_b32 v227, v212 offset:512
	ds_read_b32 v228, v212 offset:1024
	ds_read_b32 v229, v212 offset:1536
	ds_read_b32 v230, v212 offset:2048
	ds_read_b32 v231, v212 offset:2560
	ds_read_b32 v232, v212 offset:3072
	ds_read_b32 v233, v212 offset:3584
	ds_read_b32 v234, v212 offset:4096
	ds_read_b32 v235, v212 offset:4608
	ds_read_b32 v236, v212 offset:5120
	ds_read_b32 v237, v212 offset:5632
	ds_read_b32 v238, v212 offset:6144
	ds_read_b32 v239, v212 offset:6656
	ds_read_b32 v240, v212 offset:7168
	ds_read_b32 v241, v212 offset:7680
	s_waitcnt lgkmcnt(0)
; #define GAS __attribute__((address_space(1)))
; #define LAS __attribute__((address_space(3)))
; #define LDS_WAIT() asm volatile("s_waitcnt lgkmcnt(0)" ::: "memory")
;     const int pr = item >> 1, kb = 2 * (pr / nblk) + (item & 1), nb = pr % nblk, k0 = 64 * kb, n0 = 32 * nb;
;     const int nr = n0 + (lane & 31); const int sc = MAP == 1 ? src_col_in(nr) : nr;
;     float v[32];
; #pragma unroll
;     for (int i = 0; i < 32; ++i) v[i] = sc >= 0 ? W[(size_t)(k0 + 2 * i + (lane >> 5)) * Nsrc + sc] : 0.f;
; #pragma unroll
;     for (int i = 0; i < 32; ++i) { const int k = k0 + 2 * i + (lane >> 5); float x = v[i] * wscale; if (KS) x *= (k < ksplit ? ksA[k] : ksB[k - ksplit]); scr[(2 * i + (lane >> 5)) * 33 + (lane & 31)] = x; }
;     LDS_WAIT(); asm volatile("" ::: "memory");
;     const int c = lane & 7;
; #pragma unroll
;     for (int j = 0; j < 4; ++j) { const int n = (lane >> 3) + 8 * j; const LAS float* s = scr + (8 * c) * 33 + n;
;         const unsigned long long o = (unsigned long long)pg8::pk4_fp8(s[0 * 33], s[1 * 33], s[2 * 33], s[3 * 33]) | ((unsigned long long)pg8::pk4_fp8(s[4 * 33], s[5 * 33], s[6 * 33], s[7 * 33]) << 32);
;         *(GAS unsigned long long*)(WT + (size_t)(n0 + n) * K + k0 + 8 * c) = o; }
;     LDS_WAIT(); asm volatile("" ::: "memory");
	v_max_f32_e32 v226, v226, v226
	v_max_f32_e32 v227, v227, v227
	v_max_f32_e32 v228, v228, v228
	v_max_f32_e32 v229, v229, v229
	v_max_f32_e32 v230, v230, v230
	v_max_f32_e32 v231, v231, v231
	v_max_f32_e32 v232, v232, v232
	v_max_f32_e32 v233, v233, v233
	v_max_f32_e32 v234, v234, v234
	v_max_f32_e32 v235, v235, v235
	v_max_f32_e32 v236, v236, v236
	v_max_f32_e32 v237, v237, v237
	v_max_f32_e32 v238, v238, v238
	v_max_f32_e32 v239, v239, v239
	v_max_f32_e32 v240, v240, v240
	v_max_f32_e32 v241, v241, v241
	v_med3_f32 v226, v226, s44, v246
	v_med3_f32 v227, v227, s44, v246
	v_med3_f32 v228, v228, s44, v246
	v_med3_f32 v229, v229, s44, v246
	v_med3_f32 v230, v230, s44, v246
	v_med3_f32 v231, v231, s44, v246
	v_med3_f32 v232, v232, s44, v246
	v_med3_f32 v233, v233, s44, v246
	v_med3_f32 v234, v234, s44, v246
	v_med3_f32 v235, v235, s44, v246
	v_med3_f32 v236, v236, s44, v246
	v_med3_f32 v237, v237, s44, v246
	v_med3_f32 v238, v238, s44, v246
	v_med3_f32 v239, v239, s44, v246
	v_med3_f32 v240, v240, s44, v246
	v_med3_f32 v241, v241, s44, v246
	v_mov_b32_e32 v242, 0
	v_mov_b32_e32 v243, 0
	v_mov_b32_e32 v244, 0
	v_mov_b32_e32 v245, 0
	v_cvt_pk_fp8_f32 v242, v226, v227
	v_cvt_pk_fp8_f32 v243, v230, v231
	v_cvt_pk_fp8_f32 v244, v234, v235
	v_cvt_pk_fp8_f32 v245, v238, v239
	v_cvt_pk_fp8_f32 v242, v228, v229 op_sel:[0,0,1]
	v_cvt_pk_fp8_f32 v243, v232, v233 op_sel:[0,0,1]
	v_cvt_pk_fp8_f32 v244, v236, v237 op_sel:[0,0,1]
	v_cvt_pk_fp8_f32 v245, v240, v241 op_sel:[0,0,1]
	s_nop 0
	global_store_dwordx4 v108, v[242:245], s[6:7]
	ds_read_b32 v226, v214
	ds_read_b32 v227, v214 offset:512
	ds_read_b32 v228, v214 offset:1024
	ds_read_b32 v229, v214 offset:1536
	ds_read_b32 v230, v214 offset:2048
	ds_read_b32 v231, v214 offset:2560
	ds_read_b32 v232, v214 offset:3072
	ds_read_b32 v233, v214 offset:3584
	ds_read_b32 v234, v214 offset:4096
	ds_read_b32 v235, v214 offset:4608
	ds_read_b32 v236, v214 offset:5120
	ds_read_b32 v237, v214 offset:5632
	ds_read_b32 v238, v214 offset:6144
	ds_read_b32 v239, v214 offset:6656
	ds_read_b32 v240, v214 offset:7168
	ds_read_b32 v241, v214 offset:7680
	s_waitcnt lgkmcnt(0)
	v_max_f32_e32 v226, v226, v226
	v_max_f32_e32 v227, v227, v227
	v_max_f32_e32 v228, v228, v228
	v_max_f32_e32 v229, v229, v229
	v_max_f32_e32 v230, v230, v230
	v_max_f32_e32 v231, v231, v231
	v_max_f32_e32 v232, v232, v232
	v_max_f32_e32 v233, v233, v233
	v_max_f32_e32 v234, v234, v234
	v_max_f32_e32 v235, v235, v235
	v_max_f32_e32 v236, v236, v236
	v_max_f32_e32 v237, v237, v237
	v_max_f32_e32 v238, v238, v238
	v_max_f32_e32 v239, v239, v239
	v_max_f32_e32 v240, v240, v240
	v_max_f32_e32 v241, v241, v241
	v_med3_f32 v226, v226, s44, v246
	v_med3_f32 v227, v227, s44, v246
	v_med3_f32 v228, v228, s44, v246
	v_med3_f32 v229, v229, s44, v246
	v_med3_f32 v230, v230, s44, v246
	v_med3_f32 v231, v231, s44, v246
	v_med3_f32 v232, v232, s44, v246
	v_med3_f32 v233, v233, s44, v246
	v_med3_f32 v234, v234, s44, v246
	v_med3_f32 v235, v235, s44, v246
	v_med3_f32 v236, v236, s44, v246
	v_med3_f32 v237, v237, s44, v246
	v_med3_f32 v238, v238, s44, v246
	v_med3_f32 v239, v239, s44, v246
	v_med3_f32 v240, v240, s44, v246
	v_med3_f32 v241, v241, s44, v246
	v_mov_b32_e32 v242, 0
	v_mov_b32_e32 v243, 0
	v_mov_b32_e32 v244, 0
	v_mov_b32_e32 v245, 0
	v_cvt_pk_fp8_f32 v242, v226, v227
	v_cvt_pk_fp8_f32 v243, v230, v231
	v_cvt_pk_fp8_f32 v244, v234, v235
	v_cvt_pk_fp8_f32 v245, v238, v239
	v_cvt_pk_fp8_f32 v242, v228, v229 op_sel:[0,0,1]
	v_cvt_pk_fp8_f32 v243, v232, v233 op_sel:[0,0,1]
	v_cvt_pk_fp8_f32 v244, v236, v237 op_sel:[0,0,1]
	v_cvt_pk_fp8_f32 v245, v240, v241 op_sel:[0,0,1]
	s_nop 0
	global_store_dwordx4 v109, v[242:245], s[6:7]
	s_add_i32 s26, s23, 48
	s_add_i32 s27, s23, 64
	s_waitcnt vmcnt(12)
	v_mul_f32_e32 v144, v218, v144
	v_mul_f32_e32 v145, v218, v145
	v_mul_f32_e32 v146, v218, v146
	v_mul_f32_e32 v147, v218, v147
	ds_write_b128 v209, v[144:147]
	v_mul_f32_e32 v148, v219, v148
	v_mul_f32_e32 v149, v219, v149
	v_mul_f32_e32 v150, v219, v150
	v_mul_f32_e32 v151, v219, v151
	ds_write_b128 v209, v[148:151] offset:1024
	v_mul_f32_e32 v152, v220, v152
	v_mul_f32_e32 v153, v220, v153
	v_mul_f32_e32 v154, v220, v154
	v_mul_f32_e32 v155, v220, v155
	ds_write_b128 v209, v[152:155] offset:2048
	v_mul_f32_e32 v156, v221, v156
	v_mul_f32_e32 v157, v221, v157
	v_mul_f32_e32 v158, v221, v158
	v_mul_f32_e32 v159, v221, v159
	ds_write_b128 v209, v[156:159] offset:3072
	v_mul_f32_e32 v160, v222, v160
	v_mul_f32_e32 v161, v222, v161
	v_mul_f32_e32 v162, v222, v162
	v_mul_f32_e32 v163, v222, v163
	ds_write_b128 v209, v[160:163] offset:4096
	v_mul_f32_e32 v164, v223, v164
	v_mul_f32_e32 v165, v223, v165
	v_mul_f32_e32 v166, v223, v166
	v_mul_f32_e32 v167, v223, v167
	ds_write_b128 v209, v[164:167] offset:5120
	v_mul_f32_e32 v168, v224, v168
	v_mul_f32_e32 v169, v224, v169
	v_mul_f32_e32 v170, v224, v170
	v_mul_f32_e32 v171, v224, v171
	ds_write_b128 v209, v[168:171] offset:6144
	v_mul_f32_e32 v172, v225, v172
	v_mul_f32_e32 v173, v225, v173
	v_mul_f32_e32 v174, v225, v174
	v_mul_f32_e32 v175, v225, v175
	ds_write_b128 v209, v[172:175] offset:7168
	s_waitcnt lgkmcnt(0)
	s_barrier
; #define GAS __attribute__((address_space(1)))
; #define LAS __attribute__((address_space(3)))
; #define LDS_WAIT() asm volatile("s_waitcnt lgkmcnt(0)" ::: "memory")
;     const int pr = item >> 1, kb = 2 * (pr / nblk) + (item & 1), nb = pr % nblk, k0 = 64 * kb, n0 = 32 * nb;
;     const int nr = n0 + (lane & 31); const int sc = MAP == 1 ? src_col_in(nr) : nr;
;     float v[32];
; #pragma unroll
;     for (int i = 0; i < 32; ++i) v[i] = sc >= 0 ? W[(size_t)(k0 + 2 * i + (lane >> 5)) * Nsrc + sc] : 0.f;
; #pragma unroll
;     for (int i = 0; i < 32; ++i) { const int k = k0 + 2 * i + (lane >> 5); float x = v[i] * wscale; if (KS) x *= (k < ksplit ? ksA[k] : ksB[k - ksplit]); scr[(2 * i + (lane >> 5)) * 33 + (lane & 31)] = x; }
;     LDS_WAIT(); asm volatile("" ::: "memory");
;     const int c = lane & 7;
; #pragma unroll
;     for (int j = 0; j < 4; ++j) { const int n = (lane >> 3) + 8 * j; const LAS float* s = scr + (8 * c) * 33 + n;
;         const unsigned long long o = (unsigned long long)pg8::pk4_fp8(s[0 * 33], s[1 * 33], s[2 * 33], s[3 * 33]) | ((unsigned long long)pg8::pk4_fp8(s[4 * 33], s[5 * 33], s[6 * 33], s[7 * 33]) << 32);
;         *(GAS unsigned long long*)(WT + (size_t)(n0 + n) * K + k0 + 8 * c) = o; }
;     LDS_WAIT(); asm volatile("" ::: "memory");
	s_lshl_b32 s20, s27, 7
	s_cmp_lt_u32 s27, 40
	s_cselect_b32 s21, 0, 0x830
	s_cmp_lt_u32 s27, 72
	s_cselect_b32 s21, s21, 0xfffff030
	s_add_i32 s20, s20, s21
	s_lshl_b32 s20, s20, 2
	s_add_u32 s8, s16, s20
	s_addc_u32 s9, s17, 0
	global_load_dwordx4 v[144:147], v208, s[8:9]
	s_add_u32 s8, s8, 0x16280
	s_addc_u32 s9, s9, 0
	global_load_dwordx4 v[148:151], v208, s[8:9]
	s_add_u32 s8, s8, 0x16280
	s_addc_u32 s9, s9, 0
	global_load_dwordx4 v[152:155], v208, s[8:9]
	s_add_u32 s8, s8, 0x16280
	s_addc_u32 s9, s9, 0
	global_load_dwordx4 v[156:159], v208, s[8:9]
	s_add_u32 s8, s8, 0x16280
	s_addc_u32 s9, s9, 0
	global_load_dwordx4 v[160:163], v208, s[8:9]
	s_add_u32 s8, s8, 0x16280
	s_addc_u32 s9, s9, 0
	global_load_dwordx4 v[164:167], v208, s[8:9]
	s_add_u32 s8, s8, 0x16280
	s_addc_u32 s9, s9, 0
	global_load_dwordx4 v[168:171], v208, s[8:9]
	s_add_u32 s8, s8, 0x16280
	s_addc_u32 s9, s9, 0
	global_load_dwordx4 v[172:175], v208, s[8:9]
	s_mul_i32 s20, s26, 0x80000
	s_add_u32 s6, s18, s20
	s_addc_u32 s7, s19, 0
	s_cmp_lt_u32 s26, 16
	s_cselect_b32 s20, 1, 0
	s_sub_i32 s21, s26, 16
	s_bitcmp0_b32 s21, 2
	s_cselect_b32 s21, 1, 0
	s_cmp_lt_u32 s26, 40
	s_cselect_b32 s21, s21, 0
	s_or_b32 s20, s20, s21
	s_cmp_lg_u32 s20, 0
	s_cselect_b64 s[20:21], -1, 0
	v_cndmask_b32_e64 v108, v100, v104, s[20:21]
	v_cndmask_b32_e64 v109, v101, v105, s[20:21]
	ds_read_b32 v226, v211
	ds_read_b32 v227, v211 offset:512
	ds_read_b32 v228, v211 offset:1024
	ds_read_b32 v229, v211 offset:1536
	ds_read_b32 v230, v211 offset:2048
	ds_read_b32 v231, v211 offset:2560
	ds_read_b32 v232, v211 offset:3072
	ds_read_b32 v233, v211 offset:3584
	ds_read_b32 v234, v211 offset:4096
	ds_read_b32 v235, v211 offset:4608
	ds_read_b32 v236, v211 offset:5120
	ds_read_b32 v237, v211 offset:5632
	ds_read_b32 v238, v211 offset:6144
	ds_read_b32 v239, v211 offset:6656
	ds_read_b32 v240, v211 offset:7168
	ds_read_b32 v241, v211 offset:7680
	s_waitcnt lgkmcnt(0)
	v_max_f32_e32 v226, v226, v226
	v_max_f32_e32 v227, v227, v227
	v_max_f32_e32 v228, v228, v228
	v_max_f32_e32 v229, v229, v229
	v_max_f32_e32 v230, v230, v230
	v_max_f32_e32 v231, v231, v231
	v_max_f32_e32 v232, v232, v232
	v_max_f32_e32 v233, v233, v233
	v_max_f32_e32 v234, v234, v234
	v_max_f32_e32 v235, v235, v235
	v_max_f32_e32 v236, v236, v236
	v_max_f32_e32 v237, v237, v237
	v_max_f32_e32 v238, v238, v238
	v_max_f32_e32 v239, v239, v239
	v_max_f32_e32 v240, v240, v240
	v_max_f32_e32 v241, v241, v241
	v_med3_f32 v226, v226, s44, v246
	v_med3_f32 v227, v227, s44, v246
	v_med3_f32 v228, v228, s44, v246
	v_med3_f32 v229, v229, s44, v246
	v_med3_f32 v230, v230, s44, v246
	v_med3_f32 v231, v231, s44, v246
	v_med3_f32 v232, v232, s44, v246
	v_med3_f32 v233, v233, s44, v246
	v_med3_f32 v234, v234, s44, v246
	v_med3_f32 v235, v235, s44, v246
	v_med3_f32 v236, v236, s44, v246
	v_med3_f32 v237, v237, s44, v246
	v_med3_f32 v238, v238, s44, v246
	v_med3_f32 v239, v239, s44, v246
	v_med3_f32 v240, v240, s44, v246
	v_med3_f32 v241, v241, s44, v246
	v_mov_b32_e32 v242, 0
	v_mov_b32_e32 v243, 0
	v_mov_b32_e32 v244, 0
	v_mov_b32_e32 v245, 0
	v_cvt_pk_fp8_f32 v242, v226, v227
	v_cvt_pk_fp8_f32 v243, v230, v231
	v_cvt_pk_fp8_f32 v244, v234, v235
	v_cvt_pk_fp8_f32 v245, v238, v239
	v_cvt_pk_fp8_f32 v242, v228, v229 op_sel:[0,0,1]
	v_cvt_pk_fp8_f32 v243, v232, v233 op_sel:[0,0,1]
	v_cvt_pk_fp8_f32 v244, v236, v237 op_sel:[0,0,1]
	v_cvt_pk_fp8_f32 v245, v240, v241 op_sel:[0,0,1]
	s_nop 0
	global_store_dwordx4 v108, v[242:245], s[6:7]
	ds_read_b32 v226, v213
	ds_read_b32 v227, v213 offset:512
	ds_read_b32 v228, v213 offset:1024
	ds_read_b32 v229, v213 offset:1536
	ds_read_b32 v230, v213 offset:2048
	ds_read_b32 v231, v213 offset:2560
	ds_read_b32 v232, v213 offset:3072
	ds_read_b32 v233, v213 offset:3584
	ds_read_b32 v234, v213 offset:4096
	ds_read_b32 v235, v213 offset:4608
	ds_read_b32 v236, v213 offset:5120
	ds_read_b32 v237, v213 offset:5632
	ds_read_b32 v238, v213 offset:6144
	ds_read_b32 v239, v213 offset:6656
	ds_read_b32 v240, v213 offset:7168
	ds_read_b32 v241, v213 offset:7680
	s_waitcnt lgkmcnt(0)
	v_max_f32_e32 v226, v226, v226
	v_max_f32_e32 v227, v227, v227
	v_max_f32_e32 v228, v228, v228
	v_max_f32_e32 v229, v229, v229
	v_max_f32_e32 v230, v230, v230
	v_max_f32_e32 v231, v231, v231
	v_max_f32_e32 v232, v232, v232
	v_max_f32_e32 v233, v233, v233
	v_max_f32_e32 v234, v234, v234
	v_max_f32_e32 v235, v235, v235
	v_max_f32_e32 v236, v236, v236
	v_max_f32_e32 v237, v237, v237
	v_max_f32_e32 v238, v238, v238
	v_max_f32_e32 v239, v239, v239
	v_max_f32_e32 v240, v240, v240
	v_max_f32_e32 v241, v241, v241
	v_med3_f32 v226, v226, s44, v246
	v_med3_f32 v227, v227, s44, v246
	v_med3_f32 v228, v228, s44, v246
	v_med3_f32 v229, v229, s44, v246
	v_med3_f32 v230, v230, s44, v246
	v_med3_f32 v231, v231, s44, v246
	v_med3_f32 v232, v232, s44, v246
	v_med3_f32 v233, v233, s44, v246
	v_med3_f32 v234, v234, s44, v246
	v_med3_f32 v235, v235, s44, v246
	v_med3_f32 v236, v236, s44, v246
	v_med3_f32 v237, v237, s44, v246
	v_med3_f32 v238, v238, s44, v246
	v_med3_f32 v239, v239, s44, v246
	v_med3_f32 v240, v240, s44, v246
	v_med3_f32 v241, v241, s44, v246
	v_mov_b32_e32 v242, 0
	v_mov_b32_e32 v243, 0
	v_mov_b32_e32 v244, 0
	v_mov_b32_e32 v245, 0
	v_cvt_pk_fp8_f32 v242, v226, v227
	v_cvt_pk_fp8_f32 v243, v230, v231
	v_cvt_pk_fp8_f32 v244, v234, v235
	v_cvt_pk_fp8_f32 v245, v238, v239
	v_cvt_pk_fp8_f32 v242, v228, v229 op_sel:[0,0,1]
	v_cvt_pk_fp8_f32 v243, v232, v233 op_sel:[0,0,1]
	v_cvt_pk_fp8_f32 v244, v236, v237 op_sel:[0,0,1]
	v_cvt_pk_fp8_f32 v245, v240, v241 op_sel:[0,0,1]
	s_nop 0
	global_store_dwordx4 v109, v[242:245], s[6:7]
	s_add_i32 s26, s23, 56
	s_add_i32 s27, s23, 72
	s_waitcnt vmcnt(12)
; #define GAS __attribute__((address_space(1)))
; #define LAS __attribute__((address_space(3)))
; #define LDS_WAIT() asm volatile("s_waitcnt lgkmcnt(0)" ::: "memory")
;     const int pr = item >> 1, kb = 2 * (pr / nblk) + (item & 1), nb = pr % nblk, k0 = 64 * kb, n0 = 32 * nb;
;     const int nr = n0 + (lane & 31); const int sc = MAP == 1 ? src_col_in(nr) : nr;
;     float v[32];
; #pragma unroll
;     for (int i = 0; i < 32; ++i) v[i] = sc >= 0 ? W[(size_t)(k0 + 2 * i + (lane >> 5)) * Nsrc + sc] : 0.f;
; #pragma unroll
;     for (int i = 0; i < 32; ++i) { const int k = k0 + 2 * i + (lane >> 5); float x = v[i] * wscale; if (KS) x *= (k < ksplit ? ksA[k] : ksB[k - ksplit]); scr[(2 * i + (lane >> 5)) * 33 + (lane & 31)] = x; }
;     LDS_WAIT(); asm volatile("" ::: "memory");
;     const int c = lane & 7;
; #pragma unroll
;     for (int j = 0; j < 4; ++j) { const int n = (lane >> 3) + 8 * j; const LAS float* s = scr + (8 * c) * 33 + n;
;         const unsigned long long o = (unsigned long long)pg8::pk4_fp8(s[0 * 33], s[1 * 33], s[2 * 33], s[3 * 33]) | ((unsigned long long)pg8::pk4_fp8(s[4 * 33], s[5 * 33], s[6 * 33], s[7 * 33]) << 32);
;         *(GAS unsigned long long*)(WT + (size_t)(n0 + n) * K + k0 + 8 * c) = o; }
;     LDS_WAIT(); asm volatile("" ::: "memory");
	v_mul_f32_e32 v176, v218, v176
	v_mul_f32_e32 v177, v218, v177
	v_mul_f32_e32 v178, v218, v178
	v_mul_f32_e32 v179, v218, v179
	ds_write_b128 v210, v[176:179]
	v_mul_f32_e32 v180, v219, v180
	v_mul_f32_e32 v181, v219, v181
	v_mul_f32_e32 v182, v219, v182
	v_mul_f32_e32 v183, v219, v183
	ds_write_b128 v210, v[180:183] offset:1024
	v_mul_f32_e32 v184, v220, v184
	v_mul_f32_e32 v185, v220, v185
	v_mul_f32_e32 v186, v220, v186
	v_mul_f32_e32 v187, v220, v187
	ds_write_b128 v210, v[184:187] offset:2048
	v_mul_f32_e32 v188, v221, v188
	v_mul_f32_e32 v189, v221, v189
	v_mul_f32_e32 v190, v221, v190
	v_mul_f32_e32 v191, v221, v191
	ds_write_b128 v210, v[188:191] offset:3072
	v_mul_f32_e32 v192, v222, v192
	v_mul_f32_e32 v193, v222, v193
	v_mul_f32_e32 v194, v222, v194
	v_mul_f32_e32 v195, v222, v195
	ds_write_b128 v210, v[192:195] offset:4096
	v_mul_f32_e32 v196, v223, v196
	v_mul_f32_e32 v197, v223, v197
	v_mul_f32_e32 v198, v223, v198
	v_mul_f32_e32 v199, v223, v199
	ds_write_b128 v210, v[196:199] offset:5120
	v_mul_f32_e32 v200, v224, v200
	v_mul_f32_e32 v201, v224, v201
	v_mul_f32_e32 v202, v224, v202
	v_mul_f32_e32 v203, v224, v203
	ds_write_b128 v210, v[200:203] offset:6144
	v_mul_f32_e32 v204, v225, v204
	v_mul_f32_e32 v205, v225, v205
	v_mul_f32_e32 v206, v225, v206
	v_mul_f32_e32 v207, v225, v207
	ds_write_b128 v210, v[204:207] offset:7168
	s_waitcnt lgkmcnt(0)
	s_barrier
	s_lshl_b32 s20, s27, 7
	s_cmp_lt_u32 s27, 40
	s_cselect_b32 s21, 0, 0x830
	s_cmp_lt_u32 s27, 72
	s_cselect_b32 s21, s21, 0xfffff030
	s_add_i32 s20, s20, s21
	s_lshl_b32 s20, s20, 2
	s_add_u32 s8, s16, s20
	s_addc_u32 s9, s17, 0
	global_load_dwordx4 v[176:179], v208, s[8:9]
	s_add_u32 s8, s8, 0x16280
	s_addc_u32 s9, s9, 0
	global_load_dwordx4 v[180:183], v208, s[8:9]
	s_add_u32 s8, s8, 0x16280
	s_addc_u32 s9, s9, 0
	global_load_dwordx4 v[184:187], v208, s[8:9]
	s_add_u32 s8, s8, 0x16280
	s_addc_u32 s9, s9, 0
	global_load_dwordx4 v[188:191], v208, s[8:9]
	s_add_u32 s8, s8, 0x16280
	s_addc_u32 s9, s9, 0
	global_load_dwordx4 v[192:195], v208, s[8:9]
	s_add_u32 s8, s8, 0x16280
	s_addc_u32 s9, s9, 0
	global_load_dwordx4 v[196:199], v208, s[8:9]
	s_add_u32 s8, s8, 0x16280
	s_addc_u32 s9, s9, 0
	global_load_dwordx4 v[200:203], v208, s[8:9]
	s_add_u32 s8, s8, 0x16280
	s_addc_u32 s9, s9, 0
	global_load_dwordx4 v[204:207], v208, s[8:9]
	s_mul_i32 s20, s26, 0x80000
	s_add_u32 s6, s18, s20
	s_addc_u32 s7, s19, 0
	s_cmp_lt_u32 s26, 16
	s_cselect_b32 s20, 1, 0
	s_sub_i32 s21, s26, 16
	s_bitcmp0_b32 s21, 2
	s_cselect_b32 s21, 1, 0
	s_cmp_lt_u32 s26, 40
	s_cselect_b32 s21, s21, 0
	s_or_b32 s20, s20, s21
	s_cmp_lg_u32 s20, 0
	s_cselect_b64 s[20:21], -1, 0
	v_cndmask_b32_e64 v108, v100, v104, s[20:21]
	v_cndmask_b32_e64 v109, v101, v105, s[20:21]
	ds_read_b32 v226, v212
	ds_read_b32 v227, v212 offset:512
	ds_read_b32 v228, v212 offset:1024
	ds_read_b32 v229, v212 offset:1536
	ds_read_b32 v230, v212 offset:2048
	ds_read_b32 v231, v212 offset:2560
	ds_read_b32 v232, v212 offset:3072
	ds_read_b32 v233, v212 offset:3584
	ds_read_b32 v234, v212 offset:4096
	ds_read_b32 v235, v212 offset:4608
	ds_read_b32 v236, v212 offset:5120
	ds_read_b32 v237, v212 offset:5632
	ds_read_b32 v238, v212 offset:6144
	ds_read_b32 v239, v212 offset:6656
	ds_read_b32 v240, v212 offset:7168
	ds_read_b32 v241, v212 offset:7680
	s_waitcnt lgkmcnt(0)
	v_max_f32_e32 v226, v226, v226
	v_max_f32_e32 v227, v227, v227
	v_max_f32_e32 v228, v228, v228
	v_max_f32_e32 v229, v229, v229
	v_max_f32_e32 v230, v230, v230
	v_max_f32_e32 v231, v231, v231
	v_max_f32_e32 v232, v232, v232
	v_max_f32_e32 v233, v233, v233
	v_max_f32_e32 v234, v234, v234
	v_max_f32_e32 v235, v235, v235
	v_max_f32_e32 v236, v236, v236
	v_max_f32_e32 v237, v237, v237
	v_max_f32_e32 v238, v238, v238
	v_max_f32_e32 v239, v239, v239
	v_max_f32_e32 v240, v240, v240
	v_max_f32_e32 v241, v241, v241
	v_med3_f32 v226, v226, s44, v246
	v_med3_f32 v227, v227, s44, v246
	v_med3_f32 v228, v228, s44, v246
	v_med3_f32 v229, v229, s44, v246
	v_med3_f32 v230, v230, s44, v246
	v_med3_f32 v231, v231, s44, v246
	v_med3_f32 v232, v232, s44, v246
	v_med3_f32 v233, v233, s44, v246
	v_med3_f32 v234, v234, s44, v246
	v_med3_f32 v235, v235, s44, v246
	v_med3_f32 v236, v236, s44, v246
	v_med3_f32 v237, v237, s44, v246
	v_med3_f32 v238, v238, s44, v246
	v_med3_f32 v239, v239, s44, v246
	v_med3_f32 v240, v240, s44, v246
	v_med3_f32 v241, v241, s44, v246
	v_mov_b32_e32 v242, 0
	v_mov_b32_e32 v243, 0
	v_mov_b32_e32 v244, 0
	v_mov_b32_e32 v245, 0
	v_cvt_pk_fp8_f32 v242, v226, v227
	v_cvt_pk_fp8_f32 v243, v230, v231
	v_cvt_pk_fp8_f32 v244, v234, v235
	v_cvt_pk_fp8_f32 v245, v238, v239
	v_cvt_pk_fp8_f32 v242, v228, v229 op_sel:[0,0,1]
	v_cvt_pk_fp8_f32 v243, v232, v233 op_sel:[0,0,1]
	v_cvt_pk_fp8_f32 v244, v236, v237 op_sel:[0,0,1]
	v_cvt_pk_fp8_f32 v245, v240, v241 op_sel:[0,0,1]
	s_nop 0
	global_store_dwordx4 v108, v[242:245], s[6:7]
	ds_read_b32 v226, v214
	ds_read_b32 v227, v214 offset:512
	ds_read_b32 v228, v214 offset:1024
	ds_read_b32 v229, v214 offset:1536
	ds_read_b32 v230, v214 offset:2048
	ds_read_b32 v231, v214 offset:2560
	ds_read_b32 v232, v214 offset:3072
	ds_read_b32 v233, v214 offset:3584
	ds_read_b32 v234, v214 offset:4096
	ds_read_b32 v235, v214 offset:4608
	ds_read_b32 v236, v214 offset:5120
	ds_read_b32 v237, v214 offset:5632
	ds_read_b32 v238, v214 offset:6144
	ds_read_b32 v239, v214 offset:6656
	ds_read_b32 v240, v214 offset:7168
	ds_read_b32 v241, v214 offset:7680
	s_waitcnt lgkmcnt(0)
; #define GAS __attribute__((address_space(1)))
; #define LAS __attribute__((address_space(3)))
; #define LDS_WAIT() asm volatile("s_waitcnt lgkmcnt(0)" ::: "memory")
;     const int pr = item >> 1, kb = 2 * (pr / nblk) + (item & 1), nb = pr % nblk, k0 = 64 * kb, n0 = 32 * nb;
;     const int nr = n0 + (lane & 31); const int sc = MAP == 1 ? src_col_in(nr) : nr;
;     float v[32];
; #pragma unroll
;     for (int i = 0; i < 32; ++i) v[i] = sc >= 0 ? W[(size_t)(k0 + 2 * i + (lane >> 5)) * Nsrc + sc] : 0.f;
; #pragma unroll
;     for (int i = 0; i < 32; ++i) { const int k = k0 + 2 * i + (lane >> 5); float x = v[i] * wscale; if (KS) x *= (k < ksplit ? ksA[k] : ksB[k - ksplit]); scr[(2 * i + (lane >> 5)) * 33 + (lane & 31)] = x; }
;     LDS_WAIT(); asm volatile("" ::: "memory");
;     const int c = lane & 7;
; #pragma unroll
;     for (int j = 0; j < 4; ++j) { const int n = (lane >> 3) + 8 * j; const LAS float* s = scr + (8 * c) * 33 + n;
;         const unsigned long long o = (unsigned long long)pg8::pk4_fp8(s[0 * 33], s[1 * 33], s[2 * 33], s[3 * 33]) | ((unsigned long long)pg8::pk4_fp8(s[4 * 33], s[5 * 33], s[6 * 33], s[7 * 33]) << 32);
;         *(GAS unsigned long long*)(WT + (size_t)(n0 + n) * K + k0 + 8 * c) = o; }
;     LDS_WAIT(); asm volatile("" ::: "memory");
	v_max_f32_e32 v226, v226, v226
	v_max_f32_e32 v227, v227, v227
	v_max_f32_e32 v228, v228, v228
	v_max_f32_e32 v229, v229, v229
	v_max_f32_e32 v230, v230, v230
	v_max_f32_e32 v231, v231, v231
	v_max_f32_e32 v232, v232, v232
	v_max_f32_e32 v233, v233, v233
	v_max_f32_e32 v234, v234, v234
	v_max_f32_e32 v235, v235, v235
	v_max_f32_e32 v236, v236, v236
	v_max_f32_e32 v237, v237, v237
	v_max_f32_e32 v238, v238, v238
	v_max_f32_e32 v239, v239, v239
	v_max_f32_e32 v240, v240, v240
	v_max_f32_e32 v241, v241, v241
	v_med3_f32 v226, v226, s44, v246
	v_med3_f32 v227, v227, s44, v246
	v_med3_f32 v228, v228, s44, v246
	v_med3_f32 v229, v229, s44, v246
	v_med3_f32 v230, v230, s44, v246
	v_med3_f32 v231, v231, s44, v246
	v_med3_f32 v232, v232, s44, v246
	v_med3_f32 v233, v233, s44, v246
	v_med3_f32 v234, v234, s44, v246
	v_med3_f32 v235, v235, s44, v246
	v_med3_f32 v236, v236, s44, v246
	v_med3_f32 v237, v237, s44, v246
	v_med3_f32 v238, v238, s44, v246
	v_med3_f32 v239, v239, s44, v246
	v_med3_f32 v240, v240, s44, v246
	v_med3_f32 v241, v241, s44, v246
	v_mov_b32_e32 v242, 0
	v_mov_b32_e32 v243, 0
	v_mov_b32_e32 v244, 0
	v_mov_b32_e32 v245, 0
	v_cvt_pk_fp8_f32 v242, v226, v227
	v_cvt_pk_fp8_f32 v243, v230, v231
	v_cvt_pk_fp8_f32 v244, v234, v235
	v_cvt_pk_fp8_f32 v245, v238, v239
	v_cvt_pk_fp8_f32 v242, v228, v229 op_sel:[0,0,1]
	v_cvt_pk_fp8_f32 v243, v232, v233 op_sel:[0,0,1]
	v_cvt_pk_fp8_f32 v244, v236, v237 op_sel:[0,0,1]
	v_cvt_pk_fp8_f32 v245, v240, v241 op_sel:[0,0,1]
	s_nop 0
	global_store_dwordx4 v109, v[242:245], s[6:7]
	s_add_i32 s26, s23, 64
	s_add_i32 s27, s23, 80
	s_waitcnt vmcnt(12)
	v_mul_f32_e32 v144, v218, v144
	v_mul_f32_e32 v145, v218, v145
	v_mul_f32_e32 v146, v218, v146
	v_mul_f32_e32 v147, v218, v147
	ds_write_b128 v209, v[144:147]
	v_mul_f32_e32 v148, v219, v148
	v_mul_f32_e32 v149, v219, v149
	v_mul_f32_e32 v150, v219, v150
	v_mul_f32_e32 v151, v219, v151
	ds_write_b128 v209, v[148:151] offset:1024
	v_mul_f32_e32 v152, v220, v152
	v_mul_f32_e32 v153, v220, v153
	v_mul_f32_e32 v154, v220, v154
	v_mul_f32_e32 v155, v220, v155
	ds_write_b128 v209, v[152:155] offset:2048
	v_mul_f32_e32 v156, v221, v156
	v_mul_f32_e32 v157, v221, v157
	v_mul_f32_e32 v158, v221, v158
	v_mul_f32_e32 v159, v221, v159
	ds_write_b128 v209, v[156:159] offset:3072
	v_mul_f32_e32 v160, v222, v160
	v_mul_f32_e32 v161, v222, v161
	v_mul_f32_e32 v162, v222, v162
	v_mul_f32_e32 v163, v222, v163
	ds_write_b128 v209, v[160:163] offset:4096
	v_mul_f32_e32 v164, v223, v164
	v_mul_f32_e32 v165, v223, v165
	v_mul_f32_e32 v166, v223, v166
	v_mul_f32_e32 v167, v223, v167
	ds_write_b128 v209, v[164:167] offset:5120
	v_mul_f32_e32 v168, v224, v168
	v_mul_f32_e32 v169, v224, v169
	v_mul_f32_e32 v170, v224, v170
	v_mul_f32_e32 v171, v224, v171
	ds_write_b128 v209, v[168:171] offset:6144
	v_mul_f32_e32 v172, v225, v172
	v_mul_f32_e32 v173, v225, v173
	v_mul_f32_e32 v174, v225, v174
	v_mul_f32_e32 v175, v225, v175
	ds_write_b128 v209, v[172:175] offset:7168
	s_waitcnt lgkmcnt(0)
	s_barrier
	s_lshl_b32 s20, s27, 7
	s_cmp_lt_u32 s27, 40
	s_cselect_b32 s21, 0, 0x830
	s_cmp_lt_u32 s27, 72
	s_cselect_b32 s21, s21, 0xfffff030
	s_add_i32 s20, s20, s21
	s_lshl_b32 s20, s20, 2
	s_add_u32 s8, s16, s20
	s_addc_u32 s9, s17, 0
	global_load_dwordx4 v[144:147], v208, s[8:9]
	s_add_u32 s8, s8, 0x16280
	s_addc_u32 s9, s9, 0
	global_load_dwordx4 v[148:151], v208, s[8:9]
	s_add_u32 s8, s8, 0x16280
	s_addc_u32 s9, s9, 0
	global_load_dwordx4 v[152:155], v208, s[8:9]
	s_add_u32 s8, s8, 0x16280
	s_addc_u32 s9, s9, 0
	global_load_dwordx4 v[156:159], v208, s[8:9]
	s_add_u32 s8, s8, 0x16280
	s_addc_u32 s9, s9, 0
	global_load_dwordx4 v[160:163], v208, s[8:9]
	s_add_u32 s8, s8, 0x16280
	s_addc_u32 s9, s9, 0
	global_load_dwordx4 v[164:167], v208, s[8:9]
	s_add_u32 s8, s8, 0x16280
	s_addc_u32 s9, s9, 0
	global_load_dwordx4 v[168:171], v208, s[8:9]
	s_add_u32 s8, s8, 0x16280
	s_addc_u32 s9, s9, 0
	global_load_dwordx4 v[172:175], v208, s[8:9]
	s_mul_i32 s20, s26, 0x80000
	s_add_u32 s6, s18, s20
	s_addc_u32 s7, s19, 0
	s_cmp_lt_u32 s26, 16
	s_cselect_b32 s20, 1, 0
	s_sub_i32 s21, s26, 16
	s_bitcmp0_b32 s21, 2
	s_cselect_b32 s21, 1, 0
	s_cmp_lt_u32 s26, 40
	s_cselect_b32 s21, s21, 0
	s_or_b32 s20, s20, s21
	s_cmp_lg_u32 s20, 0
	s_cselect_b64 s[20:21], -1, 0
	v_cndmask_b32_e64 v108, v100, v104, s[20:21]
	v_cndmask_b32_e64 v109, v101, v105, s[20:21]
	ds_read_b32 v226, v211
	ds_read_b32 v227, v211 offset:512
	ds_read_b32 v228, v211 offset:1024
	ds_read_b32 v229, v211 offset:1536
	ds_read_b32 v230, v211 offset:2048
	ds_read_b32 v231, v211 offset:2560
	ds_read_b32 v232, v211 offset:3072
	ds_read_b32 v233, v211 offset:3584
	ds_read_b32 v234, v211 offset:4096
	ds_read_b32 v235, v211 offset:4608
	ds_read_b32 v236, v211 offset:5120
	ds_read_b32 v237, v211 offset:5632
	ds_read_b32 v238, v211 offset:6144
	ds_read_b32 v239, v211 offset:6656
	ds_read_b32 v240, v211 offset:7168
	ds_read_b32 v241, v211 offset:7680
	s_waitcnt lgkmcnt(0)
; #define GAS __attribute__((address_space(1)))
; #define LAS __attribute__((address_space(3)))
; #define LDS_WAIT() asm volatile("s_waitcnt lgkmcnt(0)" ::: "memory")
;     const int pr = item >> 1, kb = 2 * (pr / nblk) + (item & 1), nb = pr % nblk, k0 = 64 * kb, n0 = 32 * nb;
;     const int nr = n0 + (lane & 31); const int sc = MAP == 1 ? src_col_in(nr) : nr;
;     float v[32];
; #pragma unroll
;     for (int i = 0; i < 32; ++i) v[i] = sc >= 0 ? W[(size_t)(k0 + 2 * i + (lane >> 5)) * Nsrc + sc] : 0.f;
; #pragma unroll
;     for (int i = 0; i < 32; ++i) { const int k = k0 + 2 * i + (lane >> 5); float x = v[i] * wscale; if (KS) x *= (k < ksplit ? ksA[k] : ksB[k - ksplit]); scr[(2 * i + (lane >> 5)) * 33 + (lane & 31)] = x; }
;     LDS_WAIT(); asm volatile("" ::: "memory");
;     const int c = lane & 7;
; #pragma unroll
;     for (int j = 0; j < 4; ++j) { const int n = (lane >> 3) + 8 * j; const LAS float* s = scr + (8 * c) * 33 + n;
;         const unsigned long long o = (unsigned long long)pg8::pk4_fp8(s[0 * 33], s[1 * 33], s[2 * 33], s[3 * 33]) | ((unsigned long long)pg8::pk4_fp8(s[4 * 33], s[5 * 33], s[6 * 33], s[7 * 33]) << 32);
;         *(GAS unsigned long long*)(WT + (size_t)(n0 + n) * K + k0 + 8 * c) = o; }
;     LDS_WAIT(); asm volatile("" ::: "memory");
; }
	v_max_f32_e32 v226, v226, v226
	v_max_f32_e32 v227, v227, v227
	v_max_f32_e32 v228, v228, v228
	v_max_f32_e32 v229, v229, v229
	v_max_f32_e32 v230, v230, v230
	v_max_f32_e32 v231, v231, v231
	v_max_f32_e32 v232, v232, v232
	v_max_f32_e32 v233, v233, v233
	v_max_f32_e32 v234, v234, v234
	v_max_f32_e32 v235, v235, v235
	v_max_f32_e32 v236, v236, v236
	v_max_f32_e32 v237, v237, v237
	v_max_f32_e32 v238, v238, v238
	v_max_f32_e32 v239, v239, v239
	v_max_f32_e32 v240, v240, v240
	v_max_f32_e32 v241, v241, v241
	v_med3_f32 v226, v226, s44, v246
	v_med3_f32 v227, v227, s44, v246
	v_med3_f32 v228, v228, s44, v246
	v_med3_f32 v229, v229, s44, v246
	v_med3_f32 v230, v230, s44, v246
	v_med3_f32 v231, v231, s44, v246
	v_med3_f32 v232, v232, s44, v246
	v_med3_f32 v233, v233, s44, v246
	v_med3_f32 v234, v234, s44, v246
	v_med3_f32 v235, v235, s44, v246
	v_med3_f32 v236, v236, s44, v246
	v_med3_f32 v237, v237, s44, v246
	v_med3_f32 v238, v238, s44, v246
	v_med3_f32 v239, v239, s44, v246
	v_med3_f32 v240, v240, s44, v246
	v_med3_f32 v241, v241, s44, v246
	v_mov_b32_e32 v242, 0
	v_mov_b32_e32 v243, 0
	v_mov_b32_e32 v244, 0
	v_mov_b32_e32 v245, 0
	v_cvt_pk_fp8_f32 v242, v226, v227
	v_cvt_pk_fp8_f32 v243, v230, v231
	v_cvt_pk_fp8_f32 v244, v234, v235
	v_cvt_pk_fp8_f32 v245, v238, v239
	v_cvt_pk_fp8_f32 v242, v228, v229 op_sel:[0,0,1]
	v_cvt_pk_fp8_f32 v243, v232, v233 op_sel:[0,0,1]
	v_cvt_pk_fp8_f32 v244, v236, v237 op_sel:[0,0,1]
	v_cvt_pk_fp8_f32 v245, v240, v241 op_sel:[0,0,1]
	s_nop 0
	global_store_dwordx4 v108, v[242:245], s[6:7]
	ds_read_b32 v226, v213
	ds_read_b32 v227, v213 offset:512
	ds_read_b32 v228, v213 offset:1024
	ds_read_b32 v229, v213 offset:1536
	ds_read_b32 v230, v213 offset:2048
	ds_read_b32 v231, v213 offset:2560
	ds_read_b32 v232, v213 offset:3072
	ds_read_b32 v233, v213 offset:3584
	ds_read_b32 v234, v213 offset:4096
	ds_read_b32 v235, v213 offset:4608
	ds_read_b32 v236, v213 offset:5120
	ds_read_b32 v237, v213 offset:5632
	ds_read_b32 v238, v213 offset:6144
	ds_read_b32 v239, v213 offset:6656
	ds_read_b32 v240, v213 offset:7168
	ds_read_b32 v241, v213 offset:7680
	s_waitcnt lgkmcnt(0)
	v_max_f32_e32 v226, v226, v226
	v_max_f32_e32 v227, v227, v227
	v_max_f32_e32 v228, v228, v228
	v_max_f32_e32 v229, v229, v229
	v_max_f32_e32 v230, v230, v230
	v_max_f32_e32 v231, v231, v231
	v_max_f32_e32 v232, v232, v232
	v_max_f32_e32 v233, v233, v233
	v_max_f32_e32 v234, v234, v234
	v_max_f32_e32 v235, v235, v235
	v_max_f32_e32 v236, v236, v236
	v_max_f32_e32 v237, v237, v237
	v_max_f32_e32 v238, v238, v238
	v_max_f32_e32 v239, v239, v239
	v_max_f32_e32 v240, v240, v240
	v_max_f32_e32 v241, v241, v241
	v_med3_f32 v226, v226, s44, v246
	v_med3_f32 v227, v227, s44, v246
	v_med3_f32 v228, v228, s44, v246
	v_med3_f32 v229, v229, s44, v246
	v_med3_f32 v230, v230, s44, v246
	v_med3_f32 v231, v231, s44, v246
	v_med3_f32 v232, v232, s44, v246
	v_med3_f32 v233, v233, s44, v246
	v_med3_f32 v234, v234, s44, v246
	v_med3_f32 v235, v235, s44, v246
	v_med3_f32 v236, v236, s44, v246
	v_med3_f32 v237, v237, s44, v246
	v_med3_f32 v238, v238, s44, v246
	v_med3_f32 v239, v239, s44, v246
	v_med3_f32 v240, v240, s44, v246
	v_med3_f32 v241, v241, s44, v246
	v_mov_b32_e32 v242, 0
	v_mov_b32_e32 v243, 0
	v_mov_b32_e32 v244, 0
	v_mov_b32_e32 v245, 0
	v_cvt_pk_fp8_f32 v242, v226, v227
	v_cvt_pk_fp8_f32 v243, v230, v231
	v_cvt_pk_fp8_f32 v244, v234, v235
	v_cvt_pk_fp8_f32 v245, v238, v239
	v_cvt_pk_fp8_f32 v242, v228, v229 op_sel:[0,0,1]
	v_cvt_pk_fp8_f32 v243, v232, v233 op_sel:[0,0,1]
	v_cvt_pk_fp8_f32 v244, v236, v237 op_sel:[0,0,1]
	v_cvt_pk_fp8_f32 v245, v240, v241 op_sel:[0,0,1]
	s_nop 0
	global_store_dwordx4 v109, v[242:245], s[6:7]
	s_add_i32 s26, s23, 72
	s_add_i32 s27, s23, 88
	s_waitcnt vmcnt(12)
	v_mul_f32_e32 v176, v218, v176
	v_mul_f32_e32 v177, v218, v177
	v_mul_f32_e32 v178, v218, v178
	v_mul_f32_e32 v179, v218, v179
	ds_write_b128 v210, v[176:179]
	v_mul_f32_e32 v180, v219, v180
	v_mul_f32_e32 v181, v219, v181
	v_mul_f32_e32 v182, v219, v182
	v_mul_f32_e32 v183, v219, v183
	ds_write_b128 v210, v[180:183] offset:1024
	v_mul_f32_e32 v184, v220, v184
	v_mul_f32_e32 v185, v220, v185
	v_mul_f32_e32 v186, v220, v186
	v_mul_f32_e32 v187, v220, v187
	ds_write_b128 v210, v[184:187] offset:2048
	v_mul_f32_e32 v188, v221, v188
	v_mul_f32_e32 v189, v221, v189
	v_mul_f32_e32 v190, v221, v190
	v_mul_f32_e32 v191, v221, v191
	ds_write_b128 v210, v[188:191] offset:3072
	v_mul_f32_e32 v192, v222, v192
	v_mul_f32_e32 v193, v222, v193
	v_mul_f32_e32 v194, v222, v194
	v_mul_f32_e32 v195, v222, v195
	ds_write_b128 v210, v[192:195] offset:4096
	v_mul_f32_e32 v196, v223, v196
	v_mul_f32_e32 v197, v223, v197
	v_mul_f32_e32 v198, v223, v198
	v_mul_f32_e32 v199, v223, v199
	ds_write_b128 v210, v[196:199] offset:5120
	v_mul_f32_e32 v200, v224, v200
	v_mul_f32_e32 v201, v224, v201
	v_mul_f32_e32 v202, v224, v202
	v_mul_f32_e32 v203, v224, v203
	ds_write_b128 v210, v[200:203] offset:6144
	v_mul_f32_e32 v204, v225, v204
	v_mul_f32_e32 v205, v225, v205
	v_mul_f32_e32 v206, v225, v206
	v_mul_f32_e32 v207, v225, v207
	ds_write_b128 v210, v[204:207] offset:7168
	s_waitcnt lgkmcnt(0)
	s_barrier
; #define GAS __attribute__((address_space(1)))
; #define LAS __attribute__((address_space(3)))
; #define LDS_WAIT() asm volatile("s_waitcnt lgkmcnt(0)" ::: "memory")
;     const int pr = item >> 1, kb = 2 * (pr / nblk) + (item & 1), nb = pr % nblk, k0 = 64 * kb, n0 = 32 * nb;
;     const int nr = n0 + (lane & 31); const int sc = MAP == 1 ? src_col_in(nr) : nr;
;     float v[32];
; #pragma unroll
;     for (int i = 0; i < 32; ++i) v[i] = sc >= 0 ? W[(size_t)(k0 + 2 * i + (lane >> 5)) * Nsrc + sc] : 0.f;
; #pragma unroll
;     for (int i = 0; i < 32; ++i) { const int k = k0 + 2 * i + (lane >> 5); float x = v[i] * wscale; if (KS) x *= (k < ksplit ? ksA[k] : ksB[k - ksplit]); scr[(2 * i + (lane >> 5)) * 33 + (lane & 31)] = x; }
;     LDS_WAIT(); asm volatile("" ::: "memory");
;     const int c = lane & 7;
; #pragma unroll
;     for (int j = 0; j < 4; ++j) { const int n = (lane >> 3) + 8 * j; const LAS float* s = scr + (8 * c) * 33 + n;
;         const unsigned long long o = (unsigned long long)pg8::pk4_fp8(s[0 * 33], s[1 * 33], s[2 * 33], s[3 * 33]) | ((unsigned long long)pg8::pk4_fp8(s[4 * 33], s[5 * 33], s[6 * 33], s[7 * 33]) << 32);
;         *(GAS unsigned long long*)(WT + (size_t)(n0 + n) * K + k0 + 8 * c) = o; }
;     LDS_WAIT(); asm volatile("" ::: "memory");
; }
	s_mul_i32 s20, s26, 0x80000
	s_add_u32 s6, s18, s20
	s_addc_u32 s7, s19, 0
	s_cmp_lt_u32 s26, 16
	s_cselect_b32 s20, 1, 0
	s_sub_i32 s21, s26, 16
	s_bitcmp0_b32 s21, 2
	s_cselect_b32 s21, 1, 0
	s_cmp_lt_u32 s26, 40
	s_cselect_b32 s21, s21, 0
	s_or_b32 s20, s20, s21
	s_cmp_lg_u32 s20, 0
	s_cselect_b64 s[20:21], -1, 0
	v_cndmask_b32_e64 v108, v100, v104, s[20:21]
	v_cndmask_b32_e64 v109, v101, v105, s[20:21]
	ds_read_b32 v226, v212
	ds_read_b32 v227, v212 offset:512
	ds_read_b32 v228, v212 offset:1024
	ds_read_b32 v229, v212 offset:1536
	ds_read_b32 v230, v212 offset:2048
	ds_read_b32 v231, v212 offset:2560
	ds_read_b32 v232, v212 offset:3072
	ds_read_b32 v233, v212 offset:3584
	ds_read_b32 v234, v212 offset:4096
	ds_read_b32 v235, v212 offset:4608
	ds_read_b32 v236, v212 offset:5120
	ds_read_b32 v237, v212 offset:5632
	ds_read_b32 v238, v212 offset:6144
	ds_read_b32 v239, v212 offset:6656
	ds_read_b32 v240, v212 offset:7168
	ds_read_b32 v241, v212 offset:7680
	s_waitcnt lgkmcnt(0)
	v_max_f32_e32 v226, v226, v226
	v_max_f32_e32 v227, v227, v227
	v_max_f32_e32 v228, v228, v228
	v_max_f32_e32 v229, v229, v229
	v_max_f32_e32 v230, v230, v230
	v_max_f32_e32 v231, v231, v231
	v_max_f32_e32 v232, v232, v232
	v_max_f32_e32 v233, v233, v233
	v_max_f32_e32 v234, v234, v234
	v_max_f32_e32 v235, v235, v235
	v_max_f32_e32 v236, v236, v236
	v_max_f32_e32 v237, v237, v237
	v_max_f32_e32 v238, v238, v238
	v_max_f32_e32 v239, v239, v239
	v_max_f32_e32 v240, v240, v240
	v_max_f32_e32 v241, v241, v241
	v_med3_f32 v226, v226, s44, v246
	v_med3_f32 v227, v227, s44, v246
	v_med3_f32 v228, v228, s44, v246
	v_med3_f32 v229, v229, s44, v246
	v_med3_f32 v230, v230, s44, v246
	v_med3_f32 v231, v231, s44, v246
	v_med3_f32 v232, v232, s44, v246
	v_med3_f32 v233, v233, s44, v246
	v_med3_f32 v234, v234, s44, v246
	v_med3_f32 v235, v235, s44, v246
	v_med3_f32 v236, v236, s44, v246
	v_med3_f32 v237, v237, s44, v246
	v_med3_f32 v238, v238, s44, v246
	v_med3_f32 v239, v239, s44, v246
	v_med3_f32 v240, v240, s44, v246
	v_med3_f32 v241, v241, s44, v246
	v_mov_b32_e32 v242, 0
	v_mov_b32_e32 v243, 0
	v_mov_b32_e32 v244, 0
	v_mov_b32_e32 v245, 0
	v_cvt_pk_fp8_f32 v242, v226, v227
	v_cvt_pk_fp8_f32 v243, v230, v231
	v_cvt_pk_fp8_f32 v244, v234, v235
	v_cvt_pk_fp8_f32 v245, v238, v239
	v_cvt_pk_fp8_f32 v242, v228, v229 op_sel:[0,0,1]
	v_cvt_pk_fp8_f32 v243, v232, v233 op_sel:[0,0,1]
	v_cvt_pk_fp8_f32 v244, v236, v237 op_sel:[0,0,1]
	v_cvt_pk_fp8_f32 v245, v240, v241 op_sel:[0,0,1]
	s_nop 0
	global_store_dwordx4 v108, v[242:245], s[6:7]
	ds_read_b32 v226, v214
	ds_read_b32 v227, v214 offset:512
	ds_read_b32 v228, v214 offset:1024
	ds_read_b32 v229, v214 offset:1536
	ds_read_b32 v230, v214 offset:2048
	ds_read_b32 v231, v214 offset:2560
	ds_read_b32 v232, v214 offset:3072
	ds_read_b32 v233, v214 offset:3584
	ds_read_b32 v234, v214 offset:4096
	ds_read_b32 v235, v214 offset:4608
	ds_read_b32 v236, v214 offset:5120
	ds_read_b32 v237, v214 offset:5632
	ds_read_b32 v238, v214 offset:6144
	ds_read_b32 v239, v214 offset:6656
	ds_read_b32 v240, v214 offset:7168
	ds_read_b32 v241, v214 offset:7680
	s_waitcnt lgkmcnt(0)
	v_max_f32_e32 v226, v226, v226
	v_max_f32_e32 v227, v227, v227
	v_max_f32_e32 v228, v228, v228
	v_max_f32_e32 v229, v229, v229
	v_max_f32_e32 v230, v230, v230
	v_max_f32_e32 v231, v231, v231
	v_max_f32_e32 v232, v232, v232
	v_max_f32_e32 v233, v233, v233
	v_max_f32_e32 v234, v234, v234
	v_max_f32_e32 v235, v235, v235
	v_max_f32_e32 v236, v236, v236
	v_max_f32_e32 v237, v237, v237
	v_max_f32_e32 v238, v238, v238
	v_max_f32_e32 v239, v239, v239
	v_max_f32_e32 v240, v240, v240
	v_max_f32_e32 v241, v241, v241
	v_med3_f32 v226, v226, s44, v246
	v_med3_f32 v227, v227, s44, v246
	v_med3_f32 v228, v228, s44, v246
	v_med3_f32 v229, v229, s44, v246
	v_med3_f32 v230, v230, s44, v246
	v_med3_f32 v231, v231, s44, v246
	v_med3_f32 v232, v232, s44, v246
	v_med3_f32 v233, v233, s44, v246
	v_med3_f32 v234, v234, s44, v246
	v_med3_f32 v235, v235, s44, v246
	v_med3_f32 v236, v236, s44, v246
	v_med3_f32 v237, v237, s44, v246
	v_med3_f32 v238, v238, s44, v246
	v_med3_f32 v239, v239, s44, v246
	v_med3_f32 v240, v240, s44, v246
	v_med3_f32 v241, v241, s44, v246
	v_mov_b32_e32 v242, 0
	v_mov_b32_e32 v243, 0
	v_mov_b32_e32 v244, 0
	v_mov_b32_e32 v245, 0
	v_cvt_pk_fp8_f32 v242, v226, v227
	v_cvt_pk_fp8_f32 v243, v230, v231
	v_cvt_pk_fp8_f32 v244, v234, v235
	v_cvt_pk_fp8_f32 v245, v238, v239
	v_cvt_pk_fp8_f32 v242, v228, v229 op_sel:[0,0,1]
	v_cvt_pk_fp8_f32 v243, v232, v233 op_sel:[0,0,1]
	v_cvt_pk_fp8_f32 v244, v236, v237 op_sel:[0,0,1]
	v_cvt_pk_fp8_f32 v245, v240, v241 op_sel:[0,0,1]
	s_nop 0
	global_store_dwordx4 v109, v[242:245], s[6:7]
	s_add_i32 s26, s23, 80
	s_add_i32 s27, s23, 96
	s_waitcnt vmcnt(4)
	v_mul_f32_e32 v144, v218, v144
	v_mul_f32_e32 v145, v218, v145
	v_mul_f32_e32 v146, v218, v146
	v_mul_f32_e32 v147, v218, v147
	ds_write_b128 v209, v[144:147]
	v_mul_f32_e32 v148, v219, v148
	v_mul_f32_e32 v149, v219, v149
	v_mul_f32_e32 v150, v219, v150
	v_mul_f32_e32 v151, v219, v151
	ds_write_b128 v209, v[148:151] offset:1024
	v_mul_f32_e32 v152, v220, v152
	v_mul_f32_e32 v153, v220, v153
	v_mul_f32_e32 v154, v220, v154
	v_mul_f32_e32 v155, v220, v155
	ds_write_b128 v209, v[152:155] offset:2048
	v_mul_f32_e32 v156, v221, v156
	v_mul_f32_e32 v157, v221, v157
	v_mul_f32_e32 v158, v221, v158
	v_mul_f32_e32 v159, v221, v159
	ds_write_b128 v209, v[156:159] offset:3072
	v_mul_f32_e32 v160, v222, v160
	v_mul_f32_e32 v161, v222, v161
	v_mul_f32_e32 v162, v222, v162
	v_mul_f32_e32 v163, v222, v163
	ds_write_b128 v209, v[160:163] offset:4096
	v_mul_f32_e32 v164, v223, v164
	v_mul_f32_e32 v165, v223, v165
	v_mul_f32_e32 v166, v223, v166
	v_mul_f32_e32 v167, v223, v167
	ds_write_b128 v209, v[164:167] offset:5120
	v_mul_f32_e32 v168, v224, v168
	v_mul_f32_e32 v169, v224, v169
	v_mul_f32_e32 v170, v224, v170
	v_mul_f32_e32 v171, v224, v171
	ds_write_b128 v209, v[168:171] offset:6144
	v_mul_f32_e32 v172, v225, v172
	v_mul_f32_e32 v173, v225, v173
	v_mul_f32_e32 v174, v225, v174
	v_mul_f32_e32 v175, v225, v175
	ds_write_b128 v209, v[172:175] offset:7168
	s_waitcnt lgkmcnt(0)
	s_barrier
; #define GAS __attribute__((address_space(1)))
; #define LAS __attribute__((address_space(3)))
; #define LDS_WAIT() asm volatile("s_waitcnt lgkmcnt(0)" ::: "memory")
;     const int pr = item >> 1, kb = 2 * (pr / nblk) + (item & 1), nb = pr % nblk, k0 = 64 * kb, n0 = 32 * nb;
;     const int nr = n0 + (lane & 31); const int sc = MAP == 1 ? src_col_in(nr) : nr;
;     float v[32];
; #pragma unroll
;     for (int i = 0; i < 32; ++i) v[i] = sc >= 0 ? W[(size_t)(k0 + 2 * i + (lane >> 5)) * Nsrc + sc] : 0.f;
; #pragma unroll
;     for (int i = 0; i < 32; ++i) { const int k = k0 + 2 * i + (lane >> 5); float x = v[i] * wscale; if (KS) x *= (k < ksplit ? ksA[k] : ksB[k - ksplit]); scr[(2 * i + (lane >> 5)) * 33 + (lane & 31)] = x; }
;     LDS_WAIT(); asm volatile("" ::: "memory");
;     const int c = lane & 7;
; #pragma unroll
;     for (int j = 0; j < 4; ++j) { const int n = (lane >> 3) + 8 * j; const LAS float* s = scr + (8 * c) * 33 + n;
;         const unsigned long long o = (unsigned long long)pg8::pk4_fp8(s[0 * 33], s[1 * 33], s[2 * 33], s[3 * 33]) | ((unsigned long long)pg8::pk4_fp8(s[4 * 33], s[5 * 33], s[6 * 33], s[7 * 33]) << 32);
;         *(GAS unsigned long long*)(WT + (size_t)(n0 + n) * K + k0 + 8 * c) = o; }
;     LDS_WAIT(); asm volatile("" ::: "memory");
; }
	s_mul_i32 s20, s26, 0x80000
	s_add_u32 s6, s18, s20
	s_addc_u32 s7, s19, 0
	s_cmp_lt_u32 s26, 16
	s_cselect_b32 s20, 1, 0
	s_sub_i32 s21, s26, 16
	s_bitcmp0_b32 s21, 2
	s_cselect_b32 s21, 1, 0
	s_cmp_lt_u32 s26, 40
	s_cselect_b32 s21, s21, 0
	s_or_b32 s20, s20, s21
	s_cmp_lg_u32 s20, 0
	s_cselect_b64 s[20:21], -1, 0
	v_cndmask_b32_e64 v108, v100, v104, s[20:21]
	v_cndmask_b32_e64 v109, v101, v105, s[20:21]
	ds_read_b32 v226, v211
	ds_read_b32 v227, v211 offset:512
	ds_read_b32 v228, v211 offset:1024
	ds_read_b32 v229, v211 offset:1536
	ds_read_b32 v230, v211 offset:2048
	ds_read_b32 v231, v211 offset:2560
	ds_read_b32 v232, v211 offset:3072
	ds_read_b32 v233, v211 offset:3584
	ds_read_b32 v234, v211 offset:4096
	ds_read_b32 v235, v211 offset:4608
	ds_read_b32 v236, v211 offset:5120
	ds_read_b32 v237, v211 offset:5632
	ds_read_b32 v238, v211 offset:6144
	ds_read_b32 v239, v211 offset:6656
	ds_read_b32 v240, v211 offset:7168
	ds_read_b32 v241, v211 offset:7680
	s_waitcnt lgkmcnt(0)
	v_max_f32_e32 v226, v226, v226
	v_max_f32_e32 v227, v227, v227
	v_max_f32_e32 v228, v228, v228
	v_max_f32_e32 v229, v229, v229
	v_max_f32_e32 v230, v230, v230
	v_max_f32_e32 v231, v231, v231
	v_max_f32_e32 v232, v232, v232
	v_max_f32_e32 v233, v233, v233
	v_max_f32_e32 v234, v234, v234
	v_max_f32_e32 v235, v235, v235
	v_max_f32_e32 v236, v236, v236
	v_max_f32_e32 v237, v237, v237
	v_max_f32_e32 v238, v238, v238
	v_max_f32_e32 v239, v239, v239
	v_max_f32_e32 v240, v240, v240
	v_max_f32_e32 v241, v241, v241
	v_med3_f32 v226, v226, s44, v246
	v_med3_f32 v227, v227, s44, v246
	v_med3_f32 v228, v228, s44, v246
	v_med3_f32 v229, v229, s44, v246
	v_med3_f32 v230, v230, s44, v246
	v_med3_f32 v231, v231, s44, v246
	v_med3_f32 v232, v232, s44, v246
	v_med3_f32 v233, v233, s44, v246
	v_med3_f32 v234, v234, s44, v246
	v_med3_f32 v235, v235, s44, v246
	v_med3_f32 v236, v236, s44, v246
	v_med3_f32 v237, v237, s44, v246
	v_med3_f32 v238, v238, s44, v246
	v_med3_f32 v239, v239, s44, v246
	v_med3_f32 v240, v240, s44, v246
	v_med3_f32 v241, v241, s44, v246
	v_mov_b32_e32 v242, 0
	v_mov_b32_e32 v243, 0
	v_mov_b32_e32 v244, 0
	v_mov_b32_e32 v245, 0
	v_cvt_pk_fp8_f32 v242, v226, v227
	v_cvt_pk_fp8_f32 v243, v230, v231
	v_cvt_pk_fp8_f32 v244, v234, v235
	v_cvt_pk_fp8_f32 v245, v238, v239
	v_cvt_pk_fp8_f32 v242, v228, v229 op_sel:[0,0,1]
	v_cvt_pk_fp8_f32 v243, v232, v233 op_sel:[0,0,1]
	v_cvt_pk_fp8_f32 v244, v236, v237 op_sel:[0,0,1]
	v_cvt_pk_fp8_f32 v245, v240, v241 op_sel:[0,0,1]
	s_nop 0
	global_store_dwordx4 v108, v[242:245], s[6:7]
	ds_read_b32 v226, v213
	ds_read_b32 v227, v213 offset:512
	ds_read_b32 v228, v213 offset:1024
	ds_read_b32 v229, v213 offset:1536
	ds_read_b32 v230, v213 offset:2048
	ds_read_b32 v231, v213 offset:2560
	ds_read_b32 v232, v213 offset:3072
	ds_read_b32 v233, v213 offset:3584
	ds_read_b32 v234, v213 offset:4096
	ds_read_b32 v235, v213 offset:4608
	ds_read_b32 v236, v213 offset:5120
	ds_read_b32 v237, v213 offset:5632
	ds_read_b32 v238, v213 offset:6144
	ds_read_b32 v239, v213 offset:6656
	ds_read_b32 v240, v213 offset:7168
	ds_read_b32 v241, v213 offset:7680
	s_waitcnt lgkmcnt(0)
	v_max_f32_e32 v226, v226, v226
	v_max_f32_e32 v227, v227, v227
	v_max_f32_e32 v228, v228, v228
	v_max_f32_e32 v229, v229, v229
	v_max_f32_e32 v230, v230, v230
	v_max_f32_e32 v231, v231, v231
	v_max_f32_e32 v232, v232, v232
	v_max_f32_e32 v233, v233, v233
	v_max_f32_e32 v234, v234, v234
	v_max_f32_e32 v235, v235, v235
	v_max_f32_e32 v236, v236, v236
	v_max_f32_e32 v237, v237, v237
	v_max_f32_e32 v238, v238, v238
	v_max_f32_e32 v239, v239, v239
	v_max_f32_e32 v240, v240, v240
	v_max_f32_e32 v241, v241, v241
	v_med3_f32 v226, v226, s44, v246
	v_med3_f32 v227, v227, s44, v246
	v_med3_f32 v228, v228, s44, v246
	v_med3_f32 v229, v229, s44, v246
	v_med3_f32 v230, v230, s44, v246
	v_med3_f32 v231, v231, s44, v246
	v_med3_f32 v232, v232, s44, v246
	v_med3_f32 v233, v233, s44, v246
	v_med3_f32 v234, v234, s44, v246
	v_med3_f32 v235, v235, s44, v246
	v_med3_f32 v236, v236, s44, v246
	v_med3_f32 v237, v237, s44, v246
	v_med3_f32 v238, v238, s44, v246
	v_med3_f32 v239, v239, s44, v246
	v_med3_f32 v240, v240, s44, v246
	v_med3_f32 v241, v241, s44, v246
	v_mov_b32_e32 v242, 0
	v_mov_b32_e32 v243, 0
	v_mov_b32_e32 v244, 0
	v_mov_b32_e32 v245, 0
	v_cvt_pk_fp8_f32 v242, v226, v227
	v_cvt_pk_fp8_f32 v243, v230, v231
	v_cvt_pk_fp8_f32 v244, v234, v235
	v_cvt_pk_fp8_f32 v245, v238, v239
	v_cvt_pk_fp8_f32 v242, v228, v229 op_sel:[0,0,1]
	v_cvt_pk_fp8_f32 v243, v232, v233 op_sel:[0,0,1]
	v_cvt_pk_fp8_f32 v244, v236, v237 op_sel:[0,0,1]
	v_cvt_pk_fp8_f32 v245, v240, v241 op_sel:[0,0,1]
	s_nop 0
	global_store_dwordx4 v109, v[242:245], s[6:7]
	s_waitcnt lgkmcnt(0)
	s_barrier
; template <int MAP, bool KS, bool KPERM = false>
; __device__ __forceinline__ void p0_transpose_item(const float* W, int K, int Nsrc, int nblk, bf16* WT, const float* ksA, const float* ksB, int ksplit, LAS float* scr, int item, int lane) {
;     const int kb = item / nblk, nb = item % nblk, k0 = 64 * kb, n0 = 32 * nb;
;     const int nr = n0 + (lane & 31); const int sc = MAP == 1 ? src_col_in(nr) : (MAP == 2 ? nat_dim(nr) : nr);
;     float v[32];
; #pragma unroll
;     for (int i = 0; i < 32; ++i) { const int k = k0 + 2 * i + (lane >> 5); const int ksrc = KPERM ? ((k & ~127) + nat_dim(k & 127)) : k;
;         v[i] = sc >= 0 ? W[(size_t)ksrc * Nsrc + sc] : 0.f; }
; #pragma unroll
;     for (int i = 0; i < 32; ++i) { const int kk = 2 * i + (lane >> 5); const int k = k0 + kk;
; __global__ void __launch_bounds__(NWAVES * 64, 2) hybrid_fwd(Args args) {
;     ...
;         for (int it = gw; it < DEPTH * I_L; it += NGW) {
;             const int l = it / I_L; int r = it % I_L;
;             if (r < I_IN) { if (l >= PROJ_F8_FROM) p0_transpose_item_f8<true, 1>(args.in[2] + (size_t)l * DM * NSRC, DM, NSRC, NPROJ / 32, (unsigned char*)(ws + WS_WIN + l * SZ_WIN), WUP8_SCALE, args.in[1] + l * DM, args.in[1] + l * DM, DM, scr, r, lane);
;                 else p0_transpose_item<1, true>(args.in[2] + (size_t)l * DM * NSRC, DM, NSRC, NPROJ / 32, (bf16*)(ws + WS_WIN + l * SZ_WIN), args.in[1] + l * DM, args.in[1] + l * DM, DM, scr, r, lane); continue; } r -= I_IN;
;             if (r < I_O) { if (l >= WO_F8_FROM) p0_transpose_item_f8<true>(args.in[13] + (size_t)l * DM * DM, DM, DM, DM / 32, (unsigned char*)(ws + WS_WO + l * SZ_WO), 64.f, args.in[6] + l * 2048, args.in[12] + l * 2048, 2048, scr, r, lane);
;                 else p0_transpose_item<0, true>(args.in[13] + (size_t)l * DM * DM, DM, DM, DM / 32, (bf16*)(ws + WS_WO + l * SZ_WO), args.in[6] + l * 2048, args.in[12] + l * 2048, 2048, scr, r, lane); continue; } r -= I_O;
;             if (r < I_UP) { p0_transpose_item_f8<true>(args.in[15] + (size_t)l * DM * FF, DM, FF, FF / 32, (unsigned char*)(ws + WS_WUP + l * SZ_WUP), WUP8_SCALE, args.in[14] + l * DM, args.in[14] + l * DM, DM, scr, r, lane); continue; } r -= I_UP;
;             p0_transpose_item_f8<false>(args.in[16] + (size_t)l * FF * DM, FF, DM, DM / 32, (unsigned char*)(ws + WS_WDN + l * SZ_WDN), 128.f, args.in[16], args.in[16], 0, scr, r, lane);
;         }
	v_readlane_b32 s12, v253, 35
	v_readlane_b32 s18, v253, 41
	v_readlane_b32 s19, v253, 42
	s_add_u32 s81, s18, 0x1f600000
	s_addc_u32 s94, s19, 0
	s_add_u32 s24, s18, 0xf600000
	v_or_b32_e32 v2, 2, v6
	v_mov_b32_e32 v3, 0x630
	v_readlane_b32 s13, v253, 36
	v_readlane_b32 s14, v253, 37
	v_readlane_b32 s15, v253, 38
	s_addc_u32 s25, s19, 0
	v_mad_u32_u24 v58, v2, s0, v3
	v_mov_b32_e32 v3, 0xc60
	s_add_u32 s26, s18, 0xb600000
	v_mad_u32_u24 v59, v2, s0, v3
	v_readlane_b32 s0, v253, 19
	s_addc_u32 s27, s19, 0
	v_readlane_b32 s2, v253, 21
	v_readlane_b32 s10, v253, 29
	v_readlane_b32 s3, v253, 22
	v_readlane_b32 s11, v253, 30
	s_add_u32 s2, s10, 0x4000000
	v_readlane_b32 s40, v253, 3
	s_addc_u32 s3, s11, 0
	v_readlane_b32 s52, v253, 15
	v_readlane_b32 s53, v253, 16
	s_add_u32 s22, s52, 0x2000
	v_readlane_b32 s8, v253, 27
	s_addc_u32 s23, s53, 0
	v_readlane_b32 s9, v253, 28
	s_add_u32 s84, s8, 0x2000
	s_addc_u32 s85, s9, 0
	s_add_u32 s33, s18, 0x200000
	v_readlane_b32 s44, v253, 7
	s_addc_u32 s38, s19, 0
	v_mov_b32_e32 v9, v11
	v_readlane_b32 s1, v253, 20
	v_readlane_b32 s45, v253, 8
	s_add_u32 s86, s44, 0xb140000
	v_mul_u32_u24_e32 v57, 0x84, v2
	v_readlane_b32 s42, v253, 5
	v_lshl_add_u64 v[2:3], s[18:19], 0, v[8:9]
	s_mov_b64 s[0:1], 0xd600000
	s_addc_u32 s87, s45, 0
	v_readlane_b32 s12, v253, 31
	v_readlane_b32 s13, v253, 32
	v_readlane_b32 s14, v253, 33
	v_readlane_b32 s15, v253, 34
	v_readlane_b32 s43, v253, 6
	v_readlane_b32 s54, v253, 17
	v_readlane_b32 s55, v253, 18
	v_lshl_add_u64 v[12:13], v[2:3], 0, s[0:1]
	s_add_u32 s88, s42, 0x4000
	s_mov_b64 s[0:1], 0x5c00000
	v_readlane_b32 s41, v253, 4
	v_readlane_b32 s46, v253, 9
	v_readlane_b32 s47, v253, 10
	v_readlane_b32 s48, v253, 11
	v_readlane_b32 s49, v253, 12
	v_readlane_b32 s50, v253, 13
	s_addc_u32 s89, s43, 0
	v_lshlrev_b32_e32 v4, 6, v18
	v_lshl_add_u64 v[14:15], v[2:3], 0, s[0:1]
	s_lshl_b32 s0, s80, 5
	s_movk_i32 s12, 0xe000
	s_movk_i32 s14, 0xe008
	s_movk_i32 s18, 0xe010
	s_movk_i32 s78, 0xe018
	s_movk_i32 s92, 0xe0d0
	s_movk_i32 s28, 0xe0d8
	s_movk_i32 s34, 0xe0e0
	s_movk_i32 s52, 0xe0e8
	s_movk_i32 s54, 0xe0f0
	s_movk_i32 s56, 0xe0f8
	v_or_b32_e32 v26, 0x2000, v18
	v_or_b32_e32 v27, 0x4000, v18
	v_or_b32_e32 v28, 0x6000, v18
	v_or_b32_e32 v29, 0x8000, v18
	v_or_b32_e32 v30, 0xa000, v18
	v_or_b32_e32 v31, 0xc000, v18
	v_or_b32_e32 v32, 0xe000, v18
	v_or_b32_e32 v33, 0x10000, v18
	v_or_b32_e32 v34, 0x12000, v18
	v_or_b32_e32 v35, 0x14000, v18
	v_or_b32_e32 v36, 0x16000, v18
	v_or_b32_e32 v37, 0x18000, v18
	v_or_b32_e32 v38, 0x1a000, v18
	v_or_b32_e32 v39, 0x1c000, v18
	v_or_b32_e32 v40, 0x1e000, v18
	v_or_b32_e32 v41, 0x20000, v18
	v_or_b32_e32 v42, 0x22000, v18
	v_or_b32_e32 v43, 0x24000, v18
	v_or_b32_e32 v44, 0x26000, v18
	v_or_b32_e32 v45, 0x28000, v18
	v_or_b32_e32 v46, 0x2a000, v18
	v_or_b32_e32 v47, 0x2c000, v18
	v_or_b32_e32 v48, 0x2e000, v18
	v_or_b32_e32 v49, 0x30000, v18
	v_or_b32_e32 v50, 0x32000, v18
	v_or_b32_e32 v51, 0x34000, v18
	v_or_b32_e32 v52, 0x36000, v18
	v_or_b32_e32 v53, 0x38000, v18
	v_or_b32_e32 v54, 0x3a000, v18
	v_or_b32_e32 v55, 0x3c000, v18
	v_or_b32_e32 v56, 0x3e000, v18
	v_and_b32_e32 v60, 64, v4
	v_mov_b32_e32 v7, v11
	s_lshl_b32 s39, s80, 6
	s_add_i32 s40, s0, 0xfff4c000
	s_lshl_b32 s41, s83, 8
	s_lshl_b32 s42, s80, 4
	s_lshl_b32 s43, s83, 7
	s_mov_b32 s91, 0
	s_mov_b32 s44, 0xc3e00000
	s_movk_i32 s45, 0x7fff
	s_mov_b32 s46, 0xffff0000
	s_movk_i32 s47, 0x2c2f
	s_movk_i32 s48, 0x2c50
	s_mov_b32 s49, 0xb140
	v_add_u32_e32 v61, 0x400, v19
	v_add_u32_e32 v62, 0x800, v19
	v_add_u32_e32 v63, 0xc00, v19
	v_mov_b32_e32 v64, 0x43e00000
	s_mov_b32 s50, s80
	s_mov_b32 s13, -1
	s_mov_b32 s15, -1
	s_mov_b32 s19, -1
	s_mov_b32 s79, -1
	s_mov_b32 s93, -1
	s_mov_b32 s29, -1
	s_mov_b32 s35, -1
	s_mov_b32 s53, -1
	s_mov_b32 s55, -1
	s_mov_b32 s57, -1
	v_readlane_b32 s16, v253, 39
	v_readlane_b32 s17, v253, 40
	v_readlane_b32 s4, v253, 23
	v_readlane_b32 s5, v253, 24
	v_readlane_b32 s6, v253, 25
	v_readlane_b32 s7, v253, 26
	v_readlane_b32 s51, v253, 14
	s_branch .LBB0_15
